# K-loop: post-MFMA barrier issued 4 MFMAs early so the partner half starts its MFMA block while this half finishes
# baseline (speedup 1.0000x reference)
; #define PG8_STAGE(bufoff, gbase, voff) do { _Pragma("unroll") for (int _i = 0; _i < 2; ++_i) \
;         __builtin_amdgcn_global_load_lds((const unsigned*)((const char*)(gbase) + (voff)[_i]), (PG8_LAS unsigned*)(lds + (bufoff) + ldsw + _i * 8192), 16, 0, 0); } while (0)
; #define PG8_LDA(dst, b, h) do { _Pragma("unroll") for (int m = 0; m < 4; ++m) _Pragma("unroll") for (int k = 0; k < 2; ++k) dst[m][k] = *(const PG8_LAS bf16x8*)(lds + PG8_SA(b, h) + aoff + m * 2048 + k * 1024); } while (0)
; #define PG8_LDB(dst, b, h) do { _Pragma("unroll") for (int n = 0; n < 2; ++n) _Pragma("unroll") for (int k = 0; k < 2; ++k) dst[n][k] = *(const PG8_LAS bf16x8*)(lds + PG8_SB(b, h) + boff + n * 2048 + k * 1024); } while (0)
; #define PG8_MMA(ai, bj, At, Bt) do { __builtin_amdgcn_s_setprio(1); _Pragma("unroll") for (int m = 0; m < 4; ++m) _Pragma("unroll") for (int n = 0; n < 2; ++n) _Pragma("unroll") for (int k = 0; k < 2; ++k) \
;         acc[ai][bj][m][n] = __builtin_amdgcn_mfma_f32_16x16x32_bf16(Bt[n][k], At[m][k], acc[ai][bj][m][n], 0, 0, 0); __builtin_amdgcn_s_setprio(0); } while (0)
; template <class Epi, class Sched, bool ALIGN_EPI = false>
; __device__ __forceinline__ void gemm_phase(PG8_LAS unsigned char* lds, const Gemm g, const Sched& S, const Epi& E) {
;     ...
;         for (int t = 0; t < nt; t += 2) {
;             const bool last = (t == nt - 2);
;             const char* a1 = cA + (size_t)(t + 1) * kstep;
;             const char* a2 = last ? nA : cA + (size_t)(t + 2) * kstep; const char* b2 = last ? nB : cB + (size_t)(t + 2) * kstep;
;             const char* a3 = a2 + kstep; const char* b3 = b2 + kstep;
;             unsigned w0[2], w1[2];
; #pragma unroll
;             for (int i = 0; i < 2; ++i) { w0[i] = (Sched::GATHER && last) ? vn0[i] : vc0[i]; w1[i] = (Sched::GATHER && last) ? vn1[i] : vc1[i]; }
;             if (last && has_next) S.a_ready(nxt);
;             PG8_LDB(B0, 0, 0); PG8_LDB(B1, 0, 1); PG8_SCHED; PG8_LDA(At, 0, 0); PG8_STAGE(PG8_SA(1, 1), a1 + hstepA, vc1);
;             PG8_WAIT_V(8); PG8_WAIT_L(0); PG8_BAR; PG8_MMA(0, 0, At, B0); PG8_MMA(0, 1, At, B1); PG8_BAR; PG8_SCHED;
;             PG8_LDA(At, 0, 1); PG8_STAGE(PG8_SB(0, 0), b2, voffB); PG8_STAGE(PG8_SB(0, 1), b2 + hstep, voffB); PG8_STAGE(PG8_SA(0, 0), a2, w0);
;             PG8_WAIT_V(8); PG8_WAIT_L(0); PG8_BAR; PG8_MMA(1, 0, At, B0); PG8_MMA(1, 1, At, B1); PG8_BAR; PG8_SCHED;
.LBB0_247:
	ds_read_b128 v[132:135], v191
	ds_read_b128 v[136:139], v191 offset:1024
	ds_read_b128 v[140:143], v191 offset:2048
	ds_read_b128 v[144:147], v191 offset:3072
	ds_read_b128 v[148:151], v193
	ds_read_b128 v[152:155], v193 offset:1024
	ds_read_b128 v[156:159], v193 offset:2048
	ds_read_b128 v[196:199], v193 offset:3072
	s_add_u32 s52, s50, 0xfff80080
	s_addc_u32 s53, s51, -1
	s_cmp_eq_u32 s80, 28
	s_cselect_b32 s55, s9, s53
	s_cselect_b32 s54, s76, s52
	s_cselect_b32 s53, s45, s79
	s_cselect_b32 s52, s77, s78
	v_lshl_add_u64 v[160:161], s[50:51], 0, v[172:173]
	s_add_i32 m0, s59, 0xc000
	ds_read_b128 v[204:207], v195
	ds_read_b128 v[210:213], v195 offset:1024
	ds_read_b128 v[214:217], v195 offset:2048
	ds_read_b128 v[218:221], v195 offset:3072
	ds_read_b128 v[222:225], v195 offset:4096
	ds_read_b128 v[226:229], v195 offset:5120
	ds_read_b128 v[230:233], v195 offset:6144
	ds_read_b128 v[234:237], v195 offset:7168
	global_load_lds_dwordx4 v[160:161], off
	v_lshl_add_u64 v[160:161], s[50:51], 0, v[174:175]
	s_add_i32 m0, s59, 0xe000
	s_nop 0
	global_load_lds_dwordx4 v[160:161], off
	s_waitcnt vmcnt(8)
	s_waitcnt lgkmcnt(0)
	s_barrier
	v_mfma_f32_16x16x32_bf16 v[126:129], v[132:135], v[204:207], v[126:129]
	v_mfma_f32_16x16x32_bf16 v[122:125], v[140:143], v[204:207], v[122:125]
	v_mfma_f32_16x16x32_bf16 v[110:113], v[132:135], v[214:217], v[110:113]
	v_mfma_f32_16x16x32_bf16 v[106:109], v[140:143], v[214:217], v[106:109]
	v_mfma_f32_16x16x32_bf16 v[94:97], v[132:135], v[222:225], v[94:97]
	v_mfma_f32_16x16x32_bf16 v[90:93], v[140:143], v[222:225], v[90:93]
	v_mfma_f32_16x16x32_bf16 v[78:81], v[132:135], v[230:233], v[78:81]
	v_mfma_f32_16x16x32_bf16 v[74:77], v[140:143], v[230:233], v[74:77]
	v_mfma_f32_16x16x32_bf16 v[126:129], v[136:139], v[210:213], v[126:129]
	v_mfma_f32_16x16x32_bf16 v[122:125], v[144:147], v[210:213], v[122:125]
	v_mfma_f32_16x16x32_bf16 v[110:113], v[136:139], v[218:221], v[110:113]
	v_mfma_f32_16x16x32_bf16 v[106:109], v[144:147], v[218:221], v[106:109]
	v_mfma_f32_16x16x32_bf16 v[94:97], v[136:139], v[226:229], v[94:97]
	v_mfma_f32_16x16x32_bf16 v[90:93], v[144:147], v[226:229], v[90:93]
	v_mfma_f32_16x16x32_bf16 v[78:81], v[136:139], v[234:237], v[78:81]
	v_mfma_f32_16x16x32_bf16 v[74:77], v[144:147], v[234:237], v[74:77]
	v_mfma_f32_16x16x32_bf16 v[118:121], v[148:151], v[204:207], v[118:121]
	v_mfma_f32_16x16x32_bf16 v[114:117], v[156:159], v[204:207], v[114:117]
	v_mfma_f32_16x16x32_bf16 v[102:105], v[148:151], v[214:217], v[102:105]
	v_mfma_f32_16x16x32_bf16 v[98:101], v[156:159], v[214:217], v[98:101]
	v_mfma_f32_16x16x32_bf16 v[86:89], v[148:151], v[222:225], v[86:89]
	v_mfma_f32_16x16x32_bf16 v[82:85], v[156:159], v[222:225], v[82:85]
	v_mfma_f32_16x16x32_bf16 v[70:73], v[148:151], v[230:233], v[70:73]
	v_mfma_f32_16x16x32_bf16 v[66:69], v[156:159], v[230:233], v[66:69]
	v_mfma_f32_16x16x32_bf16 v[118:121], v[152:155], v[210:213], v[118:121]
	v_mfma_f32_16x16x32_bf16 v[114:117], v[196:199], v[210:213], v[114:117]
	v_mfma_f32_16x16x32_bf16 v[102:105], v[152:155], v[218:221], v[102:105]
	v_mfma_f32_16x16x32_bf16 v[98:101], v[196:199], v[218:221], v[98:101]
	s_barrier
	v_mfma_f32_16x16x32_bf16 v[86:89], v[152:155], v[226:229], v[86:89]
	v_mfma_f32_16x16x32_bf16 v[82:85], v[196:199], v[226:229], v[82:85]
	v_mfma_f32_16x16x32_bf16 v[70:73], v[152:155], v[234:237], v[70:73]
	v_mfma_f32_16x16x32_bf16 v[66:69], v[196:199], v[234:237], v[66:69]
	s_add_i32 s81, s67, s57
	v_lshl_add_u64 v[160:161], s[52:53], 0, v[164:165]
	s_mov_b32 m0, s81
	ds_read_b128 v[204:207], v195 offset:16384
	ds_read_b128 v[210:213], v195 offset:17408
	ds_read_b128 v[214:217], v195 offset:18432
	ds_read_b128 v[218:221], v195 offset:19456
	ds_read_b128 v[222:225], v195 offset:20480
	ds_read_b128 v[226:229], v195 offset:21504
	ds_read_b128 v[230:233], v195 offset:22528
	ds_read_b128 v[234:237], v195 offset:23552
	global_load_lds_dwordx4 v[160:161], off
	s_add_i32 m0, s81, 0x2000
	s_add_u32 s82, s52, 0x80000
	v_lshl_add_u64 v[200:201], s[52:53], 0, v[168:169]
	s_addc_u32 s83, s53, 0
	s_add_i32 s81, s68, s57
	global_load_lds_dwordx4 v[200:201], off
	v_lshl_add_u64 v[238:239], s[82:83], 0, v[164:165]
	s_mov_b32 m0, s81
	v_lshl_add_u64 v[240:241], s[54:55], 0, v[166:167]
	global_load_lds_dwordx4 v[238:239], off
	v_lshl_add_u64 v[238:239], s[82:83], 0, v[168:169]
	s_add_i32 m0, s81, 0x2000
	s_nop 0
	global_load_lds_dwordx4 v[238:239], off
	v_lshl_add_u64 v[238:239], s[54:55], 0, v[162:163]
	s_mov_b32 m0, s59
	s_nop 0
	global_load_lds_dwordx4 v[238:239], off
	s_mov_b32 m0, s60
	s_nop 0
	global_load_lds_dwordx4 v[240:241], off
	s_waitcnt vmcnt(8)
	s_waitcnt lgkmcnt(0)
	s_barrier
	v_mfma_f32_16x16x32_bf16 v[54:57], v[132:135], v[204:207], v[54:57]
	v_mfma_f32_16x16x32_bf16 v[50:53], v[140:143], v[204:207], v[50:53]
	v_mfma_f32_16x16x32_bf16 v[38:41], v[132:135], v[214:217], v[38:41]
	v_mfma_f32_16x16x32_bf16 v[34:37], v[140:143], v[214:217], v[34:37]
	v_mfma_f32_16x16x32_bf16 v[22:25], v[132:135], v[222:225], v[22:25]
	v_mfma_f32_16x16x32_bf16 v[18:21], v[140:143], v[222:225], v[18:21]
	v_mfma_f32_16x16x32_bf16 v[6:9], v[132:135], v[230:233], v[6:9]
	v_mfma_f32_16x16x32_bf16 v[2:5], v[140:143], v[230:233], v[2:5]
	v_mfma_f32_16x16x32_bf16 v[54:57], v[136:139], v[210:213], v[54:57]
	v_mfma_f32_16x16x32_bf16 v[50:53], v[144:147], v[210:213], v[50:53]
	v_mfma_f32_16x16x32_bf16 v[38:41], v[136:139], v[218:221], v[38:41]
	v_mfma_f32_16x16x32_bf16 v[34:37], v[144:147], v[218:221], v[34:37]
	v_mfma_f32_16x16x32_bf16 v[22:25], v[136:139], v[226:229], v[22:25]
	v_mfma_f32_16x16x32_bf16 v[18:21], v[144:147], v[226:229], v[18:21]
	v_mfma_f32_16x16x32_bf16 v[6:9], v[136:139], v[234:237], v[6:9]
	v_mfma_f32_16x16x32_bf16 v[2:5], v[144:147], v[234:237], v[2:5]
	v_mfma_f32_16x16x32_bf16 v[58:61], v[148:151], v[204:207], v[58:61]
	v_mfma_f32_16x16x32_bf16 v[62:65], v[156:159], v[204:207], v[62:65]
	v_mfma_f32_16x16x32_bf16 v[42:45], v[148:151], v[214:217], v[42:45]
	v_mfma_f32_16x16x32_bf16 v[46:49], v[156:159], v[214:217], v[46:49]
	v_mfma_f32_16x16x32_bf16 v[26:29], v[148:151], v[222:225], v[26:29]
	v_mfma_f32_16x16x32_bf16 v[30:33], v[156:159], v[222:225], v[30:33]
	v_mfma_f32_16x16x32_bf16 v[10:13], v[148:151], v[230:233], v[10:13]
	v_mfma_f32_16x16x32_bf16 v[14:17], v[156:159], v[230:233], v[14:17]
	v_mfma_f32_16x16x32_bf16 v[58:61], v[152:155], v[210:213], v[58:61]
	v_mfma_f32_16x16x32_bf16 v[62:65], v[196:199], v[210:213], v[62:65]
	v_mfma_f32_16x16x32_bf16 v[42:45], v[152:155], v[218:221], v[42:45]
	v_mfma_f32_16x16x32_bf16 v[46:49], v[196:199], v[218:221], v[46:49]
	s_barrier
; #define PG8_STAGE(bufoff, gbase, voff) do { _Pragma("unroll") for (int _i = 0; _i < 2; ++_i) \
;         __builtin_amdgcn_global_load_lds((const unsigned*)((const char*)(gbase) + (voff)[_i]), (PG8_LAS unsigned*)(lds + (bufoff) + ldsw + _i * 8192), 16, 0, 0); } while (0)
; #define PG8_LDA(dst, b, h) do { _Pragma("unroll") for (int m = 0; m < 4; ++m) _Pragma("unroll") for (int k = 0; k < 2; ++k) dst[m][k] = *(const PG8_LAS bf16x8*)(lds + PG8_SA(b, h) + aoff + m * 2048 + k * 1024); } while (0)
; #define PG8_LDB(dst, b, h) do { _Pragma("unroll") for (int n = 0; n < 2; ++n) _Pragma("unroll") for (int k = 0; k < 2; ++k) dst[n][k] = *(const PG8_LAS bf16x8*)(lds + PG8_SB(b, h) + boff + n * 2048 + k * 1024); } while (0)
; #define PG8_MMA(ai, bj, At, Bt) do { __builtin_amdgcn_s_setprio(1); _Pragma("unroll") for (int m = 0; m < 4; ++m) _Pragma("unroll") for (int n = 0; n < 2; ++n) _Pragma("unroll") for (int k = 0; k < 2; ++k) \
;         acc[ai][bj][m][n] = __builtin_amdgcn_mfma_f32_16x16x32_bf16(Bt[n][k], At[m][k], acc[ai][bj][m][n], 0, 0, 0); __builtin_amdgcn_s_setprio(0); } while (0)
; #define PG8_WAIT_V(n) asm volatile("s_waitcnt vmcnt(" #n ")" ::: "memory")
; #define PG8_WAIT_L(n) asm volatile("s_waitcnt lgkmcnt(" #n ")" ::: "memory")
; #define PG8_BAR __builtin_amdgcn_s_barrier()
; #define PG8_SCHED __builtin_amdgcn_sched_barrier(0)
; template <class Epi, class Sched, bool ALIGN_EPI = false>
; __device__ __forceinline__ void gemm_phase(PG8_LAS unsigned char* lds, const Gemm g, const Sched& S, const Epi& E) {
;     ...
;             PG8_WAIT_V(8); PG8_WAIT_L(0); PG8_BAR; PG8_MMA(1, 0, At, B0); PG8_MMA(1, 1, At, B1); PG8_BAR; PG8_SCHED;
;             PG8_LDB(B0, 1, 0); PG8_LDB(B1, 1, 1); PG8_SCHED; PG8_LDA(At, 1, 0); PG8_STAGE(PG8_SA(0, 1), a2 + hstepA, w1);
;             PG8_WAIT_V(8); PG8_WAIT_L(0); PG8_BAR; PG8_MMA(0, 0, At, B0); PG8_MMA(0, 1, At, B1); PG8_BAR; PG8_SCHED;
	v_mfma_f32_16x16x32_bf16 v[26:29], v[152:155], v[226:229], v[26:29]
	v_mfma_f32_16x16x32_bf16 v[30:33], v[196:199], v[226:229], v[30:33]
	v_mfma_f32_16x16x32_bf16 v[10:13], v[152:155], v[234:237], v[10:13]
	v_mfma_f32_16x16x32_bf16 v[14:17], v[196:199], v[234:237], v[14:17]
	s_add_i32 s81, 0, 0x18000
	v_add_u32_e32 v131, s81, v181
	s_add_i32 s82, 0, 0x1c000
	ds_read_b128 v[132:135], v131
	ds_read_b128 v[136:139], v131 offset:1024
	ds_read_b128 v[140:143], v131 offset:2048
	ds_read_b128 v[144:147], v131 offset:3072
	v_add_u32_e32 v131, s82, v181
	ds_read_b128 v[148:151], v131
	ds_read_b128 v[152:155], v131 offset:1024
	ds_read_b128 v[156:159], v131 offset:2048
	ds_read_b128 v[196:199], v131 offset:3072
	s_add_u32 s54, s54, 0x80000
	s_addc_u32 s55, s55, 0
	s_mov_b32 m0, s61
	v_lshl_add_u64 v[242:243], s[54:55], 0, v[162:163]
	ds_read_b128 v[204:207], v195 offset:32768
	ds_read_b128 v[210:213], v195 offset:33792
	ds_read_b128 v[214:217], v195 offset:34816
	ds_read_b128 v[218:221], v195 offset:35840
	ds_read_b128 v[222:225], v195 offset:36864
	ds_read_b128 v[226:229], v195 offset:37888
	ds_read_b128 v[230:233], v195 offset:38912
	ds_read_b128 v[234:237], v195 offset:39936
	global_load_lds_dwordx4 v[242:243], off
	v_lshl_add_u64 v[242:243], s[54:55], 0, v[166:167]
	s_mov_b32 m0, s62
	s_nop 0
	global_load_lds_dwordx4 v[242:243], off
	s_waitcnt vmcnt(8)
	s_waitcnt lgkmcnt(0)
	s_barrier
	v_mfma_f32_16x16x32_bf16 v[126:129], v[132:135], v[204:207], v[126:129]
	v_mfma_f32_16x16x32_bf16 v[122:125], v[140:143], v[204:207], v[122:125]
	v_mfma_f32_16x16x32_bf16 v[110:113], v[132:135], v[214:217], v[110:113]
	v_mfma_f32_16x16x32_bf16 v[106:109], v[140:143], v[214:217], v[106:109]
	v_mfma_f32_16x16x32_bf16 v[94:97], v[132:135], v[222:225], v[94:97]
	v_mfma_f32_16x16x32_bf16 v[90:93], v[140:143], v[222:225], v[90:93]
	v_mfma_f32_16x16x32_bf16 v[78:81], v[132:135], v[230:233], v[78:81]
	v_mfma_f32_16x16x32_bf16 v[74:77], v[140:143], v[230:233], v[74:77]
	v_mfma_f32_16x16x32_bf16 v[126:129], v[136:139], v[210:213], v[126:129]
	v_mfma_f32_16x16x32_bf16 v[122:125], v[144:147], v[210:213], v[122:125]
	v_mfma_f32_16x16x32_bf16 v[110:113], v[136:139], v[218:221], v[110:113]
	v_mfma_f32_16x16x32_bf16 v[106:109], v[144:147], v[218:221], v[106:109]
	v_mfma_f32_16x16x32_bf16 v[94:97], v[136:139], v[226:229], v[94:97]
	v_mfma_f32_16x16x32_bf16 v[90:93], v[144:147], v[226:229], v[90:93]
	v_mfma_f32_16x16x32_bf16 v[78:81], v[136:139], v[234:237], v[78:81]
	v_mfma_f32_16x16x32_bf16 v[74:77], v[144:147], v[234:237], v[74:77]
	v_mfma_f32_16x16x32_bf16 v[118:121], v[148:151], v[204:207], v[118:121]
	v_mfma_f32_16x16x32_bf16 v[114:117], v[156:159], v[204:207], v[114:117]
	v_mfma_f32_16x16x32_bf16 v[102:105], v[148:151], v[214:217], v[102:105]
	v_mfma_f32_16x16x32_bf16 v[98:101], v[156:159], v[214:217], v[98:101]
	v_mfma_f32_16x16x32_bf16 v[86:89], v[148:151], v[222:225], v[86:89]
	v_mfma_f32_16x16x32_bf16 v[82:85], v[156:159], v[222:225], v[82:85]
	v_mfma_f32_16x16x32_bf16 v[70:73], v[148:151], v[230:233], v[70:73]
	v_mfma_f32_16x16x32_bf16 v[66:69], v[156:159], v[230:233], v[66:69]
	v_mfma_f32_16x16x32_bf16 v[118:121], v[152:155], v[210:213], v[118:121]
	v_mfma_f32_16x16x32_bf16 v[114:117], v[196:199], v[210:213], v[114:117]
	v_mfma_f32_16x16x32_bf16 v[102:105], v[152:155], v[218:221], v[102:105]
	v_mfma_f32_16x16x32_bf16 v[98:101], v[196:199], v[218:221], v[98:101]
	s_barrier
; #define PG8_STAGE(bufoff, gbase, voff) do { _Pragma("unroll") for (int _i = 0; _i < 2; ++_i) \
;         __builtin_amdgcn_global_load_lds((const unsigned*)((const char*)(gbase) + (voff)[_i]), (PG8_LAS unsigned*)(lds + (bufoff) + ldsw + _i * 8192), 16, 0, 0); } while (0)
; #define PG8_LDA(dst, b, h) do { _Pragma("unroll") for (int m = 0; m < 4; ++m) _Pragma("unroll") for (int k = 0; k < 2; ++k) dst[m][k] = *(const PG8_LAS bf16x8*)(lds + PG8_SA(b, h) + aoff + m * 2048 + k * 1024); } while (0)
; #define PG8_MMA(ai, bj, At, Bt) do { __builtin_amdgcn_s_setprio(1); _Pragma("unroll") for (int m = 0; m < 4; ++m) _Pragma("unroll") for (int n = 0; n < 2; ++n) _Pragma("unroll") for (int k = 0; k < 2; ++k) \
;         acc[ai][bj][m][n] = __builtin_amdgcn_mfma_f32_16x16x32_bf16(Bt[n][k], At[m][k], acc[ai][bj][m][n], 0, 0, 0); __builtin_amdgcn_s_setprio(0); } while (0)
; #define PG8_WAIT_V(n) asm volatile("s_waitcnt vmcnt(" #n ")" ::: "memory")
; #define PG8_WAIT_L(n) asm volatile("s_waitcnt lgkmcnt(" #n ")" ::: "memory")
; #define PG8_BAR __builtin_amdgcn_s_barrier()
; #define PG8_SCHED __builtin_amdgcn_sched_barrier(0)
; template <class Epi, class Sched, bool ALIGN_EPI = false>
; __device__ __forceinline__ void gemm_phase(PG8_LAS unsigned char* lds, const Gemm g, const Sched& S, const Epi& E) {
;     ...
;             PG8_WAIT_V(8); PG8_WAIT_L(0); PG8_BAR; PG8_MMA(0, 0, At, B0); PG8_MMA(0, 1, At, B1); PG8_BAR; PG8_SCHED;
;             PG8_LDA(At, 1, 1); PG8_STAGE(PG8_SB(1, 0), b3, voffB); PG8_STAGE(PG8_SB(1, 1), b3 + hstep, voffB); PG8_STAGE(PG8_SA(1, 0), a3, w0);
;             PG8_WAIT_V(8); PG8_WAIT_L(0); PG8_BAR; PG8_MMA(1, 0, At, B0); PG8_MMA(1, 1, At, B1); PG8_BAR; PG8_SCHED;
;             if constexpr (Epi::KSCALE) { if (((t + 2) & 7) == 0 && t + 2 < nt) { E.kscale(acc, pf, ((t + 2) >> 3) - 1, wr, fr); PG8_SCHED; } }
;         }
;         if constexpr (ALIGN_EPI) { if (wr == 0) PG8_BAR; }
	v_mfma_f32_16x16x32_bf16 v[86:89], v[152:155], v[226:229], v[86:89]
	v_mfma_f32_16x16x32_bf16 v[82:85], v[196:199], v[226:229], v[82:85]
	v_mfma_f32_16x16x32_bf16 v[70:73], v[152:155], v[234:237], v[70:73]
	v_mfma_f32_16x16x32_bf16 v[66:69], v[196:199], v[234:237], v[66:69]
	s_add_i32 s54, s81, s57
	v_lshl_add_u64 v[160:161], v[160:161], 0, s[20:21]
	s_mov_b32 m0, s54
	ds_read_b128 v[204:207], v195 offset:49152
	ds_read_b128 v[210:213], v195 offset:50176
	ds_read_b128 v[214:217], v195 offset:51200
	ds_read_b128 v[218:221], v195 offset:52224
	ds_read_b128 v[222:225], v195 offset:53248
	ds_read_b128 v[226:229], v195 offset:54272
	ds_read_b128 v[230:233], v195 offset:55296
	ds_read_b128 v[234:237], v195 offset:56320
	global_load_lds_dwordx4 v[160:161], off
	s_add_i32 m0, s54, 0x2000
	s_add_u32 s52, s52, 0x80080
	v_lshl_add_u64 v[160:161], v[200:201], 0, s[20:21]
	s_addc_u32 s53, s53, 0
	s_add_i32 s54, s82, s57
	global_load_lds_dwordx4 v[160:161], off
	v_lshl_add_u64 v[160:161], s[52:53], 0, v[164:165]
	s_mov_b32 m0, s54
	s_nop 0
	global_load_lds_dwordx4 v[160:161], off
	v_lshl_add_u64 v[160:161], s[52:53], 0, v[168:169]
	s_add_i32 m0, s54, 0x2000
	s_nop 0
	global_load_lds_dwordx4 v[160:161], off
	v_lshl_add_u64 v[160:161], v[238:239], 0, s[20:21]
	s_mov_b32 m0, s65
	s_nop 0
	global_load_lds_dwordx4 v[160:161], off
	v_lshl_add_u64 v[160:161], v[240:241], 0, s[20:21]
	s_mov_b32 m0, s66
	s_nop 0
	global_load_lds_dwordx4 v[160:161], off
	s_waitcnt vmcnt(8)
	s_waitcnt lgkmcnt(0)
	s_barrier
	v_mfma_f32_16x16x32_bf16 v[54:57], v[132:135], v[204:207], v[54:57]
	v_mfma_f32_16x16x32_bf16 v[50:53], v[140:143], v[204:207], v[50:53]
	v_mfma_f32_16x16x32_bf16 v[38:41], v[132:135], v[214:217], v[38:41]
	v_mfma_f32_16x16x32_bf16 v[34:37], v[140:143], v[214:217], v[34:37]
	v_mfma_f32_16x16x32_bf16 v[22:25], v[132:135], v[222:225], v[22:25]
	v_mfma_f32_16x16x32_bf16 v[18:21], v[140:143], v[222:225], v[18:21]
	v_mfma_f32_16x16x32_bf16 v[6:9], v[132:135], v[230:233], v[6:9]
	v_mfma_f32_16x16x32_bf16 v[2:5], v[140:143], v[230:233], v[2:5]
	v_mfma_f32_16x16x32_bf16 v[54:57], v[136:139], v[210:213], v[54:57]
	v_mfma_f32_16x16x32_bf16 v[50:53], v[144:147], v[210:213], v[50:53]
	v_mfma_f32_16x16x32_bf16 v[38:41], v[136:139], v[218:221], v[38:41]
	v_mfma_f32_16x16x32_bf16 v[34:37], v[144:147], v[218:221], v[34:37]
	v_mfma_f32_16x16x32_bf16 v[22:25], v[136:139], v[226:229], v[22:25]
	v_mfma_f32_16x16x32_bf16 v[18:21], v[144:147], v[226:229], v[18:21]
	v_mfma_f32_16x16x32_bf16 v[6:9], v[136:139], v[234:237], v[6:9]
	v_mfma_f32_16x16x32_bf16 v[2:5], v[144:147], v[234:237], v[2:5]
	v_mfma_f32_16x16x32_bf16 v[58:61], v[148:151], v[204:207], v[58:61]
	v_mfma_f32_16x16x32_bf16 v[62:65], v[156:159], v[204:207], v[62:65]
	v_mfma_f32_16x16x32_bf16 v[42:45], v[148:151], v[214:217], v[42:45]
	v_mfma_f32_16x16x32_bf16 v[46:49], v[156:159], v[214:217], v[46:49]
	v_mfma_f32_16x16x32_bf16 v[26:29], v[148:151], v[222:225], v[26:29]
	v_mfma_f32_16x16x32_bf16 v[30:33], v[156:159], v[222:225], v[30:33]
	v_mfma_f32_16x16x32_bf16 v[10:13], v[148:151], v[230:233], v[10:13]
	v_mfma_f32_16x16x32_bf16 v[14:17], v[156:159], v[230:233], v[14:17]
	v_mfma_f32_16x16x32_bf16 v[58:61], v[152:155], v[210:213], v[58:61]
	v_mfma_f32_16x16x32_bf16 v[62:65], v[196:199], v[210:213], v[62:65]
	v_mfma_f32_16x16x32_bf16 v[42:45], v[152:155], v[218:221], v[42:45]
	v_mfma_f32_16x16x32_bf16 v[46:49], v[196:199], v[218:221], v[46:49]
	s_barrier
	v_mfma_f32_16x16x32_bf16 v[26:29], v[152:155], v[226:229], v[26:29]
	v_mfma_f32_16x16x32_bf16 v[30:33], v[196:199], v[226:229], v[30:33]
	v_mfma_f32_16x16x32_bf16 v[10:13], v[152:155], v[234:237], v[10:13]
	v_mfma_f32_16x16x32_bf16 v[14:17], v[196:199], v[234:237], v[14:17]
	s_add_i32 s80, s80, 2
	s_add_u32 s50, s50, 0x100
	s_addc_u32 s51, s51, 0
	s_add_u32 s78, s78, 0x100
	s_addc_u32 s79, s79, 0
	s_cmp_gt_u32 s80, 29
	s_cbranch_scc0 .LBB0_247
	s_and_b64 vcc, exec, s[22:23]
	s_cbranch_vccz .LBB0_250
	s_barrier

; #define PG8_STAGE(bufoff, gbase, voff) do { _Pragma("unroll") for (int _i = 0; _i < 2; ++_i) \
;         __builtin_amdgcn_global_load_lds((const unsigned*)((const char*)(gbase) + (voff)[_i]), (PG8_LAS unsigned*)(lds + (bufoff) + ldsw + _i * 8192), 16, 0, 0); } while (0)
; #define PG8_LDA(dst, b, h) do { _Pragma("unroll") for (int m = 0; m < 4; ++m) _Pragma("unroll") for (int k = 0; k < 2; ++k) dst[m][k] = *(const PG8_LAS bf16x8*)(lds + PG8_SA(b, h) + aoff + m * 2048 + k * 1024); } while (0)
; #define PG8_LDB(dst, b, h) do { _Pragma("unroll") for (int n = 0; n < 2; ++n) _Pragma("unroll") for (int k = 0; k < 2; ++k) dst[n][k] = *(const PG8_LAS bf16x8*)(lds + PG8_SB(b, h) + boff + n * 2048 + k * 1024); } while (0)
; #define PG8_MMA(ai, bj, At, Bt) do { __builtin_amdgcn_s_setprio(1); _Pragma("unroll") for (int m = 0; m < 4; ++m) _Pragma("unroll") for (int n = 0; n < 2; ++n) _Pragma("unroll") for (int k = 0; k < 2; ++k) \
;         acc[ai][bj][m][n] = __builtin_amdgcn_mfma_f32_16x16x32_bf16(Bt[n][k], At[m][k], acc[ai][bj][m][n], 0, 0, 0); __builtin_amdgcn_s_setprio(0); } while (0)
; template <class Epi, class Sched, bool ALIGN_EPI = false>
; __device__ __forceinline__ void gemm_phase(PG8_LAS unsigned char* lds, const Gemm g, const Sched& S, const Epi& E) {
;     ...
;         for (int t = 0; t < nt; t += 2) {
;             const bool last = (t == nt - 2);
;             const char* a1 = cA + (size_t)(t + 1) * kstep;
;             const char* a2 = last ? nA : cA + (size_t)(t + 2) * kstep; const char* b2 = last ? nB : cB + (size_t)(t + 2) * kstep;
;             const char* a3 = a2 + kstep; const char* b3 = b2 + kstep;
;             unsigned w0[2], w1[2];
; #pragma unroll
;             for (int i = 0; i < 2; ++i) { w0[i] = (Sched::GATHER && last) ? vn0[i] : vc0[i]; w1[i] = (Sched::GATHER && last) ? vn1[i] : vc1[i]; }
;             if (last && has_next) S.a_ready(nxt);
;             PG8_LDB(B0, 0, 0); PG8_LDB(B1, 0, 1); PG8_SCHED; PG8_LDA(At, 0, 0); PG8_STAGE(PG8_SA(1, 1), a1 + hstepA, vc1);
;             PG8_WAIT_V(8); PG8_WAIT_L(0); PG8_BAR; PG8_MMA(0, 0, At, B0); PG8_MMA(0, 1, At, B1); PG8_BAR; PG8_SCHED;
;             PG8_LDA(At, 0, 1); PG8_STAGE(PG8_SB(0, 0), b2, voffB); PG8_STAGE(PG8_SB(0, 1), b2 + hstep, voffB); PG8_STAGE(PG8_SA(0, 0), a2, w0);
;             PG8_WAIT_V(8); PG8_WAIT_L(0); PG8_BAR; PG8_MMA(1, 0, At, B0); PG8_MMA(1, 1, At, B1); PG8_BAR; PG8_SCHED;
.LBB0_504:
	v_add_u32_e32 v3, s74, v178
	s_add_u32 s54, s50, s52
	ds_read_b128 v[138:141], v3
	ds_read_b128 v[162:165], v3 offset:1024
	ds_read_b128 v[166:169], v3 offset:2048
	ds_read_b128 v[170:173], v3 offset:3072
	v_add_u32_e32 v3, s75, v178
	s_addc_u32 s55, s51, s53
	ds_read_b128 v[186:189], v3
	s_waitcnt lgkmcnt(0)
	ds_read_b128 v[190:193], v3 offset:1024
	ds_read_b128 v[194:197], v3 offset:2048
	ds_read_b128 v[198:201], v3 offset:3072
	s_add_u32 s54, s54, 0x100
	s_addc_u32 s55, s55, 0
	s_add_u32 s82, s79, s52
	s_addc_u32 s83, s80, s53
	s_cmpk_eq_i32 s52, 0xf00
	s_cselect_b32 s57, s47, s55
	s_cselect_b32 s56, s49, s54
	s_cselect_b32 s55, s45, s83
	s_cselect_b32 s54, s78, s82
	v_lshl_add_u64 v[142:143], v[132:133], 0, s[52:53]
	s_add_i32 m0, s62, 0xc000
	ds_read_b128 v[202:205], v184
	ds_read_b128 v[206:209], v184 offset:1024
	ds_read_b128 v[210:213], v184 offset:2048
	ds_read_b128 v[214:217], v184 offset:3072
	ds_read_b128 v[218:221], v184 offset:4096
	ds_read_b128 v[222:225], v184 offset:5120
	ds_read_b128 v[226:229], v184 offset:6144
	ds_read_b128 v[230:233], v184 offset:7168
	global_load_lds_dwordx4 v[142:143], off
	v_lshl_add_u64 v[142:143], v[134:135], 0, s[52:53]
	s_add_i32 m0, s62, 0xe000
	s_nop 0
	global_load_lds_dwordx4 v[142:143], off
	s_waitcnt vmcnt(8)
	s_waitcnt lgkmcnt(0)
	s_barrier
	v_mfma_f32_16x16x32_bf16 v[128:131], v[138:141], v[202:205], v[128:131]
	v_mfma_f32_16x16x32_bf16 v[124:127], v[166:169], v[202:205], v[124:127]
	v_mfma_f32_16x16x32_bf16 v[120:123], v[138:141], v[210:213], v[120:123]
	v_mfma_f32_16x16x32_bf16 v[112:115], v[166:169], v[210:213], v[112:115]
	v_mfma_f32_16x16x32_bf16 v[96:99], v[138:141], v[218:221], v[96:99]
	v_mfma_f32_16x16x32_bf16 v[92:95], v[166:169], v[218:221], v[92:95]
	v_mfma_f32_16x16x32_bf16 v[80:83], v[138:141], v[226:229], v[80:83]
	v_mfma_f32_16x16x32_bf16 v[76:79], v[166:169], v[226:229], v[76:79]
	v_mfma_f32_16x16x32_bf16 v[128:131], v[162:165], v[206:209], v[128:131]
	v_mfma_f32_16x16x32_bf16 v[124:127], v[170:173], v[206:209], v[124:127]
	v_mfma_f32_16x16x32_bf16 v[120:123], v[162:165], v[214:217], v[120:123]
	v_mfma_f32_16x16x32_bf16 v[112:115], v[170:173], v[214:217], v[112:115]
	v_mfma_f32_16x16x32_bf16 v[96:99], v[162:165], v[222:225], v[96:99]
	v_mfma_f32_16x16x32_bf16 v[92:95], v[170:173], v[222:225], v[92:95]
	v_mfma_f32_16x16x32_bf16 v[80:83], v[162:165], v[230:233], v[80:83]
	v_mfma_f32_16x16x32_bf16 v[76:79], v[170:173], v[230:233], v[76:79]
	v_mfma_f32_16x16x32_bf16 v[116:119], v[186:189], v[202:205], v[116:119]
	v_mfma_f32_16x16x32_bf16 v[108:111], v[194:197], v[202:205], v[108:111]
	v_mfma_f32_16x16x32_bf16 v[104:107], v[186:189], v[210:213], v[104:107]
	v_mfma_f32_16x16x32_bf16 v[100:103], v[194:197], v[210:213], v[100:103]
	v_mfma_f32_16x16x32_bf16 v[88:91], v[186:189], v[218:221], v[88:91]
	v_mfma_f32_16x16x32_bf16 v[84:87], v[194:197], v[218:221], v[84:87]
	v_mfma_f32_16x16x32_bf16 v[72:75], v[186:189], v[226:229], v[72:75]
	v_mfma_f32_16x16x32_bf16 v[68:71], v[194:197], v[226:229], v[68:71]
	v_mfma_f32_16x16x32_bf16 v[116:119], v[190:193], v[206:209], v[116:119]
	v_mfma_f32_16x16x32_bf16 v[108:111], v[198:201], v[206:209], v[108:111]
	v_mfma_f32_16x16x32_bf16 v[104:107], v[190:193], v[214:217], v[104:107]
	v_mfma_f32_16x16x32_bf16 v[100:103], v[198:201], v[214:217], v[100:103]
	s_barrier
	v_mfma_f32_16x16x32_bf16 v[88:91], v[190:193], v[222:225], v[88:91]
	v_mfma_f32_16x16x32_bf16 v[84:87], v[198:201], v[222:225], v[84:87]
	v_mfma_f32_16x16x32_bf16 v[72:75], v[190:193], v[230:233], v[72:75]
	v_mfma_f32_16x16x32_bf16 v[68:71], v[198:201], v[230:233], v[68:71]
	s_add_i32 s82, s74, s61
	v_lshl_add_u64 v[142:143], s[54:55], 0, v[146:147]
	s_mov_b32 m0, s82
	ds_read_b128 v[202:205], v184 offset:16384
	ds_read_b128 v[206:209], v184 offset:17408
	ds_read_b128 v[210:213], v184 offset:18432
	ds_read_b128 v[214:217], v184 offset:19456
	ds_read_b128 v[218:221], v184 offset:20480
	ds_read_b128 v[222:225], v184 offset:21504
	ds_read_b128 v[226:229], v184 offset:22528
	ds_read_b128 v[230:233], v184 offset:23552
	global_load_lds_dwordx4 v[142:143], off
	s_add_i32 m0, s82, 0x2000
	s_add_u32 s82, s54, 0x80000
	v_lshl_add_u64 v[174:175], s[54:55], 0, v[150:151]
	s_addc_u32 s83, s55, 0
	s_add_i32 s84, s75, s61
	global_load_lds_dwordx4 v[174:175], off
	v_lshl_add_u64 v[234:235], s[82:83], 0, v[146:147]
	s_mov_b32 m0, s84
	v_lshl_add_u64 v[236:237], s[56:57], 0, v[148:149]
	global_load_lds_dwordx4 v[234:235], off
	v_lshl_add_u64 v[234:235], s[82:83], 0, v[150:151]
	s_add_i32 m0, s84, 0x2000
	s_nop 0
	global_load_lds_dwordx4 v[234:235], off
	v_lshl_add_u64 v[234:235], s[56:57], 0, v[144:145]
	s_mov_b32 m0, s62
	s_nop 0
	global_load_lds_dwordx4 v[234:235], off
	s_mov_b32 m0, s63
	s_nop 0
	global_load_lds_dwordx4 v[236:237], off
	s_waitcnt vmcnt(8)
	s_waitcnt lgkmcnt(0)
	s_barrier
; #define PG8_STAGE(bufoff, gbase, voff) do { _Pragma("unroll") for (int _i = 0; _i < 2; ++_i) \
;         __builtin_amdgcn_global_load_lds((const unsigned*)((const char*)(gbase) + (voff)[_i]), (PG8_LAS unsigned*)(lds + (bufoff) + ldsw + _i * 8192), 16, 0, 0); } while (0)
; #define PG8_LDA(dst, b, h) do { _Pragma("unroll") for (int m = 0; m < 4; ++m) _Pragma("unroll") for (int k = 0; k < 2; ++k) dst[m][k] = *(const PG8_LAS bf16x8*)(lds + PG8_SA(b, h) + aoff + m * 2048 + k * 1024); } while (0)
; #define PG8_LDB(dst, b, h) do { _Pragma("unroll") for (int n = 0; n < 2; ++n) _Pragma("unroll") for (int k = 0; k < 2; ++k) dst[n][k] = *(const PG8_LAS bf16x8*)(lds + PG8_SB(b, h) + boff + n * 2048 + k * 1024); } while (0)
; #define PG8_MMA(ai, bj, At, Bt) do { __builtin_amdgcn_s_setprio(1); _Pragma("unroll") for (int m = 0; m < 4; ++m) _Pragma("unroll") for (int n = 0; n < 2; ++n) _Pragma("unroll") for (int k = 0; k < 2; ++k) \
;         acc[ai][bj][m][n] = __builtin_amdgcn_mfma_f32_16x16x32_bf16(Bt[n][k], At[m][k], acc[ai][bj][m][n], 0, 0, 0); __builtin_amdgcn_s_setprio(0); } while (0)
; #define PG8_WAIT_V(n) asm volatile("s_waitcnt vmcnt(" #n ")" ::: "memory")
; #define PG8_WAIT_L(n) asm volatile("s_waitcnt lgkmcnt(" #n ")" ::: "memory")
; #define PG8_BAR __builtin_amdgcn_s_barrier()
; #define PG8_SCHED __builtin_amdgcn_sched_barrier(0)
; template <class Epi, class Sched, bool ALIGN_EPI = false>
; __device__ __forceinline__ void gemm_phase(PG8_LAS unsigned char* lds, const Gemm g, const Sched& S, const Epi& E) {
;     ...
;             PG8_WAIT_V(8); PG8_WAIT_L(0); PG8_BAR; PG8_MMA(1, 0, At, B0); PG8_MMA(1, 1, At, B1); PG8_BAR; PG8_SCHED;
;             PG8_LDB(B0, 1, 0); PG8_LDB(B1, 1, 1); PG8_SCHED; PG8_LDA(At, 1, 0); PG8_STAGE(PG8_SA(0, 1), a2 + hstepA, w1);
;             PG8_WAIT_V(8); PG8_WAIT_L(0); PG8_BAR; PG8_MMA(0, 0, At, B0); PG8_MMA(0, 1, At, B1); PG8_BAR; PG8_SCHED;
	v_mfma_f32_16x16x32_bf16 v[64:67], v[138:141], v[202:205], v[64:67]
	v_mfma_f32_16x16x32_bf16 v[60:63], v[166:169], v[202:205], v[60:63]
	v_mfma_f32_16x16x32_bf16 v[48:51], v[138:141], v[210:213], v[48:51]
	v_mfma_f32_16x16x32_bf16 v[44:47], v[166:169], v[210:213], v[44:47]
	v_mfma_f32_16x16x32_bf16 v[32:35], v[138:141], v[218:221], v[32:35]
	v_mfma_f32_16x16x32_bf16 v[28:31], v[166:169], v[218:221], v[28:31]
	v_mfma_f32_16x16x32_bf16 v[16:19], v[138:141], v[226:229], v[16:19]
	v_mfma_f32_16x16x32_bf16 v[12:15], v[166:169], v[226:229], v[12:15]
	v_mfma_f32_16x16x32_bf16 v[64:67], v[162:165], v[206:209], v[64:67]
	v_mfma_f32_16x16x32_bf16 v[60:63], v[170:173], v[206:209], v[60:63]
	v_mfma_f32_16x16x32_bf16 v[48:51], v[162:165], v[214:217], v[48:51]
	v_mfma_f32_16x16x32_bf16 v[44:47], v[170:173], v[214:217], v[44:47]
	v_mfma_f32_16x16x32_bf16 v[32:35], v[162:165], v[222:225], v[32:35]
	v_mfma_f32_16x16x32_bf16 v[28:31], v[170:173], v[222:225], v[28:31]
	v_mfma_f32_16x16x32_bf16 v[16:19], v[162:165], v[230:233], v[16:19]
	v_mfma_f32_16x16x32_bf16 v[12:15], v[170:173], v[230:233], v[12:15]
	v_mfma_f32_16x16x32_bf16 v[56:59], v[186:189], v[202:205], v[56:59]
	v_mfma_f32_16x16x32_bf16 v[52:55], v[194:197], v[202:205], v[52:55]
	v_mfma_f32_16x16x32_bf16 v[40:43], v[186:189], v[210:213], v[40:43]
	v_mfma_f32_16x16x32_bf16 v[36:39], v[194:197], v[210:213], v[36:39]
	v_mfma_f32_16x16x32_bf16 v[24:27], v[186:189], v[218:221], v[24:27]
	v_mfma_f32_16x16x32_bf16 v[20:23], v[194:197], v[218:221], v[20:23]
	v_mfma_f32_16x16x32_bf16 v[8:11], v[186:189], v[226:229], v[8:11]
	v_mfma_f32_16x16x32_bf16 v[4:7], v[194:197], v[226:229], v[4:7]
	v_mfma_f32_16x16x32_bf16 v[56:59], v[190:193], v[206:209], v[56:59]
	v_mfma_f32_16x16x32_bf16 v[52:55], v[198:201], v[206:209], v[52:55]
	v_mfma_f32_16x16x32_bf16 v[40:43], v[190:193], v[214:217], v[40:43]
	v_mfma_f32_16x16x32_bf16 v[36:39], v[198:201], v[214:217], v[36:39]
	s_barrier
	v_mfma_f32_16x16x32_bf16 v[24:27], v[190:193], v[222:225], v[24:27]
	v_mfma_f32_16x16x32_bf16 v[20:23], v[198:201], v[222:225], v[20:23]
	v_mfma_f32_16x16x32_bf16 v[8:11], v[190:193], v[230:233], v[8:11]
	v_mfma_f32_16x16x32_bf16 v[4:7], v[198:201], v[230:233], v[4:7]
	s_add_i32 s82, 0, 0x18000
	v_add_u32_e32 v3, s82, v178
	s_add_i32 s83, 0, 0x1c000
	ds_read_b128 v[138:141], v3
	ds_read_b128 v[162:165], v3 offset:1024
	ds_read_b128 v[166:169], v3 offset:2048
	ds_read_b128 v[170:173], v3 offset:3072
	v_add_u32_e32 v3, s83, v178
	ds_read_b128 v[186:189], v3
	ds_read_b128 v[190:193], v3 offset:1024
	ds_read_b128 v[194:197], v3 offset:2048
	ds_read_b128 v[198:201], v3 offset:3072
	s_add_u32 s56, s56, 0x80000
	s_addc_u32 s57, s57, 0
	s_mov_b32 m0, s64
	v_lshl_add_u64 v[238:239], s[56:57], 0, v[144:145]
	ds_read_b128 v[202:205], v184 offset:32768
	ds_read_b128 v[206:209], v184 offset:33792
	ds_read_b128 v[210:213], v184 offset:34816
	ds_read_b128 v[214:217], v184 offset:35840
	ds_read_b128 v[218:221], v184 offset:36864
	ds_read_b128 v[222:225], v184 offset:37888
	ds_read_b128 v[226:229], v184 offset:38912
	ds_read_b128 v[230:233], v184 offset:39936
	global_load_lds_dwordx4 v[238:239], off
	v_lshl_add_u64 v[238:239], s[56:57], 0, v[148:149]
	s_mov_b32 m0, s65
	s_nop 0
	global_load_lds_dwordx4 v[238:239], off
	s_waitcnt vmcnt(8)
	s_waitcnt lgkmcnt(0)
	s_barrier
	v_mfma_f32_16x16x32_bf16 v[128:131], v[138:141], v[202:205], v[128:131]
	v_mfma_f32_16x16x32_bf16 v[124:127], v[166:169], v[202:205], v[124:127]
	v_mfma_f32_16x16x32_bf16 v[120:123], v[138:141], v[210:213], v[120:123]
	v_mfma_f32_16x16x32_bf16 v[112:115], v[166:169], v[210:213], v[112:115]
	v_mfma_f32_16x16x32_bf16 v[96:99], v[138:141], v[218:221], v[96:99]
	v_mfma_f32_16x16x32_bf16 v[92:95], v[166:169], v[218:221], v[92:95]
	v_mfma_f32_16x16x32_bf16 v[80:83], v[138:141], v[226:229], v[80:83]
	v_mfma_f32_16x16x32_bf16 v[76:79], v[166:169], v[226:229], v[76:79]
	v_mfma_f32_16x16x32_bf16 v[128:131], v[162:165], v[206:209], v[128:131]
	v_mfma_f32_16x16x32_bf16 v[124:127], v[170:173], v[206:209], v[124:127]
	v_mfma_f32_16x16x32_bf16 v[120:123], v[162:165], v[214:217], v[120:123]
	v_mfma_f32_16x16x32_bf16 v[112:115], v[170:173], v[214:217], v[112:115]
	v_mfma_f32_16x16x32_bf16 v[96:99], v[162:165], v[222:225], v[96:99]
	v_mfma_f32_16x16x32_bf16 v[92:95], v[170:173], v[222:225], v[92:95]
	v_mfma_f32_16x16x32_bf16 v[80:83], v[162:165], v[230:233], v[80:83]
	v_mfma_f32_16x16x32_bf16 v[76:79], v[170:173], v[230:233], v[76:79]
	v_mfma_f32_16x16x32_bf16 v[116:119], v[186:189], v[202:205], v[116:119]
	v_mfma_f32_16x16x32_bf16 v[108:111], v[194:197], v[202:205], v[108:111]
	v_mfma_f32_16x16x32_bf16 v[104:107], v[186:189], v[210:213], v[104:107]
	v_mfma_f32_16x16x32_bf16 v[100:103], v[194:197], v[210:213], v[100:103]
	v_mfma_f32_16x16x32_bf16 v[88:91], v[186:189], v[218:221], v[88:91]
	v_mfma_f32_16x16x32_bf16 v[84:87], v[194:197], v[218:221], v[84:87]
	v_mfma_f32_16x16x32_bf16 v[72:75], v[186:189], v[226:229], v[72:75]
	v_mfma_f32_16x16x32_bf16 v[68:71], v[194:197], v[226:229], v[68:71]
	v_mfma_f32_16x16x32_bf16 v[116:119], v[190:193], v[206:209], v[116:119]
	v_mfma_f32_16x16x32_bf16 v[108:111], v[198:201], v[206:209], v[108:111]
	v_mfma_f32_16x16x32_bf16 v[104:107], v[190:193], v[214:217], v[104:107]
	v_mfma_f32_16x16x32_bf16 v[100:103], v[198:201], v[214:217], v[100:103]
	s_barrier
; #define PG8_STAGE(bufoff, gbase, voff) do { _Pragma("unroll") for (int _i = 0; _i < 2; ++_i) \
;         __builtin_amdgcn_global_load_lds((const unsigned*)((const char*)(gbase) + (voff)[_i]), (PG8_LAS unsigned*)(lds + (bufoff) + ldsw + _i * 8192), 16, 0, 0); } while (0)
; #define PG8_LDA(dst, b, h) do { _Pragma("unroll") for (int m = 0; m < 4; ++m) _Pragma("unroll") for (int k = 0; k < 2; ++k) dst[m][k] = *(const PG8_LAS bf16x8*)(lds + PG8_SA(b, h) + aoff + m * 2048 + k * 1024); } while (0)
; #define PG8_MMA(ai, bj, At, Bt) do { __builtin_amdgcn_s_setprio(1); _Pragma("unroll") for (int m = 0; m < 4; ++m) _Pragma("unroll") for (int n = 0; n < 2; ++n) _Pragma("unroll") for (int k = 0; k < 2; ++k) \
;         acc[ai][bj][m][n] = __builtin_amdgcn_mfma_f32_16x16x32_bf16(Bt[n][k], At[m][k], acc[ai][bj][m][n], 0, 0, 0); __builtin_amdgcn_s_setprio(0); } while (0)
; #define PG8_WAIT_V(n) asm volatile("s_waitcnt vmcnt(" #n ")" ::: "memory")
; #define PG8_WAIT_L(n) asm volatile("s_waitcnt lgkmcnt(" #n ")" ::: "memory")
; #define PG8_BAR __builtin_amdgcn_s_barrier()
; #define PG8_SCHED __builtin_amdgcn_sched_barrier(0)
; template <class Epi, class Sched, bool ALIGN_EPI = false>
; __device__ __forceinline__ void gemm_phase(PG8_LAS unsigned char* lds, const Gemm g, const Sched& S, const Epi& E) {
;     ...
;             PG8_WAIT_V(8); PG8_WAIT_L(0); PG8_BAR; PG8_MMA(0, 0, At, B0); PG8_MMA(0, 1, At, B1); PG8_BAR; PG8_SCHED;
;             PG8_LDA(At, 1, 1); PG8_STAGE(PG8_SB(1, 0), b3, voffB); PG8_STAGE(PG8_SB(1, 1), b3 + hstep, voffB); PG8_STAGE(PG8_SA(1, 0), a3, w0);
;             PG8_WAIT_V(8); PG8_WAIT_L(0); PG8_BAR; PG8_MMA(1, 0, At, B0); PG8_MMA(1, 1, At, B1); PG8_BAR; PG8_SCHED;
;             if constexpr (Epi::KSCALE) { if (((t + 2) & 7) == 0 && t + 2 < nt) { E.kscale(acc, pf, ((t + 2) >> 3) - 1, wr, fr); PG8_SCHED; } }
;         }
	v_mfma_f32_16x16x32_bf16 v[88:91], v[190:193], v[222:225], v[88:91]
	v_mfma_f32_16x16x32_bf16 v[84:87], v[198:201], v[222:225], v[84:87]
	v_mfma_f32_16x16x32_bf16 v[72:75], v[190:193], v[230:233], v[72:75]
	v_mfma_f32_16x16x32_bf16 v[68:71], v[198:201], v[230:233], v[68:71]
	s_add_i32 s56, s82, s61
	v_lshl_add_u64 v[142:143], v[142:143], 0, s[18:19]
	s_mov_b32 m0, s56
	ds_read_b128 v[202:205], v184 offset:49152
	ds_read_b128 v[206:209], v184 offset:50176
	ds_read_b128 v[210:213], v184 offset:51200
	ds_read_b128 v[214:217], v184 offset:52224
	ds_read_b128 v[218:221], v184 offset:53248
	ds_read_b128 v[222:225], v184 offset:54272
	ds_read_b128 v[226:229], v184 offset:55296
	ds_read_b128 v[230:233], v184 offset:56320
	global_load_lds_dwordx4 v[142:143], off
	s_add_i32 m0, s56, 0x2000
	s_add_u32 s54, s54, 0x80080
	v_lshl_add_u64 v[142:143], v[174:175], 0, s[18:19]
	s_addc_u32 s55, s55, 0
	s_add_i32 s56, s83, s61
	global_load_lds_dwordx4 v[142:143], off
	v_lshl_add_u64 v[142:143], s[54:55], 0, v[146:147]
	s_mov_b32 m0, s56
	s_nop 0
	global_load_lds_dwordx4 v[142:143], off
	v_lshl_add_u64 v[142:143], s[54:55], 0, v[150:151]
	s_add_i32 m0, s56, 0x2000
	s_nop 0
	global_load_lds_dwordx4 v[142:143], off
	v_lshl_add_u64 v[142:143], v[234:235], 0, s[18:19]
	s_mov_b32 m0, s68
	s_nop 0
	global_load_lds_dwordx4 v[142:143], off
	v_lshl_add_u64 v[142:143], v[236:237], 0, s[18:19]
	s_mov_b32 m0, s69
	s_nop 0
	global_load_lds_dwordx4 v[142:143], off
	s_waitcnt vmcnt(8)
	s_waitcnt lgkmcnt(0)
	s_barrier
	v_mfma_f32_16x16x32_bf16 v[64:67], v[138:141], v[202:205], v[64:67]
	v_mfma_f32_16x16x32_bf16 v[60:63], v[166:169], v[202:205], v[60:63]
	v_mfma_f32_16x16x32_bf16 v[48:51], v[138:141], v[210:213], v[48:51]
	v_mfma_f32_16x16x32_bf16 v[44:47], v[166:169], v[210:213], v[44:47]
	v_mfma_f32_16x16x32_bf16 v[32:35], v[138:141], v[218:221], v[32:35]
	v_mfma_f32_16x16x32_bf16 v[28:31], v[166:169], v[218:221], v[28:31]
	v_mfma_f32_16x16x32_bf16 v[16:19], v[138:141], v[226:229], v[16:19]
	v_mfma_f32_16x16x32_bf16 v[12:15], v[166:169], v[226:229], v[12:15]
	v_mfma_f32_16x16x32_bf16 v[64:67], v[162:165], v[206:209], v[64:67]
	v_mfma_f32_16x16x32_bf16 v[60:63], v[170:173], v[206:209], v[60:63]
	v_mfma_f32_16x16x32_bf16 v[48:51], v[162:165], v[214:217], v[48:51]
	v_mfma_f32_16x16x32_bf16 v[44:47], v[170:173], v[214:217], v[44:47]
	v_mfma_f32_16x16x32_bf16 v[32:35], v[162:165], v[222:225], v[32:35]
	v_mfma_f32_16x16x32_bf16 v[28:31], v[170:173], v[222:225], v[28:31]
	v_mfma_f32_16x16x32_bf16 v[16:19], v[162:165], v[230:233], v[16:19]
	v_mfma_f32_16x16x32_bf16 v[12:15], v[170:173], v[230:233], v[12:15]
	v_mfma_f32_16x16x32_bf16 v[56:59], v[186:189], v[202:205], v[56:59]
	v_mfma_f32_16x16x32_bf16 v[52:55], v[194:197], v[202:205], v[52:55]
	v_mfma_f32_16x16x32_bf16 v[40:43], v[186:189], v[210:213], v[40:43]
	v_mfma_f32_16x16x32_bf16 v[36:39], v[194:197], v[210:213], v[36:39]
	v_mfma_f32_16x16x32_bf16 v[24:27], v[186:189], v[218:221], v[24:27]
	v_mfma_f32_16x16x32_bf16 v[20:23], v[194:197], v[218:221], v[20:23]
	v_mfma_f32_16x16x32_bf16 v[8:11], v[186:189], v[226:229], v[8:11]
	v_mfma_f32_16x16x32_bf16 v[4:7], v[194:197], v[226:229], v[4:7]
	v_mfma_f32_16x16x32_bf16 v[56:59], v[190:193], v[206:209], v[56:59]
	v_mfma_f32_16x16x32_bf16 v[52:55], v[198:201], v[206:209], v[52:55]
	v_mfma_f32_16x16x32_bf16 v[40:43], v[190:193], v[214:217], v[40:43]
	v_mfma_f32_16x16x32_bf16 v[36:39], v[198:201], v[214:217], v[36:39]
	s_barrier
	v_mfma_f32_16x16x32_bf16 v[24:27], v[190:193], v[222:225], v[24:27]
	v_mfma_f32_16x16x32_bf16 v[20:23], v[198:201], v[222:225], v[20:23]
	v_mfma_f32_16x16x32_bf16 v[8:11], v[190:193], v[230:233], v[8:11]
	v_mfma_f32_16x16x32_bf16 v[4:7], v[198:201], v[230:233], v[4:7]
	s_mov_b32 s82, s81
	s_add_i32 s81, s81, 2
	s_and_b32 s54, s81, 6
	s_cmp_eq_u32 s54, 0
	s_cselect_b64 s[56:57], -1, 0
	s_cmp_gt_u32 s82, 29
	s_cselect_b64 s[54:55], -1, 0
	s_cmp_lt_u32 s82, 30
	s_cselect_b64 s[82:83], -1, 0
	s_and_b64 s[56:57], s[56:57], s[82:83]
	s_andn2_b64 vcc, exec, s[56:57]
	s_cbranch_vccnz .LBB0_503
; #define PG8_SCHED __builtin_amdgcn_sched_barrier(0)
;     __device__ __forceinline__ void kscale(f32x4 (&acc)[2][2][4][2], const Pre& pf, int b, int wr, int fr) const {
; #pragma unroll
;         for (int ai = 0; ai < 2; ++ai)
; #pragma unroll
;             for (int m = 0; m < 4; ++m) { const float f = pf.tab[(ai * HALF + wr * 64 + m * 16 + fr) * 4 + b];
; #pragma unroll
;                 for (int bj = 0; bj < 2; ++bj)
; #pragma unroll
;                     for (int n = 0; n < 2; ++n) acc[ai][bj][m][n] = acc[ai][bj][m][n] * f; }
;     }
; template <class Epi, class Sched, bool ALIGN_EPI = false>
; __device__ __forceinline__ void gemm_phase(PG8_LAS unsigned char* lds, const Gemm g, const Sched& S, const Epi& E) {
;     ...
;             if constexpr (Epi::KSCALE) { if (((t + 2) & 7) == 0 && t + 2 < nt) { E.kscale(acc, pf, ((t + 2) >> 3) - 1, wr, fr); PG8_SCHED; } }
	s_lshr_b32 s56, s81, 1
	v_add_u32_e32 v3, s56, v137
	v_add_u32_e32 v136, -4, v3
	ds_read_b32 v136, v136
	ds_read_b32 v138, v3 offset:2812
	ds_read2_b32 v[140:141], v3 offset0:63 offset1:127
	v_add_u32_e32 v3, 0xfc, v3
	s_waitcnt lgkmcnt(0)
	v_pk_mul_f32 v[130:131], v[130:131], v[136:137] op_sel_hi:[1,0]
	v_pk_mul_f32 v[128:129], v[128:129], v[136:137] op_sel_hi:[1,0]
	v_pk_mul_f32 v[126:127], v[126:127], v[136:137] op_sel_hi:[1,0]
	v_pk_mul_f32 v[124:125], v[124:125], v[136:137] op_sel_hi:[1,0]
	v_pk_mul_f32 v[118:119], v[118:119], v[136:137] op_sel_hi:[1,0]
	v_pk_mul_f32 v[116:117], v[116:117], v[136:137] op_sel_hi:[1,0]
	v_pk_mul_f32 v[110:111], v[110:111], v[136:137] op_sel_hi:[1,0]
	v_pk_mul_f32 v[108:109], v[108:109], v[136:137] op_sel_hi:[1,0]
	v_pk_mul_f32 v[122:123], v[122:123], v[140:141] op_sel_hi:[1,0]
	v_pk_mul_f32 v[120:121], v[120:121], v[140:141] op_sel_hi:[1,0]
	v_pk_mul_f32 v[114:115], v[114:115], v[140:141] op_sel_hi:[1,0]
	v_pk_mul_f32 v[112:113], v[112:113], v[140:141] op_sel_hi:[1,0]
	v_pk_mul_f32 v[106:107], v[106:107], v[140:141] op_sel_hi:[1,0]
	v_pk_mul_f32 v[104:105], v[104:105], v[140:141] op_sel_hi:[1,0]
	v_pk_mul_f32 v[102:103], v[102:103], v[140:141] op_sel_hi:[1,0]
	v_pk_mul_f32 v[100:101], v[100:101], v[140:141] op_sel_hi:[1,0]
	v_mov_b32_e32 v136, v141
	ds_read2st64_b32 v[140:141], v3 offset0:2 offset1:7
	v_pk_mul_f32 v[98:99], v[98:99], v[136:137] op_sel_hi:[1,0]
	v_pk_mul_f32 v[96:97], v[96:97], v[136:137] op_sel_hi:[1,0]
	v_pk_mul_f32 v[94:95], v[94:95], v[136:137] op_sel_hi:[1,0]
	v_pk_mul_f32 v[92:93], v[92:93], v[136:137] op_sel_hi:[1,0]
	v_pk_mul_f32 v[90:91], v[90:91], v[136:137] op_sel_hi:[1,0]
	v_pk_mul_f32 v[88:89], v[88:89], v[136:137] op_sel_hi:[1,0]
	v_pk_mul_f32 v[86:87], v[86:87], v[136:137] op_sel_hi:[1,0]
	v_pk_mul_f32 v[84:85], v[84:85], v[136:137] op_sel_hi:[1,0]
	s_waitcnt lgkmcnt(0)
	v_pk_mul_f32 v[82:83], v[82:83], v[140:141] op_sel_hi:[1,0]
	v_pk_mul_f32 v[80:81], v[80:81], v[140:141] op_sel_hi:[1,0]
	v_pk_mul_f32 v[78:79], v[78:79], v[140:141] op_sel_hi:[1,0]
	v_pk_mul_f32 v[76:77], v[76:77], v[140:141] op_sel_hi:[1,0]
	v_pk_mul_f32 v[74:75], v[74:75], v[140:141] op_sel_hi:[1,0]
	v_pk_mul_f32 v[72:73], v[72:73], v[140:141] op_sel_hi:[1,0]
	v_pk_mul_f32 v[70:71], v[70:71], v[140:141] op_sel_hi:[1,0]
	v_pk_mul_f32 v[68:69], v[68:69], v[140:141] op_sel_hi:[1,0]
	v_mov_b32_e32 v136, v141
	ds_read2st64_b32 v[140:141], v3 offset0:8 offset1:9
	v_pk_mul_f32 v[66:67], v[66:67], v[136:137] op_sel_hi:[1,0]
	v_pk_mul_f32 v[64:65], v[64:65], v[136:137] op_sel_hi:[1,0]
	v_pk_mul_f32 v[62:63], v[62:63], v[136:137] op_sel_hi:[1,0]
	v_pk_mul_f32 v[60:61], v[60:61], v[136:137] op_sel_hi:[1,0]
	v_pk_mul_f32 v[58:59], v[58:59], v[136:137] op_sel_hi:[1,0]
	v_pk_mul_f32 v[56:57], v[56:57], v[136:137] op_sel_hi:[1,0]
	v_pk_mul_f32 v[54:55], v[54:55], v[136:137] op_sel_hi:[1,0]
	v_pk_mul_f32 v[52:53], v[52:53], v[136:137] op_sel_hi:[1,0]
	s_waitcnt lgkmcnt(0)
	v_mov_b32_e32 v136, v141
	v_pk_mul_f32 v[50:51], v[50:51], v[140:141] op_sel_hi:[1,0]
	v_pk_mul_f32 v[48:49], v[48:49], v[140:141] op_sel_hi:[1,0]
	v_pk_mul_f32 v[46:47], v[46:47], v[140:141] op_sel_hi:[1,0]
	v_pk_mul_f32 v[44:45], v[44:45], v[140:141] op_sel_hi:[1,0]
	v_pk_mul_f32 v[42:43], v[42:43], v[140:141] op_sel_hi:[1,0]
	v_pk_mul_f32 v[40:41], v[40:41], v[140:141] op_sel_hi:[1,0]
	v_pk_mul_f32 v[38:39], v[38:39], v[140:141] op_sel_hi:[1,0]
	v_pk_mul_f32 v[36:37], v[36:37], v[140:141] op_sel_hi:[1,0]
	v_pk_mul_f32 v[34:35], v[34:35], v[136:137] op_sel_hi:[1,0]
	v_pk_mul_f32 v[32:33], v[32:33], v[136:137] op_sel_hi:[1,0]
	v_pk_mul_f32 v[30:31], v[30:31], v[136:137] op_sel_hi:[1,0]
	v_pk_mul_f32 v[28:29], v[28:29], v[136:137] op_sel_hi:[1,0]
	v_pk_mul_f32 v[26:27], v[26:27], v[136:137] op_sel_hi:[1,0]
	v_pk_mul_f32 v[24:25], v[24:25], v[136:137] op_sel_hi:[1,0]
	v_pk_mul_f32 v[22:23], v[22:23], v[136:137] op_sel_hi:[1,0]
	v_pk_mul_f32 v[20:21], v[20:21], v[136:137] op_sel_hi:[1,0]
	v_pk_mul_f32 v[18:19], v[18:19], v[138:139] op_sel_hi:[1,0]
	v_pk_mul_f32 v[16:17], v[16:17], v[138:139] op_sel_hi:[1,0]
	v_pk_mul_f32 v[14:15], v[14:15], v[138:139] op_sel_hi:[1,0]
	v_pk_mul_f32 v[12:13], v[12:13], v[138:139] op_sel_hi:[1,0]
	v_pk_mul_f32 v[10:11], v[10:11], v[138:139] op_sel_hi:[1,0]
	v_pk_mul_f32 v[8:9], v[8:9], v[138:139] op_sel_hi:[1,0]
	v_pk_mul_f32 v[6:7], v[6:7], v[138:139] op_sel_hi:[1,0]
	v_pk_mul_f32 v[4:5], v[4:5], v[138:139] op_sel_hi:[1,0]
	s_branch .LBB0_503

; #define PG8_STAGE(bufoff, gbase, voff) do { _Pragma("unroll") for (int _i = 0; _i < 2; ++_i) \
;         __builtin_amdgcn_global_load_lds((const unsigned*)((const char*)(gbase) + (voff)[_i]), (PG8_LAS unsigned*)(lds + (bufoff) + ldsw + _i * 8192), 16, 0, 0); } while (0)
; #define PG8_LDA(dst, b, h) do { _Pragma("unroll") for (int m = 0; m < 4; ++m) _Pragma("unroll") for (int k = 0; k < 2; ++k) dst[m][k] = *(const PG8_LAS bf16x8*)(lds + PG8_SA(b, h) + aoff + m * 2048 + k * 1024); } while (0)
; #define PG8_LDB(dst, b, h) do { _Pragma("unroll") for (int n = 0; n < 2; ++n) _Pragma("unroll") for (int k = 0; k < 2; ++k) dst[n][k] = *(const PG8_LAS bf16x8*)(lds + PG8_SB(b, h) + boff + n * 2048 + k * 1024); } while (0)
; #define PG8_MMA(ai, bj, At, Bt) do { __builtin_amdgcn_s_setprio(1); _Pragma("unroll") for (int m = 0; m < 4; ++m) _Pragma("unroll") for (int n = 0; n < 2; ++n) _Pragma("unroll") for (int k = 0; k < 2; ++k) \
;         acc[ai][bj][m][n] = __builtin_amdgcn_mfma_f32_16x16x32_bf16(Bt[n][k], At[m][k], acc[ai][bj][m][n], 0, 0, 0); __builtin_amdgcn_s_setprio(0); } while (0)
; template <class Epi, class Sched, bool ALIGN_EPI = false>
; __device__ __forceinline__ void gemm_phase(PG8_LAS unsigned char* lds, const Gemm g, const Sched& S, const Epi& E) {
;     ...
;         for (int t = 0; t < nt; t += 2) {
;             const bool last = (t == nt - 2);
;             const char* a1 = cA + (size_t)(t + 1) * kstep;
;             const char* a2 = last ? nA : cA + (size_t)(t + 2) * kstep; const char* b2 = last ? nB : cB + (size_t)(t + 2) * kstep;
;             const char* a3 = a2 + kstep; const char* b3 = b2 + kstep;
;             unsigned w0[2], w1[2];
; #pragma unroll
;             for (int i = 0; i < 2; ++i) { w0[i] = (Sched::GATHER && last) ? vn0[i] : vc0[i]; w1[i] = (Sched::GATHER && last) ? vn1[i] : vc1[i]; }
;             if (last && has_next) S.a_ready(nxt);
;             PG8_LDB(B0, 0, 0); PG8_LDB(B1, 0, 1); PG8_SCHED; PG8_LDA(At, 0, 0); PG8_STAGE(PG8_SA(1, 1), a1 + hstepA, vc1);
;             PG8_WAIT_V(8); PG8_WAIT_L(0); PG8_BAR; PG8_MMA(0, 0, At, B0); PG8_MMA(0, 1, At, B1); PG8_BAR; PG8_SCHED;
;             PG8_LDA(At, 0, 1); PG8_STAGE(PG8_SB(0, 0), b2, voffB); PG8_STAGE(PG8_SB(0, 1), b2 + hstep, voffB); PG8_STAGE(PG8_SA(0, 0), a2, w0);
;             PG8_WAIT_V(8); PG8_WAIT_L(0); PG8_BAR; PG8_MMA(1, 0, At, B0); PG8_MMA(1, 1, At, B1); PG8_BAR; PG8_SCHED;
.LBB0_721:
	s_add_u32 s58, s36, s56
	v_add_u32_e32 v155, s82, v143
	s_addc_u32 s59, s37, s57
	ds_read_b128 v[164:167], v155
	ds_read_b128 v[168:171], v155 offset:1024
	ds_read_b128 v[172:175], v155 offset:2048
	ds_read_b128 v[176:179], v155 offset:3072
	v_add_u32_e32 v155, s83, v143
	s_add_u32 s60, s58, 0x3c800100
	ds_read_b128 v[180:183], v155
	ds_read_b128 v[184:187], v155 offset:1024
	ds_read_b128 v[188:191], v155 offset:2048
	ds_read_b128 v[192:195], v155 offset:3072
	s_addc_u32 s61, s59, 0
	s_add_u32 s91, s49, s56
	s_addc_u32 s92, s89, s57
	s_cmpk_eq_i32 s56, 0xf00
	s_cselect_b64 vcc, -1, 0
	s_and_b64 s[58:59], vcc, exec
	v_cndmask_b32_e32 v134, v151, v149, vcc
	s_cselect_b32 s61, s21, s61
	s_cselect_b32 s60, s20, s60
	v_cndmask_b32_e32 v153, v152, v157, vcc
	v_cndmask_b32_e32 v228, v150, v162, vcc
	v_cndmask_b32_e32 v155, v154, v163, vcc
	s_cselect_b32 s59, s53, s92
	s_cselect_b32 s58, s52, s91
	v_lshl_add_u64 v[230:231], v[160:161], 0, s[56:57]
	s_add_i32 m0, s55, 0xc000
	ds_read_b128 v[196:199], v147
	ds_read_b128 v[200:203], v147 offset:1024
	ds_read_b128 v[204:207], v147 offset:2048
	ds_read_b128 v[208:211], v147 offset:3072
	ds_read_b128 v[212:215], v147 offset:4096
	ds_read_b128 v[216:219], v147 offset:5120
	ds_read_b128 v[220:223], v147 offset:6144
	ds_read_b128 v[224:227], v147 offset:7168
	global_load_lds_dwordx4 v[230:231], off
	v_lshl_add_u64 v[230:231], v[158:159], 0, s[56:57]
	s_add_i32 m0, s55, 0xe000
	s_nop 0
	global_load_lds_dwordx4 v[230:231], off
	s_waitcnt vmcnt(8)
	s_waitcnt lgkmcnt(0)
	s_barrier
	v_mfma_f32_16x16x32_bf16 v[126:129], v[164:167], v[196:199], v[126:129]
	v_mfma_f32_16x16x32_bf16 v[122:125], v[172:175], v[196:199], v[122:125]
	v_mfma_f32_16x16x32_bf16 v[110:113], v[164:167], v[204:207], v[110:113]
	v_mfma_f32_16x16x32_bf16 v[106:109], v[172:175], v[204:207], v[106:109]
	v_mfma_f32_16x16x32_bf16 v[94:97], v[164:167], v[212:215], v[94:97]
	v_mfma_f32_16x16x32_bf16 v[90:93], v[172:175], v[212:215], v[90:93]
	v_mfma_f32_16x16x32_bf16 v[78:81], v[164:167], v[220:223], v[78:81]
	v_mfma_f32_16x16x32_bf16 v[74:77], v[172:175], v[220:223], v[74:77]
	v_mfma_f32_16x16x32_bf16 v[126:129], v[168:171], v[200:203], v[126:129]
	v_mfma_f32_16x16x32_bf16 v[122:125], v[176:179], v[200:203], v[122:125]
	v_mfma_f32_16x16x32_bf16 v[110:113], v[168:171], v[208:211], v[110:113]
	v_mfma_f32_16x16x32_bf16 v[106:109], v[176:179], v[208:211], v[106:109]
	v_mfma_f32_16x16x32_bf16 v[94:97], v[168:171], v[216:219], v[94:97]
	v_mfma_f32_16x16x32_bf16 v[90:93], v[176:179], v[216:219], v[90:93]
	v_mfma_f32_16x16x32_bf16 v[78:81], v[168:171], v[224:227], v[78:81]
	v_mfma_f32_16x16x32_bf16 v[74:77], v[176:179], v[224:227], v[74:77]
	v_mfma_f32_16x16x32_bf16 v[118:121], v[180:183], v[196:199], v[118:121]
	v_mfma_f32_16x16x32_bf16 v[114:117], v[188:191], v[196:199], v[114:117]
	v_mfma_f32_16x16x32_bf16 v[102:105], v[180:183], v[204:207], v[102:105]
	v_mfma_f32_16x16x32_bf16 v[98:101], v[188:191], v[204:207], v[98:101]
	v_mfma_f32_16x16x32_bf16 v[86:89], v[180:183], v[212:215], v[86:89]
	v_mfma_f32_16x16x32_bf16 v[82:85], v[188:191], v[212:215], v[82:85]
	v_mfma_f32_16x16x32_bf16 v[70:73], v[180:183], v[220:223], v[70:73]
	v_mfma_f32_16x16x32_bf16 v[66:69], v[188:191], v[220:223], v[66:69]
	v_mfma_f32_16x16x32_bf16 v[118:121], v[184:187], v[200:203], v[118:121]
	v_mfma_f32_16x16x32_bf16 v[114:117], v[192:195], v[200:203], v[114:117]
	v_mfma_f32_16x16x32_bf16 v[102:105], v[184:187], v[208:211], v[102:105]
	v_mfma_f32_16x16x32_bf16 v[98:101], v[192:195], v[208:211], v[98:101]
	s_barrier
	v_mfma_f32_16x16x32_bf16 v[86:89], v[184:187], v[216:219], v[86:89]
	v_mfma_f32_16x16x32_bf16 v[82:85], v[192:195], v[216:219], v[82:85]
	v_mfma_f32_16x16x32_bf16 v[70:73], v[184:187], v[224:227], v[70:73]
	v_mfma_f32_16x16x32_bf16 v[66:69], v[192:195], v[224:227], v[66:69]
	s_add_i32 s91, s82, s74
	v_lshl_add_u64 v[230:231], s[58:59], 0, v[130:131]
	s_mov_b32 m0, s91
	ds_read_b128 v[196:199], v147 offset:16384
	ds_read_b128 v[200:203], v147 offset:17408
	ds_read_b128 v[204:207], v147 offset:18432
	ds_read_b128 v[208:211], v147 offset:19456
	ds_read_b128 v[212:215], v147 offset:20480
	ds_read_b128 v[216:219], v147 offset:21504
	ds_read_b128 v[220:223], v147 offset:22528
	ds_read_b128 v[224:227], v147 offset:23552
	global_load_lds_dwordx4 v[230:231], off
	s_add_i32 m0, s91, 0x2000
	s_add_u32 s92, s58, 0x80000
	v_lshl_add_u64 v[232:233], s[58:59], 0, v[132:133]
	s_addc_u32 s93, s59, 0
	s_add_i32 s91, s83, s74
	global_load_lds_dwordx4 v[232:233], off
	v_lshl_add_u64 v[234:235], s[92:93], 0, v[130:131]
	s_mov_b32 m0, s91
	v_mov_b32_e32 v229, v135
	global_load_lds_dwordx4 v[234:235], off
	v_lshl_add_u64 v[234:235], s[92:93], 0, v[132:133]
	s_add_i32 m0, s91, 0x2000
	s_nop 0
	global_load_lds_dwordx4 v[234:235], off
	s_mov_b32 m0, s55
	v_lshl_add_u64 v[234:235], s[60:61], 0, v[134:135]
	global_load_lds_dwordx4 v134, s[60:61]
	s_mov_b32 m0, s75
	s_nop 0
	global_load_lds_dwordx4 v228, s[60:61]
	s_waitcnt vmcnt(8)
	s_waitcnt lgkmcnt(0)
	v_lshl_add_u64 v[228:229], s[60:61], 0, v[228:229]
	s_barrier
; #define PG8_STAGE(bufoff, gbase, voff) do { _Pragma("unroll") for (int _i = 0; _i < 2; ++_i) \
;         __builtin_amdgcn_global_load_lds((const unsigned*)((const char*)(gbase) + (voff)[_i]), (PG8_LAS unsigned*)(lds + (bufoff) + ldsw + _i * 8192), 16, 0, 0); } while (0)
; #define PG8_LDA(dst, b, h) do { _Pragma("unroll") for (int m = 0; m < 4; ++m) _Pragma("unroll") for (int k = 0; k < 2; ++k) dst[m][k] = *(const PG8_LAS bf16x8*)(lds + PG8_SA(b, h) + aoff + m * 2048 + k * 1024); } while (0)
; #define PG8_LDB(dst, b, h) do { _Pragma("unroll") for (int n = 0; n < 2; ++n) _Pragma("unroll") for (int k = 0; k < 2; ++k) dst[n][k] = *(const PG8_LAS bf16x8*)(lds + PG8_SB(b, h) + boff + n * 2048 + k * 1024); } while (0)
; #define PG8_MMA(ai, bj, At, Bt) do { __builtin_amdgcn_s_setprio(1); _Pragma("unroll") for (int m = 0; m < 4; ++m) _Pragma("unroll") for (int n = 0; n < 2; ++n) _Pragma("unroll") for (int k = 0; k < 2; ++k) \
;         acc[ai][bj][m][n] = __builtin_amdgcn_mfma_f32_16x16x32_bf16(Bt[n][k], At[m][k], acc[ai][bj][m][n], 0, 0, 0); __builtin_amdgcn_s_setprio(0); } while (0)
; #define PG8_WAIT_V(n) asm volatile("s_waitcnt vmcnt(" #n ")" ::: "memory")
; #define PG8_WAIT_L(n) asm volatile("s_waitcnt lgkmcnt(" #n ")" ::: "memory")
; #define PG8_BAR __builtin_amdgcn_s_barrier()
; #define PG8_SCHED __builtin_amdgcn_sched_barrier(0)
; template <class Epi, class Sched, bool ALIGN_EPI = false>
; __device__ __forceinline__ void gemm_phase(PG8_LAS unsigned char* lds, const Gemm g, const Sched& S, const Epi& E) {
;     ...
;             PG8_WAIT_V(8); PG8_WAIT_L(0); PG8_BAR; PG8_MMA(1, 0, At, B0); PG8_MMA(1, 1, At, B1); PG8_BAR; PG8_SCHED;
;             PG8_LDB(B0, 1, 0); PG8_LDB(B1, 1, 1); PG8_SCHED; PG8_LDA(At, 1, 0); PG8_STAGE(PG8_SA(0, 1), a2 + hstepA, w1);
;             PG8_WAIT_V(8); PG8_WAIT_L(0); PG8_BAR; PG8_MMA(0, 0, At, B0); PG8_MMA(0, 1, At, B1); PG8_BAR; PG8_SCHED;
	v_mfma_f32_16x16x32_bf16 v[62:65], v[164:167], v[196:199], v[62:65]
	v_mfma_f32_16x16x32_bf16 v[58:61], v[172:175], v[196:199], v[58:61]
	v_mfma_f32_16x16x32_bf16 v[50:53], v[164:167], v[204:207], v[50:53]
	v_mfma_f32_16x16x32_bf16 v[42:45], v[172:175], v[204:207], v[42:45]
	v_mfma_f32_16x16x32_bf16 v[34:37], v[164:167], v[212:215], v[34:37]
	v_mfma_f32_16x16x32_bf16 v[30:33], v[172:175], v[212:215], v[30:33]
	v_mfma_f32_16x16x32_bf16 v[14:17], v[164:167], v[220:223], v[14:17]
	v_mfma_f32_16x16x32_bf16 v[2:5], v[172:175], v[220:223], v[2:5]
	v_mfma_f32_16x16x32_bf16 v[62:65], v[168:171], v[200:203], v[62:65]
	v_mfma_f32_16x16x32_bf16 v[58:61], v[176:179], v[200:203], v[58:61]
	v_mfma_f32_16x16x32_bf16 v[50:53], v[168:171], v[208:211], v[50:53]
	v_mfma_f32_16x16x32_bf16 v[42:45], v[176:179], v[208:211], v[42:45]
	v_mfma_f32_16x16x32_bf16 v[34:37], v[168:171], v[216:219], v[34:37]
	v_mfma_f32_16x16x32_bf16 v[30:33], v[176:179], v[216:219], v[30:33]
	v_mfma_f32_16x16x32_bf16 v[14:17], v[168:171], v[224:227], v[14:17]
	v_mfma_f32_16x16x32_bf16 v[2:5], v[176:179], v[224:227], v[2:5]
	v_mfma_f32_16x16x32_bf16 v[54:57], v[180:183], v[196:199], v[54:57]
	v_mfma_f32_16x16x32_bf16 v[46:49], v[188:191], v[196:199], v[46:49]
	v_mfma_f32_16x16x32_bf16 v[38:41], v[180:183], v[204:207], v[38:41]
	v_mfma_f32_16x16x32_bf16 v[26:29], v[188:191], v[204:207], v[26:29]
	v_mfma_f32_16x16x32_bf16 v[22:25], v[180:183], v[212:215], v[22:25]
	v_mfma_f32_16x16x32_bf16 v[18:21], v[188:191], v[212:215], v[18:21]
	v_mfma_f32_16x16x32_bf16 v[10:13], v[180:183], v[220:223], v[10:13]
	v_mfma_f32_16x16x32_bf16 v[6:9], v[188:191], v[220:223], v[6:9]
	v_mfma_f32_16x16x32_bf16 v[54:57], v[184:187], v[200:203], v[54:57]
	v_mfma_f32_16x16x32_bf16 v[46:49], v[192:195], v[200:203], v[46:49]
	v_mfma_f32_16x16x32_bf16 v[38:41], v[184:187], v[208:211], v[38:41]
	v_mfma_f32_16x16x32_bf16 v[26:29], v[192:195], v[208:211], v[26:29]
	s_barrier
	v_mfma_f32_16x16x32_bf16 v[22:25], v[184:187], v[216:219], v[22:25]
	v_mfma_f32_16x16x32_bf16 v[18:21], v[192:195], v[216:219], v[18:21]
	v_mfma_f32_16x16x32_bf16 v[10:13], v[184:187], v[224:227], v[10:13]
	v_mfma_f32_16x16x32_bf16 v[6:9], v[192:195], v[224:227], v[6:9]
	s_add_i32 s91, 0, 0x18000
	v_add_u32_e32 v134, s91, v143
	s_add_i32 s92, 0, 0x1c000
	ds_read_b128 v[164:167], v134
	ds_read_b128 v[168:171], v134 offset:1024
	ds_read_b128 v[172:175], v134 offset:2048
	ds_read_b128 v[176:179], v134 offset:3072
	v_add_u32_e32 v134, s92, v143
	ds_read_b128 v[180:183], v134
	ds_read_b128 v[184:187], v134 offset:1024
	ds_read_b128 v[188:191], v134 offset:2048
	ds_read_b128 v[192:195], v134 offset:3072
	s_mov_b32 m0, s76
	ds_read_b128 v[196:199], v147 offset:32768
	ds_read_b128 v[200:203], v147 offset:33792
	ds_read_b128 v[204:207], v147 offset:34816
	ds_read_b128 v[208:211], v147 offset:35840
	ds_read_b128 v[212:215], v147 offset:36864
	ds_read_b128 v[216:219], v147 offset:37888
	ds_read_b128 v[220:223], v147 offset:38912
	ds_read_b128 v[224:227], v147 offset:39936
	global_load_lds_dwordx4 v153, s[60:61]
	s_mov_b32 m0, s77
	s_nop 0
	global_load_lds_dwordx4 v155, s[60:61]
	s_waitcnt vmcnt(8)
	s_waitcnt lgkmcnt(0)
	s_barrier
	v_mfma_f32_16x16x32_bf16 v[126:129], v[164:167], v[196:199], v[126:129]
	v_mfma_f32_16x16x32_bf16 v[122:125], v[172:175], v[196:199], v[122:125]
	v_mfma_f32_16x16x32_bf16 v[110:113], v[164:167], v[204:207], v[110:113]
	v_mfma_f32_16x16x32_bf16 v[106:109], v[172:175], v[204:207], v[106:109]
	v_mfma_f32_16x16x32_bf16 v[94:97], v[164:167], v[212:215], v[94:97]
	v_mfma_f32_16x16x32_bf16 v[90:93], v[172:175], v[212:215], v[90:93]
	v_mfma_f32_16x16x32_bf16 v[78:81], v[164:167], v[220:223], v[78:81]
	v_mfma_f32_16x16x32_bf16 v[74:77], v[172:175], v[220:223], v[74:77]
	v_mfma_f32_16x16x32_bf16 v[126:129], v[168:171], v[200:203], v[126:129]
	v_mfma_f32_16x16x32_bf16 v[122:125], v[176:179], v[200:203], v[122:125]
	v_mfma_f32_16x16x32_bf16 v[110:113], v[168:171], v[208:211], v[110:113]
	v_mfma_f32_16x16x32_bf16 v[106:109], v[176:179], v[208:211], v[106:109]
	v_mfma_f32_16x16x32_bf16 v[94:97], v[168:171], v[216:219], v[94:97]
	v_mfma_f32_16x16x32_bf16 v[90:93], v[176:179], v[216:219], v[90:93]
	v_mfma_f32_16x16x32_bf16 v[78:81], v[168:171], v[224:227], v[78:81]
	v_mfma_f32_16x16x32_bf16 v[74:77], v[176:179], v[224:227], v[74:77]
	v_mfma_f32_16x16x32_bf16 v[118:121], v[180:183], v[196:199], v[118:121]
	v_mfma_f32_16x16x32_bf16 v[114:117], v[188:191], v[196:199], v[114:117]
	v_mfma_f32_16x16x32_bf16 v[102:105], v[180:183], v[204:207], v[102:105]
	v_mfma_f32_16x16x32_bf16 v[98:101], v[188:191], v[204:207], v[98:101]
	v_mfma_f32_16x16x32_bf16 v[86:89], v[180:183], v[212:215], v[86:89]
	v_mfma_f32_16x16x32_bf16 v[82:85], v[188:191], v[212:215], v[82:85]
	v_mfma_f32_16x16x32_bf16 v[70:73], v[180:183], v[220:223], v[70:73]
	v_mfma_f32_16x16x32_bf16 v[66:69], v[188:191], v[220:223], v[66:69]
	v_mfma_f32_16x16x32_bf16 v[118:121], v[184:187], v[200:203], v[118:121]
	v_mfma_f32_16x16x32_bf16 v[114:117], v[192:195], v[200:203], v[114:117]
	v_mfma_f32_16x16x32_bf16 v[102:105], v[184:187], v[208:211], v[102:105]
	v_mfma_f32_16x16x32_bf16 v[98:101], v[192:195], v[208:211], v[98:101]
	s_barrier
; #define PG8_STAGE(bufoff, gbase, voff) do { _Pragma("unroll") for (int _i = 0; _i < 2; ++_i) \
;         __builtin_amdgcn_global_load_lds((const unsigned*)((const char*)(gbase) + (voff)[_i]), (PG8_LAS unsigned*)(lds + (bufoff) + ldsw + _i * 8192), 16, 0, 0); } while (0)
; #define PG8_LDA(dst, b, h) do { _Pragma("unroll") for (int m = 0; m < 4; ++m) _Pragma("unroll") for (int k = 0; k < 2; ++k) dst[m][k] = *(const PG8_LAS bf16x8*)(lds + PG8_SA(b, h) + aoff + m * 2048 + k * 1024); } while (0)
; #define PG8_MMA(ai, bj, At, Bt) do { __builtin_amdgcn_s_setprio(1); _Pragma("unroll") for (int m = 0; m < 4; ++m) _Pragma("unroll") for (int n = 0; n < 2; ++n) _Pragma("unroll") for (int k = 0; k < 2; ++k) \
;         acc[ai][bj][m][n] = __builtin_amdgcn_mfma_f32_16x16x32_bf16(Bt[n][k], At[m][k], acc[ai][bj][m][n], 0, 0, 0); __builtin_amdgcn_s_setprio(0); } while (0)
; #define PG8_WAIT_V(n) asm volatile("s_waitcnt vmcnt(" #n ")" ::: "memory")
; #define PG8_WAIT_L(n) asm volatile("s_waitcnt lgkmcnt(" #n ")" ::: "memory")
; #define PG8_BAR __builtin_amdgcn_s_barrier()
; #define PG8_SCHED __builtin_amdgcn_sched_barrier(0)
; template <class Epi, class Sched, bool ALIGN_EPI = false>
; __device__ __forceinline__ void gemm_phase(PG8_LAS unsigned char* lds, const Gemm g, const Sched& S, const Epi& E) {
;     ...
;             PG8_WAIT_V(8); PG8_WAIT_L(0); PG8_BAR; PG8_MMA(0, 0, At, B0); PG8_MMA(0, 1, At, B1); PG8_BAR; PG8_SCHED;
;             PG8_LDA(At, 1, 1); PG8_STAGE(PG8_SB(1, 0), b3, voffB); PG8_STAGE(PG8_SB(1, 1), b3 + hstep, voffB); PG8_STAGE(PG8_SA(1, 0), a3, w0);
;             PG8_WAIT_V(8); PG8_WAIT_L(0); PG8_BAR; PG8_MMA(1, 0, At, B0); PG8_MMA(1, 1, At, B1); PG8_BAR; PG8_SCHED;
;             if constexpr (Epi::KSCALE) { if (((t + 2) & 7) == 0 && t + 2 < nt) { E.kscale(acc, pf, ((t + 2) >> 3) - 1, wr, fr); PG8_SCHED; } }
;         }
;         if constexpr (ALIGN_EPI) { if (wr == 0) PG8_BAR; }
	v_mfma_f32_16x16x32_bf16 v[86:89], v[184:187], v[216:219], v[86:89]
	v_mfma_f32_16x16x32_bf16 v[82:85], v[192:195], v[216:219], v[82:85]
	v_mfma_f32_16x16x32_bf16 v[70:73], v[184:187], v[224:227], v[70:73]
	v_mfma_f32_16x16x32_bf16 v[66:69], v[192:195], v[224:227], v[66:69]
	s_add_i32 s60, s91, s74
	v_lshl_add_u64 v[230:231], v[230:231], 0, s[44:45]
	s_mov_b32 m0, s60
	ds_read_b128 v[196:199], v147 offset:49152
	ds_read_b128 v[200:203], v147 offset:50176
	ds_read_b128 v[204:207], v147 offset:51200
	ds_read_b128 v[208:211], v147 offset:52224
	ds_read_b128 v[212:215], v147 offset:53248
	ds_read_b128 v[216:219], v147 offset:54272
	ds_read_b128 v[220:223], v147 offset:55296
	ds_read_b128 v[224:227], v147 offset:56320
	global_load_lds_dwordx4 v[230:231], off
	s_add_i32 m0, s60, 0x2000
	s_add_u32 s58, s58, 0x80080
	v_lshl_add_u64 v[230:231], v[232:233], 0, s[44:45]
	s_addc_u32 s59, s59, 0
	s_add_i32 s60, s92, s74
	global_load_lds_dwordx4 v[230:231], off
	v_lshl_add_u64 v[230:231], s[58:59], 0, v[130:131]
	s_mov_b32 m0, s60
	v_lshl_add_u64 v[228:229], v[228:229], 0, s[44:45]
	global_load_lds_dwordx4 v[230:231], off
	v_lshl_add_u64 v[230:231], s[58:59], 0, v[132:133]
	s_add_i32 m0, s60, 0x2000
	s_nop 0
	global_load_lds_dwordx4 v[230:231], off
	v_lshl_add_u64 v[230:231], v[234:235], 0, s[44:45]
	s_mov_b32 m0, s80
	s_nop 0
	global_load_lds_dwordx4 v[230:231], off
	s_mov_b32 m0, s81
	s_nop 0
	global_load_lds_dwordx4 v[228:229], off
	s_waitcnt vmcnt(8)
	s_waitcnt lgkmcnt(0)
	s_barrier
	v_mfma_f32_16x16x32_bf16 v[62:65], v[164:167], v[196:199], v[62:65]
	v_mfma_f32_16x16x32_bf16 v[58:61], v[172:175], v[196:199], v[58:61]
	v_mfma_f32_16x16x32_bf16 v[50:53], v[164:167], v[204:207], v[50:53]
	v_mfma_f32_16x16x32_bf16 v[42:45], v[172:175], v[204:207], v[42:45]
	v_mfma_f32_16x16x32_bf16 v[34:37], v[164:167], v[212:215], v[34:37]
	v_mfma_f32_16x16x32_bf16 v[30:33], v[172:175], v[212:215], v[30:33]
	v_mfma_f32_16x16x32_bf16 v[14:17], v[164:167], v[220:223], v[14:17]
	v_mfma_f32_16x16x32_bf16 v[2:5], v[172:175], v[220:223], v[2:5]
	v_mfma_f32_16x16x32_bf16 v[62:65], v[168:171], v[200:203], v[62:65]
	v_mfma_f32_16x16x32_bf16 v[58:61], v[176:179], v[200:203], v[58:61]
	v_mfma_f32_16x16x32_bf16 v[50:53], v[168:171], v[208:211], v[50:53]
	v_mfma_f32_16x16x32_bf16 v[42:45], v[176:179], v[208:211], v[42:45]
	v_mfma_f32_16x16x32_bf16 v[34:37], v[168:171], v[216:219], v[34:37]
	v_mfma_f32_16x16x32_bf16 v[30:33], v[176:179], v[216:219], v[30:33]
	v_mfma_f32_16x16x32_bf16 v[14:17], v[168:171], v[224:227], v[14:17]
	v_mfma_f32_16x16x32_bf16 v[2:5], v[176:179], v[224:227], v[2:5]
	v_mfma_f32_16x16x32_bf16 v[54:57], v[180:183], v[196:199], v[54:57]
	v_mfma_f32_16x16x32_bf16 v[46:49], v[188:191], v[196:199], v[46:49]
	v_mfma_f32_16x16x32_bf16 v[38:41], v[180:183], v[204:207], v[38:41]
	v_mfma_f32_16x16x32_bf16 v[26:29], v[188:191], v[204:207], v[26:29]
	v_mfma_f32_16x16x32_bf16 v[22:25], v[180:183], v[212:215], v[22:25]
	v_mfma_f32_16x16x32_bf16 v[18:21], v[188:191], v[212:215], v[18:21]
	v_mfma_f32_16x16x32_bf16 v[10:13], v[180:183], v[220:223], v[10:13]
	v_mfma_f32_16x16x32_bf16 v[6:9], v[188:191], v[220:223], v[6:9]
	v_mfma_f32_16x16x32_bf16 v[54:57], v[184:187], v[200:203], v[54:57]
	v_mfma_f32_16x16x32_bf16 v[46:49], v[192:195], v[200:203], v[46:49]
	v_mfma_f32_16x16x32_bf16 v[38:41], v[184:187], v[208:211], v[38:41]
	v_mfma_f32_16x16x32_bf16 v[26:29], v[192:195], v[208:211], v[26:29]
	s_barrier
	v_mfma_f32_16x16x32_bf16 v[22:25], v[184:187], v[216:219], v[22:25]
	v_mfma_f32_16x16x32_bf16 v[18:21], v[192:195], v[216:219], v[18:21]
	v_mfma_f32_16x16x32_bf16 v[10:13], v[184:187], v[224:227], v[10:13]
	v_mfma_f32_16x16x32_bf16 v[6:9], v[192:195], v[224:227], v[6:9]
	s_add_i32 s90, s90, 2
	s_add_u32 s56, s56, 0x100
	s_addc_u32 s57, s57, 0
	s_cmp_gt_u32 s90, 29
	s_cbranch_scc0 .LBB0_721
	s_and_b64 vcc, exec, s[46:47]
	s_cbranch_vccz .LBB0_724
	s_barrier

; #define PG8_STAGE(bufoff, gbase, voff) do { _Pragma("unroll") for (int _i = 0; _i < 2; ++_i) \
;         __builtin_amdgcn_global_load_lds((const unsigned*)((const char*)(gbase) + (voff)[_i]), (PG8_LAS unsigned*)(lds + (bufoff) + ldsw + _i * 8192), 16, 0, 0); } while (0)
; #define PG8_LDA(dst, b, h) do { _Pragma("unroll") for (int m = 0; m < 4; ++m) _Pragma("unroll") for (int k = 0; k < 2; ++k) dst[m][k] = *(const PG8_LAS bf16x8*)(lds + PG8_SA(b, h) + aoff + m * 2048 + k * 1024); } while (0)
; #define PG8_LDB(dst, b, h) do { _Pragma("unroll") for (int n = 0; n < 2; ++n) _Pragma("unroll") for (int k = 0; k < 2; ++k) dst[n][k] = *(const PG8_LAS bf16x8*)(lds + PG8_SB(b, h) + boff + n * 2048 + k * 1024); } while (0)
; #define PG8_MMA(ai, bj, At, Bt) do { __builtin_amdgcn_s_setprio(1); _Pragma("unroll") for (int m = 0; m < 4; ++m) _Pragma("unroll") for (int n = 0; n < 2; ++n) _Pragma("unroll") for (int k = 0; k < 2; ++k) \
;         acc[ai][bj][m][n] = __builtin_amdgcn_mfma_f32_16x16x32_bf16(Bt[n][k], At[m][k], acc[ai][bj][m][n], 0, 0, 0); __builtin_amdgcn_s_setprio(0); } while (0)
; template <class Epi, class Sched, bool ALIGN_EPI = false>
; __device__ __forceinline__ void gemm_phase(PG8_LAS unsigned char* lds, const Gemm g, const Sched& S, const Epi& E) {
;     ...
;         for (int t = 0; t < nt; t += 2) {
;             const bool last = (t == nt - 2);
;             const char* a1 = cA + (size_t)(t + 1) * kstep;
;             const char* a2 = last ? nA : cA + (size_t)(t + 2) * kstep; const char* b2 = last ? nB : cB + (size_t)(t + 2) * kstep;
;             const char* a3 = a2 + kstep; const char* b3 = b2 + kstep;
;             unsigned w0[2], w1[2];
; #pragma unroll
;             for (int i = 0; i < 2; ++i) { w0[i] = (Sched::GATHER && last) ? vn0[i] : vc0[i]; w1[i] = (Sched::GATHER && last) ? vn1[i] : vc1[i]; }
;             if (last && has_next) S.a_ready(nxt);
;             PG8_LDB(B0, 0, 0); PG8_LDB(B1, 0, 1); PG8_SCHED; PG8_LDA(At, 0, 0); PG8_STAGE(PG8_SA(1, 1), a1 + hstepA, vc1);
;             PG8_WAIT_V(8); PG8_WAIT_L(0); PG8_BAR; PG8_MMA(0, 0, At, B0); PG8_MMA(0, 1, At, B1); PG8_BAR; PG8_SCHED;
;             PG8_LDA(At, 0, 1); PG8_STAGE(PG8_SB(0, 0), b2, voffB); PG8_STAGE(PG8_SB(0, 1), b2 + hstep, voffB); PG8_STAGE(PG8_SA(0, 0), a2, w0);
;             PG8_WAIT_V(8); PG8_WAIT_L(0); PG8_BAR; PG8_MMA(1, 0, At, B0); PG8_MMA(1, 1, At, B1); PG8_BAR; PG8_SCHED;
.LBB0_787:
	ds_read_b128 v[172:175], v167
	ds_read_b128 v[176:179], v167 offset:1024
	ds_read_b128 v[180:183], v167 offset:2048
	ds_read_b128 v[184:187], v167 offset:3072
	ds_read_b128 v[188:191], v168
	ds_read_b128 v[192:195], v168 offset:1024
	ds_read_b128 v[196:199], v168 offset:2048
	ds_read_b128 v[200:203], v168 offset:3072
	s_add_u32 s18, s16, 0x3c800100
	s_addc_u32 s19, s17, 0
	s_add_u32 s58, s16, s45
	s_addc_u32 s59, s17, s46
	s_cmp_eq_u32 s47, 28
	s_cselect_b32 s23, s21, s19
	s_cselect_b32 s22, s20, s18
	s_cselect_b32 s19, s13, s59
	s_cselect_b32 s18, s12, s58
	s_mov_b32 m0, s48
	v_lshl_add_u64 v[236:237], s[16:17], 0, v[160:161]
	ds_read_b128 v[204:207], v169
	ds_read_b128 v[208:211], v169 offset:1024
	ds_read_b128 v[212:215], v169 offset:2048
	ds_read_b128 v[216:219], v169 offset:3072
	ds_read_b128 v[220:223], v169 offset:4096
	ds_read_b128 v[224:227], v169 offset:5120
	ds_read_b128 v[228:231], v169 offset:6144
	ds_read_b128 v[232:235], v169 offset:7168
	global_load_lds_dwordx4 v[236:237], off
	v_lshl_add_u64 v[236:237], s[16:17], 0, v[158:159]
	s_mov_b32 m0, s49
	s_nop 0
	global_load_lds_dwordx4 v[236:237], off
	s_waitcnt vmcnt(8)
	s_waitcnt lgkmcnt(0)
	s_barrier
	v_mfma_f32_16x16x32_bf16 v[126:129], v[172:175], v[204:207], v[126:129]
	v_mfma_f32_16x16x32_bf16 v[122:125], v[180:183], v[204:207], v[122:125]
	v_mfma_f32_16x16x32_bf16 v[110:113], v[172:175], v[212:215], v[110:113]
	v_mfma_f32_16x16x32_bf16 v[106:109], v[180:183], v[212:215], v[106:109]
	v_mfma_f32_16x16x32_bf16 v[94:97], v[172:175], v[220:223], v[94:97]
	v_mfma_f32_16x16x32_bf16 v[90:93], v[180:183], v[220:223], v[90:93]
	v_mfma_f32_16x16x32_bf16 v[78:81], v[172:175], v[228:231], v[78:81]
	v_mfma_f32_16x16x32_bf16 v[74:77], v[180:183], v[228:231], v[74:77]
	v_mfma_f32_16x16x32_bf16 v[126:129], v[176:179], v[208:211], v[126:129]
	v_mfma_f32_16x16x32_bf16 v[122:125], v[184:187], v[208:211], v[122:125]
	v_mfma_f32_16x16x32_bf16 v[110:113], v[176:179], v[216:219], v[110:113]
	v_mfma_f32_16x16x32_bf16 v[106:109], v[184:187], v[216:219], v[106:109]
	v_mfma_f32_16x16x32_bf16 v[94:97], v[176:179], v[224:227], v[94:97]
	v_mfma_f32_16x16x32_bf16 v[90:93], v[184:187], v[224:227], v[90:93]
	v_mfma_f32_16x16x32_bf16 v[78:81], v[176:179], v[232:235], v[78:81]
	v_mfma_f32_16x16x32_bf16 v[74:77], v[184:187], v[232:235], v[74:77]
	v_mfma_f32_16x16x32_bf16 v[118:121], v[188:191], v[204:207], v[118:121]
	v_mfma_f32_16x16x32_bf16 v[114:117], v[196:199], v[204:207], v[114:117]
	v_mfma_f32_16x16x32_bf16 v[102:105], v[188:191], v[212:215], v[102:105]
	v_mfma_f32_16x16x32_bf16 v[98:101], v[196:199], v[212:215], v[98:101]
	v_mfma_f32_16x16x32_bf16 v[86:89], v[188:191], v[220:223], v[86:89]
	v_mfma_f32_16x16x32_bf16 v[82:85], v[196:199], v[220:223], v[82:85]
	v_mfma_f32_16x16x32_bf16 v[70:73], v[188:191], v[228:231], v[70:73]
	v_mfma_f32_16x16x32_bf16 v[66:69], v[196:199], v[228:231], v[66:69]
	v_mfma_f32_16x16x32_bf16 v[118:121], v[192:195], v[208:211], v[118:121]
	v_mfma_f32_16x16x32_bf16 v[114:117], v[200:203], v[208:211], v[114:117]
	v_mfma_f32_16x16x32_bf16 v[102:105], v[192:195], v[216:219], v[102:105]
	v_mfma_f32_16x16x32_bf16 v[98:101], v[200:203], v[216:219], v[98:101]
	s_barrier
	v_mfma_f32_16x16x32_bf16 v[86:89], v[192:195], v[224:227], v[86:89]
	v_mfma_f32_16x16x32_bf16 v[82:85], v[200:203], v[224:227], v[82:85]
	v_mfma_f32_16x16x32_bf16 v[70:73], v[192:195], v[232:235], v[70:73]
	v_mfma_f32_16x16x32_bf16 v[66:69], v[200:203], v[232:235], v[66:69]
	s_mov_b32 m0, s50
	v_lshl_add_u64 v[236:237], s[18:19], 0, v[146:147]
	s_add_u32 s58, s18, 0x80000
	ds_read_b128 v[204:207], v169 offset:16384
	ds_read_b128 v[208:211], v169 offset:17408
	ds_read_b128 v[212:215], v169 offset:18432
	ds_read_b128 v[216:219], v169 offset:19456
	ds_read_b128 v[220:223], v169 offset:20480
	ds_read_b128 v[224:227], v169 offset:21504
	ds_read_b128 v[228:231], v169 offset:22528
	ds_read_b128 v[232:235], v169 offset:23552
	global_load_lds_dwordx4 v[236:237], off
	v_lshl_add_u64 v[238:239], s[18:19], 0, v[144:145]
	s_mov_b32 m0, s51
	s_addc_u32 s59, s19, 0
	global_load_lds_dwordx4 v[238:239], off
	v_lshl_add_u64 v[240:241], s[58:59], 0, v[146:147]
	s_mov_b32 m0, s52
	v_lshl_add_u64 v[242:243], s[22:23], 0, v[150:151]
	global_load_lds_dwordx4 v[240:241], off
	v_lshl_add_u64 v[240:241], s[58:59], 0, v[144:145]
	s_mov_b32 m0, s53
	s_nop 0
	global_load_lds_dwordx4 v[240:241], off
	v_lshl_add_u64 v[240:241], s[22:23], 0, v[148:149]
	s_mov_b32 m0, s27
	s_nop 0
	global_load_lds_dwordx4 v[240:241], off
	s_mov_b32 m0, s35
	s_nop 0
	global_load_lds_dwordx4 v[242:243], off
	s_waitcnt vmcnt(8)
	s_waitcnt lgkmcnt(0)
	s_barrier
	v_mfma_f32_16x16x32_bf16 v[62:65], v[172:175], v[204:207], v[62:65]
	v_mfma_f32_16x16x32_bf16 v[58:61], v[180:183], v[204:207], v[58:61]
	v_mfma_f32_16x16x32_bf16 v[50:53], v[172:175], v[212:215], v[50:53]
	v_mfma_f32_16x16x32_bf16 v[42:45], v[180:183], v[212:215], v[42:45]
	v_mfma_f32_16x16x32_bf16 v[34:37], v[172:175], v[220:223], v[34:37]
	v_mfma_f32_16x16x32_bf16 v[26:29], v[180:183], v[220:223], v[26:29]
	v_mfma_f32_16x16x32_bf16 v[14:17], v[172:175], v[228:231], v[14:17]
	v_mfma_f32_16x16x32_bf16 v[2:5], v[180:183], v[228:231], v[2:5]
	v_mfma_f32_16x16x32_bf16 v[62:65], v[176:179], v[208:211], v[62:65]
	v_mfma_f32_16x16x32_bf16 v[58:61], v[184:187], v[208:211], v[58:61]
	v_mfma_f32_16x16x32_bf16 v[50:53], v[176:179], v[216:219], v[50:53]
	v_mfma_f32_16x16x32_bf16 v[42:45], v[184:187], v[216:219], v[42:45]
	v_mfma_f32_16x16x32_bf16 v[34:37], v[176:179], v[224:227], v[34:37]
	v_mfma_f32_16x16x32_bf16 v[26:29], v[184:187], v[224:227], v[26:29]
	v_mfma_f32_16x16x32_bf16 v[14:17], v[176:179], v[232:235], v[14:17]
	v_mfma_f32_16x16x32_bf16 v[2:5], v[184:187], v[232:235], v[2:5]
	v_mfma_f32_16x16x32_bf16 v[54:57], v[188:191], v[204:207], v[54:57]
	v_mfma_f32_16x16x32_bf16 v[46:49], v[196:199], v[204:207], v[46:49]
	v_mfma_f32_16x16x32_bf16 v[38:41], v[188:191], v[212:215], v[38:41]
	v_mfma_f32_16x16x32_bf16 v[30:33], v[196:199], v[212:215], v[30:33]
	v_mfma_f32_16x16x32_bf16 v[22:25], v[188:191], v[220:223], v[22:25]
	v_mfma_f32_16x16x32_bf16 v[18:21], v[196:199], v[220:223], v[18:21]
	v_mfma_f32_16x16x32_bf16 v[10:13], v[188:191], v[228:231], v[10:13]
	v_mfma_f32_16x16x32_bf16 v[6:9], v[196:199], v[228:231], v[6:9]
	v_mfma_f32_16x16x32_bf16 v[54:57], v[192:195], v[208:211], v[54:57]
	v_mfma_f32_16x16x32_bf16 v[46:49], v[200:203], v[208:211], v[46:49]
	v_mfma_f32_16x16x32_bf16 v[38:41], v[192:195], v[216:219], v[38:41]
	v_mfma_f32_16x16x32_bf16 v[30:33], v[200:203], v[216:219], v[30:33]
	s_barrier
; #define PG8_STAGE(bufoff, gbase, voff) do { _Pragma("unroll") for (int _i = 0; _i < 2; ++_i) \
;         __builtin_amdgcn_global_load_lds((const unsigned*)((const char*)(gbase) + (voff)[_i]), (PG8_LAS unsigned*)(lds + (bufoff) + ldsw + _i * 8192), 16, 0, 0); } while (0)
; #define PG8_LDA(dst, b, h) do { _Pragma("unroll") for (int m = 0; m < 4; ++m) _Pragma("unroll") for (int k = 0; k < 2; ++k) dst[m][k] = *(const PG8_LAS bf16x8*)(lds + PG8_SA(b, h) + aoff + m * 2048 + k * 1024); } while (0)
; #define PG8_LDB(dst, b, h) do { _Pragma("unroll") for (int n = 0; n < 2; ++n) _Pragma("unroll") for (int k = 0; k < 2; ++k) dst[n][k] = *(const PG8_LAS bf16x8*)(lds + PG8_SB(b, h) + boff + n * 2048 + k * 1024); } while (0)
; #define PG8_MMA(ai, bj, At, Bt) do { __builtin_amdgcn_s_setprio(1); _Pragma("unroll") for (int m = 0; m < 4; ++m) _Pragma("unroll") for (int n = 0; n < 2; ++n) _Pragma("unroll") for (int k = 0; k < 2; ++k) \
;         acc[ai][bj][m][n] = __builtin_amdgcn_mfma_f32_16x16x32_bf16(Bt[n][k], At[m][k], acc[ai][bj][m][n], 0, 0, 0); __builtin_amdgcn_s_setprio(0); } while (0)
; #define PG8_WAIT_V(n) asm volatile("s_waitcnt vmcnt(" #n ")" ::: "memory")
; #define PG8_WAIT_L(n) asm volatile("s_waitcnt lgkmcnt(" #n ")" ::: "memory")
; #define PG8_BAR __builtin_amdgcn_s_barrier()
; #define PG8_SCHED __builtin_amdgcn_sched_barrier(0)
; template <class Epi, class Sched, bool ALIGN_EPI = false>
; __device__ __forceinline__ void gemm_phase(PG8_LAS unsigned char* lds, const Gemm g, const Sched& S, const Epi& E) {
;     ...
;             PG8_WAIT_V(8); PG8_WAIT_L(0); PG8_BAR; PG8_MMA(1, 0, At, B0); PG8_MMA(1, 1, At, B1); PG8_BAR; PG8_SCHED;
;             PG8_LDB(B0, 1, 0); PG8_LDB(B1, 1, 1); PG8_SCHED; PG8_LDA(At, 1, 0); PG8_STAGE(PG8_SA(0, 1), a2 + hstepA, w1);
;             PG8_WAIT_V(8); PG8_WAIT_L(0); PG8_BAR; PG8_MMA(0, 0, At, B0); PG8_MMA(0, 1, At, B1); PG8_BAR; PG8_SCHED;
	v_mfma_f32_16x16x32_bf16 v[22:25], v[192:195], v[224:227], v[22:25]
	v_mfma_f32_16x16x32_bf16 v[18:21], v[200:203], v[224:227], v[18:21]
	v_mfma_f32_16x16x32_bf16 v[10:13], v[192:195], v[232:235], v[10:13]
	v_mfma_f32_16x16x32_bf16 v[6:9], v[200:203], v[232:235], v[6:9]
	ds_read_b128 v[172:175], v170
	ds_read_b128 v[176:179], v170 offset:1024
	ds_read_b128 v[180:183], v170 offset:2048
	ds_read_b128 v[184:187], v170 offset:3072
	ds_read_b128 v[188:191], v171
	ds_read_b128 v[192:195], v171 offset:1024
	ds_read_b128 v[196:199], v171 offset:2048
	ds_read_b128 v[200:203], v171 offset:3072
	s_mov_b32 m0, s40
	v_lshl_add_u64 v[244:245], s[22:23], 0, v[152:153]
	ds_read_b128 v[204:207], v169 offset:32768
	ds_read_b128 v[208:211], v169 offset:33792
	ds_read_b128 v[212:215], v169 offset:34816
	ds_read_b128 v[216:219], v169 offset:35840
	ds_read_b128 v[220:223], v169 offset:36864
	ds_read_b128 v[224:227], v169 offset:37888
	ds_read_b128 v[228:231], v169 offset:38912
	ds_read_b128 v[232:235], v169 offset:39936
	global_load_lds_dwordx4 v[244:245], off
	v_lshl_add_u64 v[244:245], s[22:23], 0, v[154:155]
	s_mov_b32 m0, s41
	s_nop 0
	global_load_lds_dwordx4 v[244:245], off
	s_waitcnt vmcnt(8)
	s_waitcnt lgkmcnt(0)
	s_barrier
	v_mfma_f32_16x16x32_bf16 v[126:129], v[172:175], v[204:207], v[126:129]
	v_mfma_f32_16x16x32_bf16 v[122:125], v[180:183], v[204:207], v[122:125]
	v_mfma_f32_16x16x32_bf16 v[110:113], v[172:175], v[212:215], v[110:113]
	v_mfma_f32_16x16x32_bf16 v[106:109], v[180:183], v[212:215], v[106:109]
	v_mfma_f32_16x16x32_bf16 v[94:97], v[172:175], v[220:223], v[94:97]
	v_mfma_f32_16x16x32_bf16 v[90:93], v[180:183], v[220:223], v[90:93]
	v_mfma_f32_16x16x32_bf16 v[78:81], v[172:175], v[228:231], v[78:81]
	v_mfma_f32_16x16x32_bf16 v[74:77], v[180:183], v[228:231], v[74:77]
	v_mfma_f32_16x16x32_bf16 v[126:129], v[176:179], v[208:211], v[126:129]
	v_mfma_f32_16x16x32_bf16 v[122:125], v[184:187], v[208:211], v[122:125]
	v_mfma_f32_16x16x32_bf16 v[110:113], v[176:179], v[216:219], v[110:113]
	v_mfma_f32_16x16x32_bf16 v[106:109], v[184:187], v[216:219], v[106:109]
	v_mfma_f32_16x16x32_bf16 v[94:97], v[176:179], v[224:227], v[94:97]
	v_mfma_f32_16x16x32_bf16 v[90:93], v[184:187], v[224:227], v[90:93]
	v_mfma_f32_16x16x32_bf16 v[78:81], v[176:179], v[232:235], v[78:81]
	v_mfma_f32_16x16x32_bf16 v[74:77], v[184:187], v[232:235], v[74:77]
	v_mfma_f32_16x16x32_bf16 v[118:121], v[188:191], v[204:207], v[118:121]
	v_mfma_f32_16x16x32_bf16 v[114:117], v[196:199], v[204:207], v[114:117]
	v_mfma_f32_16x16x32_bf16 v[102:105], v[188:191], v[212:215], v[102:105]
	v_mfma_f32_16x16x32_bf16 v[98:101], v[196:199], v[212:215], v[98:101]
	v_mfma_f32_16x16x32_bf16 v[86:89], v[188:191], v[220:223], v[86:89]
	v_mfma_f32_16x16x32_bf16 v[82:85], v[196:199], v[220:223], v[82:85]
	v_mfma_f32_16x16x32_bf16 v[70:73], v[188:191], v[228:231], v[70:73]
	v_mfma_f32_16x16x32_bf16 v[66:69], v[196:199], v[228:231], v[66:69]
	v_mfma_f32_16x16x32_bf16 v[118:121], v[192:195], v[208:211], v[118:121]
	v_mfma_f32_16x16x32_bf16 v[114:117], v[200:203], v[208:211], v[114:117]
	v_mfma_f32_16x16x32_bf16 v[102:105], v[192:195], v[216:219], v[102:105]
	v_mfma_f32_16x16x32_bf16 v[98:101], v[200:203], v[216:219], v[98:101]
	s_barrier
; #define PG8_STAGE(bufoff, gbase, voff) do { _Pragma("unroll") for (int _i = 0; _i < 2; ++_i) \
;         __builtin_amdgcn_global_load_lds((const unsigned*)((const char*)(gbase) + (voff)[_i]), (PG8_LAS unsigned*)(lds + (bufoff) + ldsw + _i * 8192), 16, 0, 0); } while (0)
; #define PG8_LDA(dst, b, h) do { _Pragma("unroll") for (int m = 0; m < 4; ++m) _Pragma("unroll") for (int k = 0; k < 2; ++k) dst[m][k] = *(const PG8_LAS bf16x8*)(lds + PG8_SA(b, h) + aoff + m * 2048 + k * 1024); } while (0)
; #define PG8_MMA(ai, bj, At, Bt) do { __builtin_amdgcn_s_setprio(1); _Pragma("unroll") for (int m = 0; m < 4; ++m) _Pragma("unroll") for (int n = 0; n < 2; ++n) _Pragma("unroll") for (int k = 0; k < 2; ++k) \
;         acc[ai][bj][m][n] = __builtin_amdgcn_mfma_f32_16x16x32_bf16(Bt[n][k], At[m][k], acc[ai][bj][m][n], 0, 0, 0); __builtin_amdgcn_s_setprio(0); } while (0)
; #define PG8_WAIT_V(n) asm volatile("s_waitcnt vmcnt(" #n ")" ::: "memory")
; #define PG8_WAIT_L(n) asm volatile("s_waitcnt lgkmcnt(" #n ")" ::: "memory")
; #define PG8_BAR __builtin_amdgcn_s_barrier()
; #define PG8_SCHED __builtin_amdgcn_sched_barrier(0)
; template <class Epi, class Sched, bool ALIGN_EPI = false>
; __device__ __forceinline__ void gemm_phase(PG8_LAS unsigned char* lds, const Gemm g, const Sched& S, const Epi& E) {
;     ...
;             PG8_WAIT_V(8); PG8_WAIT_L(0); PG8_BAR; PG8_MMA(0, 0, At, B0); PG8_MMA(0, 1, At, B1); PG8_BAR; PG8_SCHED;
;             PG8_LDA(At, 1, 1); PG8_STAGE(PG8_SB(1, 0), b3, voffB); PG8_STAGE(PG8_SB(1, 1), b3 + hstep, voffB); PG8_STAGE(PG8_SA(1, 0), a3, w0);
;             PG8_WAIT_V(8); PG8_WAIT_L(0); PG8_BAR; PG8_MMA(1, 0, At, B0); PG8_MMA(1, 1, At, B1); PG8_BAR; PG8_SCHED;
;             if constexpr (Epi::KSCALE) { if (((t + 2) & 7) == 0 && t + 2 < nt) { E.kscale(acc, pf, ((t + 2) >> 3) - 1, wr, fr); PG8_SCHED; } }
;         }
;         if constexpr (ALIGN_EPI) { if (wr == 0) PG8_BAR; }
	v_mfma_f32_16x16x32_bf16 v[86:89], v[192:195], v[224:227], v[86:89]
	v_mfma_f32_16x16x32_bf16 v[82:85], v[200:203], v[224:227], v[82:85]
	v_mfma_f32_16x16x32_bf16 v[70:73], v[192:195], v[232:235], v[70:73]
	v_mfma_f32_16x16x32_bf16 v[66:69], v[200:203], v[232:235], v[66:69]
	s_mov_b32 m0, s54
	v_lshl_add_u64 v[236:237], v[236:237], 0, s[14:15]
	s_add_u32 s18, s18, 0x80080
	ds_read_b128 v[204:207], v169 offset:49152
	ds_read_b128 v[208:211], v169 offset:50176
	ds_read_b128 v[212:215], v169 offset:51200
	ds_read_b128 v[216:219], v169 offset:52224
	ds_read_b128 v[220:223], v169 offset:53248
	ds_read_b128 v[224:227], v169 offset:54272
	ds_read_b128 v[228:231], v169 offset:55296
	ds_read_b128 v[232:235], v169 offset:56320
	global_load_lds_dwordx4 v[236:237], off
	v_lshl_add_u64 v[236:237], v[238:239], 0, s[14:15]
	s_mov_b32 m0, s55
	s_addc_u32 s19, s19, 0
	global_load_lds_dwordx4 v[236:237], off
	v_lshl_add_u64 v[236:237], s[18:19], 0, v[146:147]
	s_mov_b32 m0, s56
	s_nop 0
	global_load_lds_dwordx4 v[236:237], off
	v_lshl_add_u64 v[236:237], s[18:19], 0, v[144:145]
	s_mov_b32 m0, s57
	s_nop 0
	global_load_lds_dwordx4 v[236:237], off
	v_lshl_add_u64 v[236:237], v[240:241], 0, s[14:15]
	s_mov_b32 m0, s43
	s_nop 0
	global_load_lds_dwordx4 v[236:237], off
	v_lshl_add_u64 v[236:237], v[242:243], 0, s[14:15]
	s_mov_b32 m0, s44
	s_nop 0
	global_load_lds_dwordx4 v[236:237], off
	s_waitcnt vmcnt(8)
	s_waitcnt lgkmcnt(0)
	s_barrier
	v_mfma_f32_16x16x32_bf16 v[62:65], v[172:175], v[204:207], v[62:65]
	v_mfma_f32_16x16x32_bf16 v[58:61], v[180:183], v[204:207], v[58:61]
	v_mfma_f32_16x16x32_bf16 v[50:53], v[172:175], v[212:215], v[50:53]
	v_mfma_f32_16x16x32_bf16 v[42:45], v[180:183], v[212:215], v[42:45]
	v_mfma_f32_16x16x32_bf16 v[34:37], v[172:175], v[220:223], v[34:37]
	v_mfma_f32_16x16x32_bf16 v[26:29], v[180:183], v[220:223], v[26:29]
	v_mfma_f32_16x16x32_bf16 v[14:17], v[172:175], v[228:231], v[14:17]
	v_mfma_f32_16x16x32_bf16 v[2:5], v[180:183], v[228:231], v[2:5]
	v_mfma_f32_16x16x32_bf16 v[62:65], v[176:179], v[208:211], v[62:65]
	v_mfma_f32_16x16x32_bf16 v[58:61], v[184:187], v[208:211], v[58:61]
	v_mfma_f32_16x16x32_bf16 v[50:53], v[176:179], v[216:219], v[50:53]
	v_mfma_f32_16x16x32_bf16 v[42:45], v[184:187], v[216:219], v[42:45]
	v_mfma_f32_16x16x32_bf16 v[34:37], v[176:179], v[224:227], v[34:37]
	v_mfma_f32_16x16x32_bf16 v[26:29], v[184:187], v[224:227], v[26:29]
	v_mfma_f32_16x16x32_bf16 v[14:17], v[176:179], v[232:235], v[14:17]
	v_mfma_f32_16x16x32_bf16 v[2:5], v[184:187], v[232:235], v[2:5]
	v_mfma_f32_16x16x32_bf16 v[54:57], v[188:191], v[204:207], v[54:57]
	v_mfma_f32_16x16x32_bf16 v[46:49], v[196:199], v[204:207], v[46:49]
	v_mfma_f32_16x16x32_bf16 v[38:41], v[188:191], v[212:215], v[38:41]
	v_mfma_f32_16x16x32_bf16 v[30:33], v[196:199], v[212:215], v[30:33]
	v_mfma_f32_16x16x32_bf16 v[22:25], v[188:191], v[220:223], v[22:25]
	v_mfma_f32_16x16x32_bf16 v[18:21], v[196:199], v[220:223], v[18:21]
	v_mfma_f32_16x16x32_bf16 v[10:13], v[188:191], v[228:231], v[10:13]
	v_mfma_f32_16x16x32_bf16 v[6:9], v[196:199], v[228:231], v[6:9]
	v_mfma_f32_16x16x32_bf16 v[54:57], v[192:195], v[208:211], v[54:57]
	v_mfma_f32_16x16x32_bf16 v[46:49], v[200:203], v[208:211], v[46:49]
	v_mfma_f32_16x16x32_bf16 v[38:41], v[192:195], v[216:219], v[38:41]
	v_mfma_f32_16x16x32_bf16 v[30:33], v[200:203], v[216:219], v[30:33]
	s_barrier
	v_mfma_f32_16x16x32_bf16 v[22:25], v[192:195], v[224:227], v[22:25]
	v_mfma_f32_16x16x32_bf16 v[18:21], v[200:203], v[224:227], v[18:21]
	v_mfma_f32_16x16x32_bf16 v[10:13], v[192:195], v[232:235], v[10:13]
	v_mfma_f32_16x16x32_bf16 v[6:9], v[200:203], v[232:235], v[6:9]
	s_add_i32 s47, s47, 2
	s_add_u32 s16, s16, 0x100
	s_addc_u32 s17, s17, 0
	s_cmp_gt_u32 s47, 29
	s_cbranch_scc0 .LBB0_787
	s_cmpk_lt_u32 s24, 0x100
	s_cbranch_scc0 .LBB0_790
	s_barrier

; #define PG8_STAGE(bufoff, gbase, voff) do { _Pragma("unroll") for (int _i = 0; _i < 2; ++_i) \
;         __builtin_amdgcn_global_load_lds((const unsigned*)((const char*)(gbase) + (voff)[_i]), (PG8_LAS unsigned*)(lds + (bufoff) + ldsw + _i * 8192), 16, 0, 0); } while (0)
; #define PG8_LDA(dst, b, h) do { _Pragma("unroll") for (int m = 0; m < 4; ++m) _Pragma("unroll") for (int k = 0; k < 2; ++k) dst[m][k] = *(const PG8_LAS bf16x8*)(lds + PG8_SA(b, h) + aoff + m * 2048 + k * 1024); } while (0)
; #define PG8_LDB(dst, b, h) do { _Pragma("unroll") for (int n = 0; n < 2; ++n) _Pragma("unroll") for (int k = 0; k < 2; ++k) dst[n][k] = *(const PG8_LAS bf16x8*)(lds + PG8_SB(b, h) + boff + n * 2048 + k * 1024); } while (0)
; #define PG8_MMA(ai, bj, At, Bt) do { __builtin_amdgcn_s_setprio(1); _Pragma("unroll") for (int m = 0; m < 4; ++m) _Pragma("unroll") for (int n = 0; n < 2; ++n) _Pragma("unroll") for (int k = 0; k < 2; ++k) \
;         acc[ai][bj][m][n] = __builtin_amdgcn_mfma_f32_16x16x32_bf16(Bt[n][k], At[m][k], acc[ai][bj][m][n], 0, 0, 0); __builtin_amdgcn_s_setprio(0); } while (0)
; template <class Epi, class Sched, bool ALIGN_EPI = false>
; __device__ __forceinline__ void gemm_phase(PG8_LAS unsigned char* lds, const Gemm g, const Sched& S, const Epi& E) {
;     ...
;         for (int t = 0; t < nt; t += 2) {
;             const bool last = (t == nt - 2);
;             const char* a1 = cA + (size_t)(t + 1) * kstep;
;             const char* a2 = last ? nA : cA + (size_t)(t + 2) * kstep; const char* b2 = last ? nB : cB + (size_t)(t + 2) * kstep;
;             const char* a3 = a2 + kstep; const char* b3 = b2 + kstep;
;             unsigned w0[2], w1[2];
; #pragma unroll
;             for (int i = 0; i < 2; ++i) { w0[i] = (Sched::GATHER && last) ? vn0[i] : vc0[i]; w1[i] = (Sched::GATHER && last) ? vn1[i] : vc1[i]; }
;             if (last && has_next) S.a_ready(nxt);
;             PG8_LDB(B0, 0, 0); PG8_LDB(B1, 0, 1); PG8_SCHED; PG8_LDA(At, 0, 0); PG8_STAGE(PG8_SA(1, 1), a1 + hstepA, vc1);
;             PG8_WAIT_V(8); PG8_WAIT_L(0); PG8_BAR; PG8_MMA(0, 0, At, B0); PG8_MMA(0, 1, At, B1); PG8_BAR; PG8_SCHED;
;             PG8_LDA(At, 0, 1); PG8_STAGE(PG8_SB(0, 0), b2, voffB); PG8_STAGE(PG8_SB(0, 1), b2 + hstep, voffB); PG8_STAGE(PG8_SA(0, 0), a2, w0);
;             PG8_WAIT_V(8); PG8_WAIT_L(0); PG8_BAR; PG8_MMA(1, 0, At, B0); PG8_MMA(1, 1, At, B1); PG8_BAR; PG8_SCHED;
.LBB0_805:
	ds_read_b128 v[142:145], v1
	ds_read_b128 v[158:161], v1 offset:1024
	ds_read_b128 v[162:165], v1 offset:2048
	ds_read_b128 v[166:169], v1 offset:3072
	ds_read_b128 v[170:173], v156
	ds_read_b128 v[174:177], v156 offset:1024
	ds_read_b128 v[178:181], v156 offset:2048
	ds_read_b128 v[182:185], v156 offset:3072
	s_add_u32 s62, s60, 0xfffe0080
	s_addc_u32 s63, s61, -1
	s_cmp_eq_u32 s92, 4
	s_cselect_b32 s65, s45, s63
	s_cselect_b32 s64, s57, s62
	s_cselect_b32 s63, s47, s91
	s_cselect_b32 s62, s89, s90
	v_lshl_add_u64 v[218:219], s[60:61], 0, v[140:141]
	s_add_i32 m0, s59, 0xc000
	ds_read_b128 v[186:189], v157
	ds_read_b128 v[190:193], v157 offset:1024
	ds_read_b128 v[194:197], v157 offset:2048
	ds_read_b128 v[198:201], v157 offset:3072
	ds_read_b128 v[202:205], v157 offset:4096
	ds_read_b128 v[206:209], v157 offset:5120
	ds_read_b128 v[210:213], v157 offset:6144
	ds_read_b128 v[214:217], v157 offset:7168
	global_load_lds_dwordx4 v[218:219], off
	v_lshl_add_u64 v[218:219], s[60:61], 0, v[138:139]
	s_add_i32 m0, s59, 0xe000
	s_nop 0
	global_load_lds_dwordx4 v[218:219], off
	s_waitcnt vmcnt(8)
	s_waitcnt lgkmcnt(0)
	s_barrier
	v_mfma_f32_16x16x32_bf16 v[126:129], v[142:145], v[186:189], v[126:129]
	v_mfma_f32_16x16x32_bf16 v[122:125], v[162:165], v[186:189], v[122:125]
	v_mfma_f32_16x16x32_bf16 v[114:117], v[142:145], v[194:197], v[114:117]
	v_mfma_f32_16x16x32_bf16 v[106:109], v[162:165], v[194:197], v[106:109]
	v_mfma_f32_16x16x32_bf16 v[98:101], v[142:145], v[202:205], v[98:101]
	v_mfma_f32_16x16x32_bf16 v[90:93], v[162:165], v[202:205], v[90:93]
	v_mfma_f32_16x16x32_bf16 v[82:85], v[142:145], v[210:213], v[82:85]
	v_mfma_f32_16x16x32_bf16 v[74:77], v[162:165], v[210:213], v[74:77]
	v_mfma_f32_16x16x32_bf16 v[126:129], v[158:161], v[190:193], v[126:129]
	v_mfma_f32_16x16x32_bf16 v[122:125], v[166:169], v[190:193], v[122:125]
	v_mfma_f32_16x16x32_bf16 v[114:117], v[158:161], v[198:201], v[114:117]
	v_mfma_f32_16x16x32_bf16 v[106:109], v[166:169], v[198:201], v[106:109]
	v_mfma_f32_16x16x32_bf16 v[98:101], v[158:161], v[206:209], v[98:101]
	v_mfma_f32_16x16x32_bf16 v[90:93], v[166:169], v[206:209], v[90:93]
	v_mfma_f32_16x16x32_bf16 v[82:85], v[158:161], v[214:217], v[82:85]
	v_mfma_f32_16x16x32_bf16 v[74:77], v[166:169], v[214:217], v[74:77]
	v_mfma_f32_16x16x32_bf16 v[118:121], v[170:173], v[186:189], v[118:121]
	v_mfma_f32_16x16x32_bf16 v[110:113], v[178:181], v[186:189], v[110:113]
	v_mfma_f32_16x16x32_bf16 v[102:105], v[170:173], v[194:197], v[102:105]
	v_mfma_f32_16x16x32_bf16 v[94:97], v[178:181], v[194:197], v[94:97]
	v_mfma_f32_16x16x32_bf16 v[86:89], v[170:173], v[202:205], v[86:89]
	v_mfma_f32_16x16x32_bf16 v[78:81], v[178:181], v[202:205], v[78:81]
	v_mfma_f32_16x16x32_bf16 v[62:65], v[170:173], v[210:213], v[62:65]
	v_mfma_f32_16x16x32_bf16 v[58:61], v[178:181], v[210:213], v[58:61]
	v_mfma_f32_16x16x32_bf16 v[118:121], v[174:177], v[190:193], v[118:121]
	v_mfma_f32_16x16x32_bf16 v[110:113], v[182:185], v[190:193], v[110:113]
	v_mfma_f32_16x16x32_bf16 v[102:105], v[174:177], v[198:201], v[102:105]
	v_mfma_f32_16x16x32_bf16 v[94:97], v[182:185], v[198:201], v[94:97]
	s_barrier
	v_mfma_f32_16x16x32_bf16 v[86:89], v[174:177], v[206:209], v[86:89]
	v_mfma_f32_16x16x32_bf16 v[78:81], v[182:185], v[206:209], v[78:81]
	v_mfma_f32_16x16x32_bf16 v[62:65], v[174:177], v[214:217], v[62:65]
	v_mfma_f32_16x16x32_bf16 v[58:61], v[182:185], v[214:217], v[58:61]
	s_add_i32 s93, s79, s66
	v_lshl_add_u64 v[218:219], s[62:63], 0, v[132:133]
	s_mov_b32 m0, s93
	ds_read_b128 v[186:189], v157 offset:16384
	ds_read_b128 v[190:193], v157 offset:17408
	ds_read_b128 v[194:197], v157 offset:18432
	ds_read_b128 v[198:201], v157 offset:19456
	ds_read_b128 v[202:205], v157 offset:20480
	ds_read_b128 v[206:209], v157 offset:21504
	ds_read_b128 v[210:213], v157 offset:22528
	ds_read_b128 v[214:217], v157 offset:23552
	global_load_lds_dwordx4 v[218:219], off
	s_add_i32 m0, s93, 0x2000
	s_add_u32 s94, s62, 0x20000
	v_lshl_add_u64 v[220:221], s[62:63], 0, v[136:137]
	s_addc_u32 s95, s63, 0
	s_add_i32 s93, s80, s66
	global_load_lds_dwordx4 v[220:221], off
	v_lshl_add_u64 v[222:223], s[94:95], 0, v[132:133]
	s_mov_b32 m0, s93
	v_lshl_add_u64 v[224:225], s[64:65], 0, v[134:135]
	global_load_lds_dwordx4 v[222:223], off
	v_lshl_add_u64 v[222:223], s[94:95], 0, v[136:137]
	s_add_i32 m0, s93, 0x2000
	s_nop 0
	global_load_lds_dwordx4 v[222:223], off
	v_lshl_add_u64 v[222:223], s[64:65], 0, v[130:131]
	s_mov_b32 m0, s59
	s_nop 0
	global_load_lds_dwordx4 v[222:223], off
	s_mov_b32 m0, s67
	s_nop 0
	global_load_lds_dwordx4 v[224:225], off
	s_waitcnt vmcnt(8)
	s_waitcnt lgkmcnt(0)
	s_barrier
	v_mfma_f32_16x16x32_bf16 v[54:57], v[142:145], v[186:189], v[54:57]
	v_mfma_f32_16x16x32_bf16 v[42:45], v[162:165], v[186:189], v[42:45]
	v_mfma_f32_16x16x32_bf16 v[30:33], v[142:145], v[194:197], v[30:33]
	v_mfma_f32_16x16x32_bf16 v[26:29], v[162:165], v[194:197], v[26:29]
	v_mfma_f32_16x16x32_bf16 v[14:17], v[142:145], v[202:205], v[14:17]
	v_mfma_f32_16x16x32_bf16 v[10:13], v[162:165], v[202:205], v[10:13]
	v_mfma_f32_16x16x32_bf16 v[6:9], v[142:145], v[210:213], v[6:9]
	v_mfma_f32_16x16x32_bf16 v[2:5], v[162:165], v[210:213], v[2:5]
	v_mfma_f32_16x16x32_bf16 v[54:57], v[158:161], v[190:193], v[54:57]
	v_mfma_f32_16x16x32_bf16 v[42:45], v[166:169], v[190:193], v[42:45]
	v_mfma_f32_16x16x32_bf16 v[30:33], v[158:161], v[198:201], v[30:33]
	v_mfma_f32_16x16x32_bf16 v[26:29], v[166:169], v[198:201], v[26:29]
	v_mfma_f32_16x16x32_bf16 v[14:17], v[158:161], v[206:209], v[14:17]
	v_mfma_f32_16x16x32_bf16 v[10:13], v[166:169], v[206:209], v[10:13]
	v_mfma_f32_16x16x32_bf16 v[6:9], v[158:161], v[214:217], v[6:9]
	v_mfma_f32_16x16x32_bf16 v[2:5], v[166:169], v[214:217], v[2:5]
	v_mfma_f32_16x16x32_bf16 v[70:73], v[170:173], v[186:189], v[70:73]
	v_mfma_f32_16x16x32_bf16 v[66:69], v[178:181], v[186:189], v[66:69]
	v_mfma_f32_16x16x32_bf16 v[50:53], v[170:173], v[194:197], v[50:53]
	v_mfma_f32_16x16x32_bf16 v[46:49], v[178:181], v[194:197], v[46:49]
	v_mfma_f32_16x16x32_bf16 v[38:41], v[170:173], v[202:205], v[38:41]
	v_mfma_f32_16x16x32_bf16 v[34:37], v[178:181], v[202:205], v[34:37]
	v_mfma_f32_16x16x32_bf16 v[22:25], v[170:173], v[210:213], v[22:25]
	v_mfma_f32_16x16x32_bf16 v[18:21], v[178:181], v[210:213], v[18:21]
	v_mfma_f32_16x16x32_bf16 v[70:73], v[174:177], v[190:193], v[70:73]
	v_mfma_f32_16x16x32_bf16 v[66:69], v[182:185], v[190:193], v[66:69]
	v_mfma_f32_16x16x32_bf16 v[50:53], v[174:177], v[198:201], v[50:53]
	v_mfma_f32_16x16x32_bf16 v[46:49], v[182:185], v[198:201], v[46:49]
	s_barrier
; #define PG8_STAGE(bufoff, gbase, voff) do { _Pragma("unroll") for (int _i = 0; _i < 2; ++_i) \
;         __builtin_amdgcn_global_load_lds((const unsigned*)((const char*)(gbase) + (voff)[_i]), (PG8_LAS unsigned*)(lds + (bufoff) + ldsw + _i * 8192), 16, 0, 0); } while (0)
; #define PG8_LDA(dst, b, h) do { _Pragma("unroll") for (int m = 0; m < 4; ++m) _Pragma("unroll") for (int k = 0; k < 2; ++k) dst[m][k] = *(const PG8_LAS bf16x8*)(lds + PG8_SA(b, h) + aoff + m * 2048 + k * 1024); } while (0)
; #define PG8_LDB(dst, b, h) do { _Pragma("unroll") for (int n = 0; n < 2; ++n) _Pragma("unroll") for (int k = 0; k < 2; ++k) dst[n][k] = *(const PG8_LAS bf16x8*)(lds + PG8_SB(b, h) + boff + n * 2048 + k * 1024); } while (0)
; #define PG8_MMA(ai, bj, At, Bt) do { __builtin_amdgcn_s_setprio(1); _Pragma("unroll") for (int m = 0; m < 4; ++m) _Pragma("unroll") for (int n = 0; n < 2; ++n) _Pragma("unroll") for (int k = 0; k < 2; ++k) \
;         acc[ai][bj][m][n] = __builtin_amdgcn_mfma_f32_16x16x32_bf16(Bt[n][k], At[m][k], acc[ai][bj][m][n], 0, 0, 0); __builtin_amdgcn_s_setprio(0); } while (0)
; #define PG8_WAIT_V(n) asm volatile("s_waitcnt vmcnt(" #n ")" ::: "memory")
; #define PG8_WAIT_L(n) asm volatile("s_waitcnt lgkmcnt(" #n ")" ::: "memory")
; #define PG8_BAR __builtin_amdgcn_s_barrier()
; #define PG8_SCHED __builtin_amdgcn_sched_barrier(0)
; template <class Epi, class Sched, bool ALIGN_EPI = false>
; __device__ __forceinline__ void gemm_phase(PG8_LAS unsigned char* lds, const Gemm g, const Sched& S, const Epi& E) {
;     ...
;             PG8_WAIT_V(8); PG8_WAIT_L(0); PG8_BAR; PG8_MMA(1, 0, At, B0); PG8_MMA(1, 1, At, B1); PG8_BAR; PG8_SCHED;
;             PG8_LDB(B0, 1, 0); PG8_LDB(B1, 1, 1); PG8_SCHED; PG8_LDA(At, 1, 0); PG8_STAGE(PG8_SA(0, 1), a2 + hstepA, w1);
;             PG8_WAIT_V(8); PG8_WAIT_L(0); PG8_BAR; PG8_MMA(0, 0, At, B0); PG8_MMA(0, 1, At, B1); PG8_BAR; PG8_SCHED;
	v_mfma_f32_16x16x32_bf16 v[38:41], v[174:177], v[206:209], v[38:41]
	v_mfma_f32_16x16x32_bf16 v[34:37], v[182:185], v[206:209], v[34:37]
	v_mfma_f32_16x16x32_bf16 v[22:25], v[174:177], v[214:217], v[22:25]
	v_mfma_f32_16x16x32_bf16 v[18:21], v[182:185], v[214:217], v[18:21]
	s_add_i32 s93, 0, 0x18000
	s_add_i32 s94, 0, 0x1c000
	v_add_u32_e32 v166, s93, v147
	v_add_u32_e32 v182, s94, v147
	ds_read_b128 v[142:145], v166
	ds_read_b128 v[158:161], v166 offset:1024
	ds_read_b128 v[162:165], v166 offset:2048
	ds_read_b128 v[166:169], v166 offset:3072
	ds_read_b128 v[170:173], v182
	ds_read_b128 v[174:177], v182 offset:1024
	ds_read_b128 v[178:181], v182 offset:2048
	ds_read_b128 v[182:185], v182 offset:3072
	s_add_u32 s64, s64, 0x20000
	s_addc_u32 s65, s65, 0
	s_mov_b32 m0, s68
	v_lshl_add_u64 v[226:227], s[64:65], 0, v[130:131]
	ds_read_b128 v[186:189], v157 offset:32768
	ds_read_b128 v[190:193], v157 offset:33792
	ds_read_b128 v[194:197], v157 offset:34816
	ds_read_b128 v[198:201], v157 offset:35840
	ds_read_b128 v[202:205], v157 offset:36864
	ds_read_b128 v[206:209], v157 offset:37888
	ds_read_b128 v[210:213], v157 offset:38912
	ds_read_b128 v[214:217], v157 offset:39936
	global_load_lds_dwordx4 v[226:227], off
	v_lshl_add_u64 v[226:227], s[64:65], 0, v[134:135]
	s_mov_b32 m0, s69
	s_nop 0
	global_load_lds_dwordx4 v[226:227], off
	s_waitcnt vmcnt(8)
	s_waitcnt lgkmcnt(0)
	s_barrier
	v_mfma_f32_16x16x32_bf16 v[126:129], v[142:145], v[186:189], v[126:129]
	v_mfma_f32_16x16x32_bf16 v[122:125], v[162:165], v[186:189], v[122:125]
	v_mfma_f32_16x16x32_bf16 v[114:117], v[142:145], v[194:197], v[114:117]
	v_mfma_f32_16x16x32_bf16 v[106:109], v[162:165], v[194:197], v[106:109]
	v_mfma_f32_16x16x32_bf16 v[98:101], v[142:145], v[202:205], v[98:101]
	v_mfma_f32_16x16x32_bf16 v[90:93], v[162:165], v[202:205], v[90:93]
	v_mfma_f32_16x16x32_bf16 v[82:85], v[142:145], v[210:213], v[82:85]
	v_mfma_f32_16x16x32_bf16 v[74:77], v[162:165], v[210:213], v[74:77]
	v_mfma_f32_16x16x32_bf16 v[126:129], v[158:161], v[190:193], v[126:129]
	v_mfma_f32_16x16x32_bf16 v[122:125], v[166:169], v[190:193], v[122:125]
	v_mfma_f32_16x16x32_bf16 v[114:117], v[158:161], v[198:201], v[114:117]
	v_mfma_f32_16x16x32_bf16 v[106:109], v[166:169], v[198:201], v[106:109]
	v_mfma_f32_16x16x32_bf16 v[98:101], v[158:161], v[206:209], v[98:101]
	v_mfma_f32_16x16x32_bf16 v[90:93], v[166:169], v[206:209], v[90:93]
	v_mfma_f32_16x16x32_bf16 v[82:85], v[158:161], v[214:217], v[82:85]
	v_mfma_f32_16x16x32_bf16 v[74:77], v[166:169], v[214:217], v[74:77]
	v_mfma_f32_16x16x32_bf16 v[118:121], v[170:173], v[186:189], v[118:121]
	v_mfma_f32_16x16x32_bf16 v[110:113], v[178:181], v[186:189], v[110:113]
	v_mfma_f32_16x16x32_bf16 v[102:105], v[170:173], v[194:197], v[102:105]
	v_mfma_f32_16x16x32_bf16 v[94:97], v[178:181], v[194:197], v[94:97]
	v_mfma_f32_16x16x32_bf16 v[86:89], v[170:173], v[202:205], v[86:89]
	v_mfma_f32_16x16x32_bf16 v[78:81], v[178:181], v[202:205], v[78:81]
	v_mfma_f32_16x16x32_bf16 v[62:65], v[170:173], v[210:213], v[62:65]
	v_mfma_f32_16x16x32_bf16 v[58:61], v[178:181], v[210:213], v[58:61]
	v_mfma_f32_16x16x32_bf16 v[118:121], v[174:177], v[190:193], v[118:121]
	v_mfma_f32_16x16x32_bf16 v[110:113], v[182:185], v[190:193], v[110:113]
	v_mfma_f32_16x16x32_bf16 v[102:105], v[174:177], v[198:201], v[102:105]
	v_mfma_f32_16x16x32_bf16 v[94:97], v[182:185], v[198:201], v[94:97]
	s_barrier
; #define PG8_STAGE(bufoff, gbase, voff) do { _Pragma("unroll") for (int _i = 0; _i < 2; ++_i) \
;         __builtin_amdgcn_global_load_lds((const unsigned*)((const char*)(gbase) + (voff)[_i]), (PG8_LAS unsigned*)(lds + (bufoff) + ldsw + _i * 8192), 16, 0, 0); } while (0)
; #define PG8_LDA(dst, b, h) do { _Pragma("unroll") for (int m = 0; m < 4; ++m) _Pragma("unroll") for (int k = 0; k < 2; ++k) dst[m][k] = *(const PG8_LAS bf16x8*)(lds + PG8_SA(b, h) + aoff + m * 2048 + k * 1024); } while (0)
; #define PG8_MMA(ai, bj, At, Bt) do { __builtin_amdgcn_s_setprio(1); _Pragma("unroll") for (int m = 0; m < 4; ++m) _Pragma("unroll") for (int n = 0; n < 2; ++n) _Pragma("unroll") for (int k = 0; k < 2; ++k) \
;         acc[ai][bj][m][n] = __builtin_amdgcn_mfma_f32_16x16x32_bf16(Bt[n][k], At[m][k], acc[ai][bj][m][n], 0, 0, 0); __builtin_amdgcn_s_setprio(0); } while (0)
; #define PG8_WAIT_V(n) asm volatile("s_waitcnt vmcnt(" #n ")" ::: "memory")
; #define PG8_WAIT_L(n) asm volatile("s_waitcnt lgkmcnt(" #n ")" ::: "memory")
; #define PG8_BAR __builtin_amdgcn_s_barrier()
; #define PG8_SCHED __builtin_amdgcn_sched_barrier(0)
; template <class Epi, class Sched, bool ALIGN_EPI = false>
; __device__ __forceinline__ void gemm_phase(PG8_LAS unsigned char* lds, const Gemm g, const Sched& S, const Epi& E) {
;     ...
;             PG8_WAIT_V(8); PG8_WAIT_L(0); PG8_BAR; PG8_MMA(0, 0, At, B0); PG8_MMA(0, 1, At, B1); PG8_BAR; PG8_SCHED;
;             PG8_LDA(At, 1, 1); PG8_STAGE(PG8_SB(1, 0), b3, voffB); PG8_STAGE(PG8_SB(1, 1), b3 + hstep, voffB); PG8_STAGE(PG8_SA(1, 0), a3, w0);
;             PG8_WAIT_V(8); PG8_WAIT_L(0); PG8_BAR; PG8_MMA(1, 0, At, B0); PG8_MMA(1, 1, At, B1); PG8_BAR; PG8_SCHED;
;             if constexpr (Epi::KSCALE) { if (((t + 2) & 7) == 0 && t + 2 < nt) { E.kscale(acc, pf, ((t + 2) >> 3) - 1, wr, fr); PG8_SCHED; } }
;         }
;         if constexpr (ALIGN_EPI) { if (wr == 0) PG8_BAR; }
	v_mfma_f32_16x16x32_bf16 v[86:89], v[174:177], v[206:209], v[86:89]
	v_mfma_f32_16x16x32_bf16 v[78:81], v[182:185], v[206:209], v[78:81]
	v_mfma_f32_16x16x32_bf16 v[62:65], v[174:177], v[214:217], v[62:65]
	v_mfma_f32_16x16x32_bf16 v[58:61], v[182:185], v[214:217], v[58:61]
	s_add_i32 s64, s93, s66
	v_lshl_add_u64 v[218:219], v[218:219], 0, s[18:19]
	s_mov_b32 m0, s64
	ds_read_b128 v[186:189], v157 offset:49152
	ds_read_b128 v[190:193], v157 offset:50176
	ds_read_b128 v[194:197], v157 offset:51200
	ds_read_b128 v[198:201], v157 offset:52224
	ds_read_b128 v[202:205], v157 offset:53248
	ds_read_b128 v[206:209], v157 offset:54272
	ds_read_b128 v[210:213], v157 offset:55296
	ds_read_b128 v[214:217], v157 offset:56320
	global_load_lds_dwordx4 v[218:219], off
	s_add_i32 m0, s64, 0x2000
	s_add_u32 s62, s62, 0x20080
	v_lshl_add_u64 v[218:219], v[220:221], 0, s[18:19]
	s_addc_u32 s63, s63, 0
	s_add_i32 s64, s94, s66
	global_load_lds_dwordx4 v[218:219], off
	v_lshl_add_u64 v[218:219], s[62:63], 0, v[132:133]
	s_mov_b32 m0, s64
	s_nop 0
	global_load_lds_dwordx4 v[218:219], off
	v_lshl_add_u64 v[218:219], s[62:63], 0, v[136:137]
	s_add_i32 m0, s64, 0x2000
	s_nop 0
	global_load_lds_dwordx4 v[218:219], off
	v_lshl_add_u64 v[218:219], v[222:223], 0, s[18:19]
	s_mov_b32 m0, s73
	s_nop 0
	global_load_lds_dwordx4 v[218:219], off
	v_lshl_add_u64 v[218:219], v[224:225], 0, s[18:19]
	s_mov_b32 m0, s74
	s_nop 0
	global_load_lds_dwordx4 v[218:219], off
	s_waitcnt vmcnt(8)
	s_waitcnt lgkmcnt(0)
	s_barrier
	v_mfma_f32_16x16x32_bf16 v[54:57], v[142:145], v[186:189], v[54:57]
	v_mfma_f32_16x16x32_bf16 v[42:45], v[162:165], v[186:189], v[42:45]
	v_mfma_f32_16x16x32_bf16 v[30:33], v[142:145], v[194:197], v[30:33]
	v_mfma_f32_16x16x32_bf16 v[26:29], v[162:165], v[194:197], v[26:29]
	v_mfma_f32_16x16x32_bf16 v[14:17], v[142:145], v[202:205], v[14:17]
	v_mfma_f32_16x16x32_bf16 v[10:13], v[162:165], v[202:205], v[10:13]
	v_mfma_f32_16x16x32_bf16 v[6:9], v[142:145], v[210:213], v[6:9]
	v_mfma_f32_16x16x32_bf16 v[2:5], v[162:165], v[210:213], v[2:5]
	v_mfma_f32_16x16x32_bf16 v[54:57], v[158:161], v[190:193], v[54:57]
	v_mfma_f32_16x16x32_bf16 v[42:45], v[166:169], v[190:193], v[42:45]
	v_mfma_f32_16x16x32_bf16 v[30:33], v[158:161], v[198:201], v[30:33]
	v_mfma_f32_16x16x32_bf16 v[26:29], v[166:169], v[198:201], v[26:29]
	v_mfma_f32_16x16x32_bf16 v[14:17], v[158:161], v[206:209], v[14:17]
	v_mfma_f32_16x16x32_bf16 v[10:13], v[166:169], v[206:209], v[10:13]
	v_mfma_f32_16x16x32_bf16 v[6:9], v[158:161], v[214:217], v[6:9]
	v_mfma_f32_16x16x32_bf16 v[2:5], v[166:169], v[214:217], v[2:5]
	v_mfma_f32_16x16x32_bf16 v[70:73], v[170:173], v[186:189], v[70:73]
	v_mfma_f32_16x16x32_bf16 v[66:69], v[178:181], v[186:189], v[66:69]
	v_mfma_f32_16x16x32_bf16 v[50:53], v[170:173], v[194:197], v[50:53]
	v_mfma_f32_16x16x32_bf16 v[46:49], v[178:181], v[194:197], v[46:49]
	v_mfma_f32_16x16x32_bf16 v[38:41], v[170:173], v[202:205], v[38:41]
	v_mfma_f32_16x16x32_bf16 v[34:37], v[178:181], v[202:205], v[34:37]
	v_mfma_f32_16x16x32_bf16 v[22:25], v[170:173], v[210:213], v[22:25]
	v_mfma_f32_16x16x32_bf16 v[18:21], v[178:181], v[210:213], v[18:21]
	v_mfma_f32_16x16x32_bf16 v[70:73], v[174:177], v[190:193], v[70:73]
	v_mfma_f32_16x16x32_bf16 v[66:69], v[182:185], v[190:193], v[66:69]
	v_mfma_f32_16x16x32_bf16 v[50:53], v[174:177], v[198:201], v[50:53]
	v_mfma_f32_16x16x32_bf16 v[46:49], v[182:185], v[198:201], v[46:49]
	s_barrier
	v_mfma_f32_16x16x32_bf16 v[38:41], v[174:177], v[206:209], v[38:41]
	v_mfma_f32_16x16x32_bf16 v[34:37], v[182:185], v[206:209], v[34:37]
	v_mfma_f32_16x16x32_bf16 v[22:25], v[174:177], v[214:217], v[22:25]
	v_mfma_f32_16x16x32_bf16 v[18:21], v[182:185], v[214:217], v[18:21]
	s_add_i32 s92, s92, 2
	s_add_u32 s90, s90, 0x100
	s_addc_u32 s91, s91, 0
	s_add_u32 s60, s60, 0x100
	s_addc_u32 s61, s61, 0
	s_cmp_gt_u32 s92, 5
	s_cbranch_scc0 .LBB0_805
	s_and_b64 vcc, exec, s[22:23]
	s_cbranch_vccz .LBB0_808
	s_barrier

; #define PG8_STAGE(bufoff, gbase, voff) do { _Pragma("unroll") for (int _i = 0; _i < 2; ++_i) \
;         __builtin_amdgcn_global_load_lds((const unsigned*)((const char*)(gbase) + (voff)[_i]), (PG8_LAS unsigned*)(lds + (bufoff) + ldsw + _i * 8192), 16, 0, 0); } while (0)
; #define PG8_LDA(dst, b, h) do { _Pragma("unroll") for (int m = 0; m < 4; ++m) _Pragma("unroll") for (int k = 0; k < 2; ++k) dst[m][k] = *(const PG8_LAS bf16x8*)(lds + PG8_SA(b, h) + aoff + m * 2048 + k * 1024); } while (0)
; #define PG8_LDB(dst, b, h) do { _Pragma("unroll") for (int n = 0; n < 2; ++n) _Pragma("unroll") for (int k = 0; k < 2; ++k) dst[n][k] = *(const PG8_LAS bf16x8*)(lds + PG8_SB(b, h) + boff + n * 2048 + k * 1024); } while (0)
; #define PG8_MMA(ai, bj, At, Bt) do { __builtin_amdgcn_s_setprio(1); _Pragma("unroll") for (int m = 0; m < 4; ++m) _Pragma("unroll") for (int n = 0; n < 2; ++n) _Pragma("unroll") for (int k = 0; k < 2; ++k) \
;         acc[ai][bj][m][n] = __builtin_amdgcn_mfma_f32_16x16x32_bf16(Bt[n][k], At[m][k], acc[ai][bj][m][n], 0, 0, 0); __builtin_amdgcn_s_setprio(0); } while (0)
; template <class Epi, class Sched, bool ALIGN_EPI = false>
; __device__ __forceinline__ void gemm_phase(PG8_LAS unsigned char* lds, const Gemm g, const Sched& S, const Epi& E) {
;     ...
;         for (int t = 0; t < nt; t += 2) {
;             const bool last = (t == nt - 2);
;             const char* a1 = cA + (size_t)(t + 1) * kstep;
;             const char* a2 = last ? nA : cA + (size_t)(t + 2) * kstep; const char* b2 = last ? nB : cB + (size_t)(t + 2) * kstep;
;             const char* a3 = a2 + kstep; const char* b3 = b2 + kstep;
;             unsigned w0[2], w1[2];
; #pragma unroll
;             for (int i = 0; i < 2; ++i) { w0[i] = (Sched::GATHER && last) ? vn0[i] : vc0[i]; w1[i] = (Sched::GATHER && last) ? vn1[i] : vc1[i]; }
;             if (last && has_next) S.a_ready(nxt);
;             PG8_LDB(B0, 0, 0); PG8_LDB(B1, 0, 1); PG8_SCHED; PG8_LDA(At, 0, 0); PG8_STAGE(PG8_SA(1, 1), a1 + hstepA, vc1);
;             PG8_WAIT_V(8); PG8_WAIT_L(0); PG8_BAR; PG8_MMA(0, 0, At, B0); PG8_MMA(0, 1, At, B1); PG8_BAR; PG8_SCHED;
;             PG8_LDA(At, 0, 1); PG8_STAGE(PG8_SB(0, 0), b2, voffB); PG8_STAGE(PG8_SB(0, 1), b2 + hstep, voffB); PG8_STAGE(PG8_SA(0, 0), a2, w0);
;             PG8_WAIT_V(8); PG8_WAIT_L(0); PG8_BAR; PG8_MMA(1, 0, At, B0); PG8_MMA(1, 1, At, B1); PG8_BAR; PG8_SCHED;
.LBB0_908:
	ds_read_b128 v[144:147], v157
	ds_read_b128 v[160:163], v157 offset:1024
	ds_read_b128 v[164:167], v157 offset:2048
	ds_read_b128 v[168:171], v157 offset:3072
	ds_read_b128 v[172:175], v158
	ds_read_b128 v[176:179], v158 offset:1024
	ds_read_b128 v[180:183], v158 offset:2048
	ds_read_b128 v[184:187], v158 offset:3072
	s_add_u32 s58, s56, 0xfffe0080
	s_addc_u32 s59, s57, -1
	s_cmp_eq_u32 s92, 4
	s_cselect_b32 s61, s41, s59
	s_cselect_b32 s60, s47, s58
	s_cselect_b32 s59, s43, s91
	s_cselect_b32 s58, s89, s90
	v_lshl_add_u64 v[220:221], s[56:57], 0, v[142:143]
	s_add_i32 m0, s49, 0xc000
	ds_read_b128 v[188:191], v159
	ds_read_b128 v[192:195], v159 offset:1024
	ds_read_b128 v[196:199], v159 offset:2048
	ds_read_b128 v[200:203], v159 offset:3072
	ds_read_b128 v[204:207], v159 offset:4096
	ds_read_b128 v[208:211], v159 offset:5120
	ds_read_b128 v[212:215], v159 offset:6144
	ds_read_b128 v[216:219], v159 offset:7168
	global_load_lds_dwordx4 v[220:221], off
	v_lshl_add_u64 v[220:221], s[56:57], 0, v[140:141]
	s_add_i32 m0, s49, 0xe000
	s_nop 0
	global_load_lds_dwordx4 v[220:221], off
	s_waitcnt vmcnt(8)
	s_waitcnt lgkmcnt(0)
	s_barrier
	v_mfma_f32_16x16x32_bf16 v[126:129], v[144:147], v[188:191], v[126:129]
	v_mfma_f32_16x16x32_bf16 v[122:125], v[164:167], v[188:191], v[122:125]
	v_mfma_f32_16x16x32_bf16 v[114:117], v[144:147], v[196:199], v[114:117]
	v_mfma_f32_16x16x32_bf16 v[106:109], v[164:167], v[196:199], v[106:109]
	v_mfma_f32_16x16x32_bf16 v[98:101], v[144:147], v[204:207], v[98:101]
	v_mfma_f32_16x16x32_bf16 v[90:93], v[164:167], v[204:207], v[90:93]
	v_mfma_f32_16x16x32_bf16 v[82:85], v[144:147], v[212:215], v[82:85]
	v_mfma_f32_16x16x32_bf16 v[74:77], v[164:167], v[212:215], v[74:77]
	v_mfma_f32_16x16x32_bf16 v[126:129], v[160:163], v[192:195], v[126:129]
	v_mfma_f32_16x16x32_bf16 v[122:125], v[168:171], v[192:195], v[122:125]
	v_mfma_f32_16x16x32_bf16 v[114:117], v[160:163], v[200:203], v[114:117]
	v_mfma_f32_16x16x32_bf16 v[106:109], v[168:171], v[200:203], v[106:109]
	v_mfma_f32_16x16x32_bf16 v[98:101], v[160:163], v[208:211], v[98:101]
	v_mfma_f32_16x16x32_bf16 v[90:93], v[168:171], v[208:211], v[90:93]
	v_mfma_f32_16x16x32_bf16 v[82:85], v[160:163], v[216:219], v[82:85]
	v_mfma_f32_16x16x32_bf16 v[74:77], v[168:171], v[216:219], v[74:77]
	v_mfma_f32_16x16x32_bf16 v[118:121], v[172:175], v[188:191], v[118:121]
	v_mfma_f32_16x16x32_bf16 v[110:113], v[180:183], v[188:191], v[110:113]
	v_mfma_f32_16x16x32_bf16 v[102:105], v[172:175], v[196:199], v[102:105]
	v_mfma_f32_16x16x32_bf16 v[94:97], v[180:183], v[196:199], v[94:97]
	v_mfma_f32_16x16x32_bf16 v[86:89], v[172:175], v[204:207], v[86:89]
	v_mfma_f32_16x16x32_bf16 v[78:81], v[180:183], v[204:207], v[78:81]
	v_mfma_f32_16x16x32_bf16 v[62:65], v[172:175], v[212:215], v[62:65]
	v_mfma_f32_16x16x32_bf16 v[58:61], v[180:183], v[212:215], v[58:61]
	v_mfma_f32_16x16x32_bf16 v[118:121], v[176:179], v[192:195], v[118:121]
	v_mfma_f32_16x16x32_bf16 v[110:113], v[184:187], v[192:195], v[110:113]
	v_mfma_f32_16x16x32_bf16 v[102:105], v[176:179], v[200:203], v[102:105]
	v_mfma_f32_16x16x32_bf16 v[94:97], v[184:187], v[200:203], v[94:97]
	s_barrier
	v_mfma_f32_16x16x32_bf16 v[86:89], v[176:179], v[208:211], v[86:89]
	v_mfma_f32_16x16x32_bf16 v[78:81], v[184:187], v[208:211], v[78:81]
	v_mfma_f32_16x16x32_bf16 v[62:65], v[176:179], v[216:219], v[62:65]
	v_mfma_f32_16x16x32_bf16 v[58:61], v[184:187], v[216:219], v[58:61]
	s_add_i32 s93, s79, s66
	v_lshl_add_u64 v[220:221], s[58:59], 0, v[134:135]
	s_mov_b32 m0, s93
	ds_read_b128 v[188:191], v159 offset:16384
	ds_read_b128 v[192:195], v159 offset:17408
	ds_read_b128 v[196:199], v159 offset:18432
	ds_read_b128 v[200:203], v159 offset:19456
	ds_read_b128 v[204:207], v159 offset:20480
	ds_read_b128 v[208:211], v159 offset:21504
	ds_read_b128 v[212:215], v159 offset:22528
	ds_read_b128 v[216:219], v159 offset:23552
	global_load_lds_dwordx4 v[220:221], off
	s_add_i32 m0, s93, 0x2000
	s_add_u32 s94, s58, 0x20000
	v_lshl_add_u64 v[222:223], s[58:59], 0, v[138:139]
	s_addc_u32 s95, s59, 0
	s_add_i32 s93, s80, s66
	global_load_lds_dwordx4 v[222:223], off
	v_lshl_add_u64 v[224:225], s[94:95], 0, v[134:135]
	s_mov_b32 m0, s93
	v_lshl_add_u64 v[226:227], s[60:61], 0, v[136:137]
	global_load_lds_dwordx4 v[224:225], off
	v_lshl_add_u64 v[224:225], s[94:95], 0, v[138:139]
	s_add_i32 m0, s93, 0x2000
	s_nop 0
	global_load_lds_dwordx4 v[224:225], off
	v_lshl_add_u64 v[224:225], s[60:61], 0, v[132:133]
	s_mov_b32 m0, s49
	s_nop 0
	global_load_lds_dwordx4 v[224:225], off
	s_mov_b32 m0, s67
	s_nop 0
	global_load_lds_dwordx4 v[226:227], off
	s_waitcnt vmcnt(8)
	s_waitcnt lgkmcnt(0)
	s_barrier
	v_mfma_f32_16x16x32_bf16 v[54:57], v[144:147], v[188:191], v[54:57]
	v_mfma_f32_16x16x32_bf16 v[42:45], v[164:167], v[188:191], v[42:45]
	v_mfma_f32_16x16x32_bf16 v[30:33], v[144:147], v[196:199], v[30:33]
	v_mfma_f32_16x16x32_bf16 v[26:29], v[164:167], v[196:199], v[26:29]
	v_mfma_f32_16x16x32_bf16 v[14:17], v[144:147], v[204:207], v[14:17]
	v_mfma_f32_16x16x32_bf16 v[10:13], v[164:167], v[204:207], v[10:13]
	v_mfma_f32_16x16x32_bf16 v[6:9], v[144:147], v[212:215], v[6:9]
	v_mfma_f32_16x16x32_bf16 v[2:5], v[164:167], v[212:215], v[2:5]
	v_mfma_f32_16x16x32_bf16 v[54:57], v[160:163], v[192:195], v[54:57]
	v_mfma_f32_16x16x32_bf16 v[42:45], v[168:171], v[192:195], v[42:45]
	v_mfma_f32_16x16x32_bf16 v[30:33], v[160:163], v[200:203], v[30:33]
	v_mfma_f32_16x16x32_bf16 v[26:29], v[168:171], v[200:203], v[26:29]
	v_mfma_f32_16x16x32_bf16 v[14:17], v[160:163], v[208:211], v[14:17]
	v_mfma_f32_16x16x32_bf16 v[10:13], v[168:171], v[208:211], v[10:13]
	v_mfma_f32_16x16x32_bf16 v[6:9], v[160:163], v[216:219], v[6:9]
	v_mfma_f32_16x16x32_bf16 v[2:5], v[168:171], v[216:219], v[2:5]
	v_mfma_f32_16x16x32_bf16 v[70:73], v[172:175], v[188:191], v[70:73]
	v_mfma_f32_16x16x32_bf16 v[66:69], v[180:183], v[188:191], v[66:69]
	v_mfma_f32_16x16x32_bf16 v[50:53], v[172:175], v[196:199], v[50:53]
	v_mfma_f32_16x16x32_bf16 v[46:49], v[180:183], v[196:199], v[46:49]
	v_mfma_f32_16x16x32_bf16 v[38:41], v[172:175], v[204:207], v[38:41]
	v_mfma_f32_16x16x32_bf16 v[34:37], v[180:183], v[204:207], v[34:37]
	v_mfma_f32_16x16x32_bf16 v[22:25], v[172:175], v[212:215], v[22:25]
	v_mfma_f32_16x16x32_bf16 v[18:21], v[180:183], v[212:215], v[18:21]
	v_mfma_f32_16x16x32_bf16 v[70:73], v[176:179], v[192:195], v[70:73]
	v_mfma_f32_16x16x32_bf16 v[66:69], v[184:187], v[192:195], v[66:69]
	v_mfma_f32_16x16x32_bf16 v[50:53], v[176:179], v[200:203], v[50:53]
	v_mfma_f32_16x16x32_bf16 v[46:49], v[184:187], v[200:203], v[46:49]
	s_barrier
; #define PG8_STAGE(bufoff, gbase, voff) do { _Pragma("unroll") for (int _i = 0; _i < 2; ++_i) \
;         __builtin_amdgcn_global_load_lds((const unsigned*)((const char*)(gbase) + (voff)[_i]), (PG8_LAS unsigned*)(lds + (bufoff) + ldsw + _i * 8192), 16, 0, 0); } while (0)
; #define PG8_LDA(dst, b, h) do { _Pragma("unroll") for (int m = 0; m < 4; ++m) _Pragma("unroll") for (int k = 0; k < 2; ++k) dst[m][k] = *(const PG8_LAS bf16x8*)(lds + PG8_SA(b, h) + aoff + m * 2048 + k * 1024); } while (0)
; #define PG8_LDB(dst, b, h) do { _Pragma("unroll") for (int n = 0; n < 2; ++n) _Pragma("unroll") for (int k = 0; k < 2; ++k) dst[n][k] = *(const PG8_LAS bf16x8*)(lds + PG8_SB(b, h) + boff + n * 2048 + k * 1024); } while (0)
; #define PG8_MMA(ai, bj, At, Bt) do { __builtin_amdgcn_s_setprio(1); _Pragma("unroll") for (int m = 0; m < 4; ++m) _Pragma("unroll") for (int n = 0; n < 2; ++n) _Pragma("unroll") for (int k = 0; k < 2; ++k) \
;         acc[ai][bj][m][n] = __builtin_amdgcn_mfma_f32_16x16x32_bf16(Bt[n][k], At[m][k], acc[ai][bj][m][n], 0, 0, 0); __builtin_amdgcn_s_setprio(0); } while (0)
; #define PG8_WAIT_V(n) asm volatile("s_waitcnt vmcnt(" #n ")" ::: "memory")
; #define PG8_WAIT_L(n) asm volatile("s_waitcnt lgkmcnt(" #n ")" ::: "memory")
; #define PG8_BAR __builtin_amdgcn_s_barrier()
; #define PG8_SCHED __builtin_amdgcn_sched_barrier(0)
; template <class Epi, class Sched, bool ALIGN_EPI = false>
; __device__ __forceinline__ void gemm_phase(PG8_LAS unsigned char* lds, const Gemm g, const Sched& S, const Epi& E) {
;     ...
;             PG8_WAIT_V(8); PG8_WAIT_L(0); PG8_BAR; PG8_MMA(1, 0, At, B0); PG8_MMA(1, 1, At, B1); PG8_BAR; PG8_SCHED;
;             PG8_LDB(B0, 1, 0); PG8_LDB(B1, 1, 1); PG8_SCHED; PG8_LDA(At, 1, 0); PG8_STAGE(PG8_SA(0, 1), a2 + hstepA, w1);
;             PG8_WAIT_V(8); PG8_WAIT_L(0); PG8_BAR; PG8_MMA(0, 0, At, B0); PG8_MMA(0, 1, At, B1); PG8_BAR; PG8_SCHED;
	v_mfma_f32_16x16x32_bf16 v[38:41], v[176:179], v[208:211], v[38:41]
	v_mfma_f32_16x16x32_bf16 v[34:37], v[184:187], v[208:211], v[34:37]
	v_mfma_f32_16x16x32_bf16 v[22:25], v[176:179], v[216:219], v[22:25]
	v_mfma_f32_16x16x32_bf16 v[18:21], v[184:187], v[216:219], v[18:21]
	s_add_i32 s93, 0, 0x18000
	s_add_i32 s94, 0, 0x1c000
	v_add_u32_e32 v168, s93, v148
	v_add_u32_e32 v184, s94, v148
	ds_read_b128 v[144:147], v168
	ds_read_b128 v[160:163], v168 offset:1024
	ds_read_b128 v[164:167], v168 offset:2048
	ds_read_b128 v[168:171], v168 offset:3072
	ds_read_b128 v[172:175], v184
	ds_read_b128 v[176:179], v184 offset:1024
	ds_read_b128 v[180:183], v184 offset:2048
	ds_read_b128 v[184:187], v184 offset:3072
	s_add_u32 s60, s60, 0x20000
	s_addc_u32 s61, s61, 0
	s_mov_b32 m0, s68
	v_lshl_add_u64 v[228:229], s[60:61], 0, v[132:133]
	ds_read_b128 v[188:191], v159 offset:32768
	ds_read_b128 v[192:195], v159 offset:33792
	ds_read_b128 v[196:199], v159 offset:34816
	ds_read_b128 v[200:203], v159 offset:35840
	ds_read_b128 v[204:207], v159 offset:36864
	ds_read_b128 v[208:211], v159 offset:37888
	ds_read_b128 v[212:215], v159 offset:38912
	ds_read_b128 v[216:219], v159 offset:39936
	global_load_lds_dwordx4 v[228:229], off
	v_lshl_add_u64 v[228:229], s[60:61], 0, v[136:137]
	s_mov_b32 m0, s69
	s_nop 0
	global_load_lds_dwordx4 v[228:229], off
	s_waitcnt vmcnt(8)
	s_waitcnt lgkmcnt(0)
	s_barrier
	v_mfma_f32_16x16x32_bf16 v[126:129], v[144:147], v[188:191], v[126:129]
	v_mfma_f32_16x16x32_bf16 v[122:125], v[164:167], v[188:191], v[122:125]
	v_mfma_f32_16x16x32_bf16 v[114:117], v[144:147], v[196:199], v[114:117]
	v_mfma_f32_16x16x32_bf16 v[106:109], v[164:167], v[196:199], v[106:109]
	v_mfma_f32_16x16x32_bf16 v[98:101], v[144:147], v[204:207], v[98:101]
	v_mfma_f32_16x16x32_bf16 v[90:93], v[164:167], v[204:207], v[90:93]
	v_mfma_f32_16x16x32_bf16 v[82:85], v[144:147], v[212:215], v[82:85]
	v_mfma_f32_16x16x32_bf16 v[74:77], v[164:167], v[212:215], v[74:77]
	v_mfma_f32_16x16x32_bf16 v[126:129], v[160:163], v[192:195], v[126:129]
	v_mfma_f32_16x16x32_bf16 v[122:125], v[168:171], v[192:195], v[122:125]
	v_mfma_f32_16x16x32_bf16 v[114:117], v[160:163], v[200:203], v[114:117]
	v_mfma_f32_16x16x32_bf16 v[106:109], v[168:171], v[200:203], v[106:109]
	v_mfma_f32_16x16x32_bf16 v[98:101], v[160:163], v[208:211], v[98:101]
	v_mfma_f32_16x16x32_bf16 v[90:93], v[168:171], v[208:211], v[90:93]
	v_mfma_f32_16x16x32_bf16 v[82:85], v[160:163], v[216:219], v[82:85]
	v_mfma_f32_16x16x32_bf16 v[74:77], v[168:171], v[216:219], v[74:77]
	v_mfma_f32_16x16x32_bf16 v[118:121], v[172:175], v[188:191], v[118:121]
	v_mfma_f32_16x16x32_bf16 v[110:113], v[180:183], v[188:191], v[110:113]
	v_mfma_f32_16x16x32_bf16 v[102:105], v[172:175], v[196:199], v[102:105]
	v_mfma_f32_16x16x32_bf16 v[94:97], v[180:183], v[196:199], v[94:97]
	v_mfma_f32_16x16x32_bf16 v[86:89], v[172:175], v[204:207], v[86:89]
	v_mfma_f32_16x16x32_bf16 v[78:81], v[180:183], v[204:207], v[78:81]
	v_mfma_f32_16x16x32_bf16 v[62:65], v[172:175], v[212:215], v[62:65]
	v_mfma_f32_16x16x32_bf16 v[58:61], v[180:183], v[212:215], v[58:61]
	v_mfma_f32_16x16x32_bf16 v[118:121], v[176:179], v[192:195], v[118:121]
	v_mfma_f32_16x16x32_bf16 v[110:113], v[184:187], v[192:195], v[110:113]
	v_mfma_f32_16x16x32_bf16 v[102:105], v[176:179], v[200:203], v[102:105]
	v_mfma_f32_16x16x32_bf16 v[94:97], v[184:187], v[200:203], v[94:97]
	s_barrier
; #define PG8_STAGE(bufoff, gbase, voff) do { _Pragma("unroll") for (int _i = 0; _i < 2; ++_i) \
;         __builtin_amdgcn_global_load_lds((const unsigned*)((const char*)(gbase) + (voff)[_i]), (PG8_LAS unsigned*)(lds + (bufoff) + ldsw + _i * 8192), 16, 0, 0); } while (0)
; #define PG8_LDA(dst, b, h) do { _Pragma("unroll") for (int m = 0; m < 4; ++m) _Pragma("unroll") for (int k = 0; k < 2; ++k) dst[m][k] = *(const PG8_LAS bf16x8*)(lds + PG8_SA(b, h) + aoff + m * 2048 + k * 1024); } while (0)
; #define PG8_MMA(ai, bj, At, Bt) do { __builtin_amdgcn_s_setprio(1); _Pragma("unroll") for (int m = 0; m < 4; ++m) _Pragma("unroll") for (int n = 0; n < 2; ++n) _Pragma("unroll") for (int k = 0; k < 2; ++k) \
;         acc[ai][bj][m][n] = __builtin_amdgcn_mfma_f32_16x16x32_bf16(Bt[n][k], At[m][k], acc[ai][bj][m][n], 0, 0, 0); __builtin_amdgcn_s_setprio(0); } while (0)
; #define PG8_WAIT_V(n) asm volatile("s_waitcnt vmcnt(" #n ")" ::: "memory")
; #define PG8_WAIT_L(n) asm volatile("s_waitcnt lgkmcnt(" #n ")" ::: "memory")
; #define PG8_BAR __builtin_amdgcn_s_barrier()
; #define PG8_SCHED __builtin_amdgcn_sched_barrier(0)
; template <class Epi, class Sched, bool ALIGN_EPI = false>
; __device__ __forceinline__ void gemm_phase(PG8_LAS unsigned char* lds, const Gemm g, const Sched& S, const Epi& E) {
;     ...
;             PG8_WAIT_V(8); PG8_WAIT_L(0); PG8_BAR; PG8_MMA(0, 0, At, B0); PG8_MMA(0, 1, At, B1); PG8_BAR; PG8_SCHED;
;             PG8_LDA(At, 1, 1); PG8_STAGE(PG8_SB(1, 0), b3, voffB); PG8_STAGE(PG8_SB(1, 1), b3 + hstep, voffB); PG8_STAGE(PG8_SA(1, 0), a3, w0);
;             PG8_WAIT_V(8); PG8_WAIT_L(0); PG8_BAR; PG8_MMA(1, 0, At, B0); PG8_MMA(1, 1, At, B1); PG8_BAR; PG8_SCHED;
;             if constexpr (Epi::KSCALE) { if (((t + 2) & 7) == 0 && t + 2 < nt) { E.kscale(acc, pf, ((t + 2) >> 3) - 1, wr, fr); PG8_SCHED; } }
;         }
;         if constexpr (ALIGN_EPI) { if (wr == 0) PG8_BAR; }
	v_mfma_f32_16x16x32_bf16 v[86:89], v[176:179], v[208:211], v[86:89]
	v_mfma_f32_16x16x32_bf16 v[78:81], v[184:187], v[208:211], v[78:81]
	v_mfma_f32_16x16x32_bf16 v[62:65], v[176:179], v[216:219], v[62:65]
	v_mfma_f32_16x16x32_bf16 v[58:61], v[184:187], v[216:219], v[58:61]
	s_add_i32 s60, s93, s66
	v_lshl_add_u64 v[220:221], v[220:221], 0, s[14:15]
	s_mov_b32 m0, s60
	ds_read_b128 v[188:191], v159 offset:49152
	ds_read_b128 v[192:195], v159 offset:50176
	ds_read_b128 v[196:199], v159 offset:51200
	ds_read_b128 v[200:203], v159 offset:52224
	ds_read_b128 v[204:207], v159 offset:53248
	ds_read_b128 v[208:211], v159 offset:54272
	ds_read_b128 v[212:215], v159 offset:55296
	ds_read_b128 v[216:219], v159 offset:56320
	global_load_lds_dwordx4 v[220:221], off
	s_add_i32 m0, s60, 0x2000
	s_add_u32 s58, s58, 0x20080
	v_lshl_add_u64 v[220:221], v[222:223], 0, s[14:15]
	s_addc_u32 s59, s59, 0
	s_add_i32 s60, s94, s66
	global_load_lds_dwordx4 v[220:221], off
	v_lshl_add_u64 v[220:221], s[58:59], 0, v[134:135]
	s_mov_b32 m0, s60
	s_nop 0
	global_load_lds_dwordx4 v[220:221], off
	v_lshl_add_u64 v[220:221], s[58:59], 0, v[138:139]
	s_add_i32 m0, s60, 0x2000
	s_nop 0
	global_load_lds_dwordx4 v[220:221], off
	v_lshl_add_u64 v[220:221], v[224:225], 0, s[14:15]
	s_mov_b32 m0, s74
	s_nop 0
	global_load_lds_dwordx4 v[220:221], off
	v_lshl_add_u64 v[220:221], v[226:227], 0, s[14:15]
	s_mov_b32 m0, s75
	s_nop 0
	global_load_lds_dwordx4 v[220:221], off
	s_waitcnt vmcnt(8)
	s_waitcnt lgkmcnt(0)
	s_barrier
	v_mfma_f32_16x16x32_bf16 v[54:57], v[144:147], v[188:191], v[54:57]
	v_mfma_f32_16x16x32_bf16 v[42:45], v[164:167], v[188:191], v[42:45]
	v_mfma_f32_16x16x32_bf16 v[30:33], v[144:147], v[196:199], v[30:33]
	v_mfma_f32_16x16x32_bf16 v[26:29], v[164:167], v[196:199], v[26:29]
	v_mfma_f32_16x16x32_bf16 v[14:17], v[144:147], v[204:207], v[14:17]
	v_mfma_f32_16x16x32_bf16 v[10:13], v[164:167], v[204:207], v[10:13]
	v_mfma_f32_16x16x32_bf16 v[6:9], v[144:147], v[212:215], v[6:9]
	v_mfma_f32_16x16x32_bf16 v[2:5], v[164:167], v[212:215], v[2:5]
	v_mfma_f32_16x16x32_bf16 v[54:57], v[160:163], v[192:195], v[54:57]
	v_mfma_f32_16x16x32_bf16 v[42:45], v[168:171], v[192:195], v[42:45]
	v_mfma_f32_16x16x32_bf16 v[30:33], v[160:163], v[200:203], v[30:33]
	v_mfma_f32_16x16x32_bf16 v[26:29], v[168:171], v[200:203], v[26:29]
	v_mfma_f32_16x16x32_bf16 v[14:17], v[160:163], v[208:211], v[14:17]
	v_mfma_f32_16x16x32_bf16 v[10:13], v[168:171], v[208:211], v[10:13]
	v_mfma_f32_16x16x32_bf16 v[6:9], v[160:163], v[216:219], v[6:9]
	v_mfma_f32_16x16x32_bf16 v[2:5], v[168:171], v[216:219], v[2:5]
	v_mfma_f32_16x16x32_bf16 v[70:73], v[172:175], v[188:191], v[70:73]
	v_mfma_f32_16x16x32_bf16 v[66:69], v[180:183], v[188:191], v[66:69]
	v_mfma_f32_16x16x32_bf16 v[50:53], v[172:175], v[196:199], v[50:53]
	v_mfma_f32_16x16x32_bf16 v[46:49], v[180:183], v[196:199], v[46:49]
	v_mfma_f32_16x16x32_bf16 v[38:41], v[172:175], v[204:207], v[38:41]
	v_mfma_f32_16x16x32_bf16 v[34:37], v[180:183], v[204:207], v[34:37]
	v_mfma_f32_16x16x32_bf16 v[22:25], v[172:175], v[212:215], v[22:25]
	v_mfma_f32_16x16x32_bf16 v[18:21], v[180:183], v[212:215], v[18:21]
	v_mfma_f32_16x16x32_bf16 v[70:73], v[176:179], v[192:195], v[70:73]
	v_mfma_f32_16x16x32_bf16 v[66:69], v[184:187], v[192:195], v[66:69]
	v_mfma_f32_16x16x32_bf16 v[50:53], v[176:179], v[200:203], v[50:53]
	v_mfma_f32_16x16x32_bf16 v[46:49], v[184:187], v[200:203], v[46:49]
	s_barrier
	v_mfma_f32_16x16x32_bf16 v[38:41], v[176:179], v[208:211], v[38:41]
	v_mfma_f32_16x16x32_bf16 v[34:37], v[184:187], v[208:211], v[34:37]
	v_mfma_f32_16x16x32_bf16 v[22:25], v[176:179], v[216:219], v[22:25]
	v_mfma_f32_16x16x32_bf16 v[18:21], v[184:187], v[216:219], v[18:21]
	s_add_i32 s92, s92, 2
	s_add_u32 s90, s90, 0x100
	s_addc_u32 s91, s91, 0
	s_add_u32 s56, s56, 0x100
	s_addc_u32 s57, s57, 0
	s_cmp_gt_u32 s92, 5
	s_cbranch_scc0 .LBB0_908
	s_and_b64 vcc, exec, s[16:17]
	s_cbranch_vccz .LBB0_911
	s_barrier

; #define PG8_STAGE(bufoff, gbase, voff) do { _Pragma("unroll") for (int _i = 0; _i < 2; ++_i) \
;         __builtin_amdgcn_global_load_lds((const unsigned*)((const char*)(gbase) + (voff)[_i]), (PG8_LAS unsigned*)(lds + (bufoff) + ldsw + _i * 8192), 16, 0, 0); } while (0)
; #define PG8_LDA(dst, b, h) do { _Pragma("unroll") for (int m = 0; m < 4; ++m) _Pragma("unroll") for (int k = 0; k < 2; ++k) dst[m][k] = *(const PG8_LAS bf16x8*)(lds + PG8_SA(b, h) + aoff + m * 2048 + k * 1024); } while (0)
; #define PG8_LDB(dst, b, h) do { _Pragma("unroll") for (int n = 0; n < 2; ++n) _Pragma("unroll") for (int k = 0; k < 2; ++k) dst[n][k] = *(const PG8_LAS bf16x8*)(lds + PG8_SB(b, h) + boff + n * 2048 + k * 1024); } while (0)
; #define PG8_MMA(ai, bj, At, Bt) do { __builtin_amdgcn_s_setprio(1); _Pragma("unroll") for (int m = 0; m < 4; ++m) _Pragma("unroll") for (int n = 0; n < 2; ++n) _Pragma("unroll") for (int k = 0; k < 2; ++k) \
;         acc[ai][bj][m][n] = __builtin_amdgcn_mfma_f32_16x16x32_bf16(Bt[n][k], At[m][k], acc[ai][bj][m][n], 0, 0, 0); __builtin_amdgcn_s_setprio(0); } while (0)
; template <class Epi, class Sched, bool ALIGN_EPI = false>
; __device__ __forceinline__ void gemm_phase(PG8_LAS unsigned char* lds, const Gemm g, const Sched& S, const Epi& E) {
;     ...
;         for (int t = 0; t < nt; t += 2) {
;             const bool last = (t == nt - 2);
;             const char* a1 = cA + (size_t)(t + 1) * kstep;
;             const char* a2 = last ? nA : cA + (size_t)(t + 2) * kstep; const char* b2 = last ? nB : cB + (size_t)(t + 2) * kstep;
;             const char* a3 = a2 + kstep; const char* b3 = b2 + kstep;
;             unsigned w0[2], w1[2];
; #pragma unroll
;             for (int i = 0; i < 2; ++i) { w0[i] = (Sched::GATHER && last) ? vn0[i] : vc0[i]; w1[i] = (Sched::GATHER && last) ? vn1[i] : vc1[i]; }
;             if (last && has_next) S.a_ready(nxt);
;             PG8_LDB(B0, 0, 0); PG8_LDB(B1, 0, 1); PG8_SCHED; PG8_LDA(At, 0, 0); PG8_STAGE(PG8_SA(1, 1), a1 + hstepA, vc1);
;             PG8_WAIT_V(8); PG8_WAIT_L(0); PG8_BAR; PG8_MMA(0, 0, At, B0); PG8_MMA(0, 1, At, B1); PG8_BAR; PG8_SCHED;
;             PG8_LDA(At, 0, 1); PG8_STAGE(PG8_SB(0, 0), b2, voffB); PG8_STAGE(PG8_SB(0, 1), b2 + hstep, voffB); PG8_STAGE(PG8_SA(0, 0), a2, w0);
;             PG8_WAIT_V(8); PG8_WAIT_L(0); PG8_BAR; PG8_MMA(1, 0, At, B0); PG8_MMA(1, 1, At, B1); PG8_BAR; PG8_SCHED;
.LBB0_1055:
	ds_read_b128 v[166:169], v155
	ds_read_b128 v[170:173], v155 offset:1024
	ds_read_b128 v[174:177], v155 offset:2048
	ds_read_b128 v[178:181], v155 offset:3072
	ds_read_b128 v[182:185], v157
	ds_read_b128 v[186:189], v157 offset:1024
	ds_read_b128 v[190:193], v157 offset:2048
	ds_read_b128 v[194:197], v157 offset:3072
	s_add_u32 s56, s54, 0xfff80080
	s_addc_u32 s57, s55, -1
	s_cmp_eq_u32 s83, 28
	s_cselect_b32 s59, s15, s57
	s_cselect_b32 s58, s79, s56
	s_cselect_b32 s57, s49, s82
	s_cselect_b32 s56, s80, s81
	v_lshl_add_u64 v[230:231], s[54:55], 0, v[140:141]
	s_add_i32 m0, s63, 0xc000
	ds_read_b128 v[198:201], v159
	ds_read_b128 v[202:205], v159 offset:1024
	ds_read_b128 v[206:209], v159 offset:2048
	ds_read_b128 v[210:213], v159 offset:3072
	ds_read_b128 v[214:217], v159 offset:4096
	ds_read_b128 v[218:221], v159 offset:5120
	ds_read_b128 v[222:225], v159 offset:6144
	ds_read_b128 v[226:229], v159 offset:7168
	global_load_lds_dwordx4 v[230:231], off
	v_lshl_add_u64 v[230:231], s[54:55], 0, v[142:143]
	s_add_i32 m0, s63, 0xe000
	s_nop 0
	global_load_lds_dwordx4 v[230:231], off
	s_waitcnt vmcnt(8)
	s_waitcnt lgkmcnt(0)
	s_barrier
	v_mfma_f32_16x16x32_bf16 v[126:129], v[166:169], v[198:201], v[126:129]
	v_mfma_f32_16x16x32_bf16 v[122:125], v[174:177], v[198:201], v[122:125]
	v_mfma_f32_16x16x32_bf16 v[114:117], v[166:169], v[206:209], v[114:117]
	v_mfma_f32_16x16x32_bf16 v[106:109], v[174:177], v[206:209], v[106:109]
	v_mfma_f32_16x16x32_bf16 v[98:101], v[166:169], v[214:217], v[98:101]
	v_mfma_f32_16x16x32_bf16 v[90:93], v[174:177], v[214:217], v[90:93]
	v_mfma_f32_16x16x32_bf16 v[82:85], v[166:169], v[222:225], v[82:85]
	v_mfma_f32_16x16x32_bf16 v[74:77], v[174:177], v[222:225], v[74:77]
	v_mfma_f32_16x16x32_bf16 v[126:129], v[170:173], v[202:205], v[126:129]
	v_mfma_f32_16x16x32_bf16 v[122:125], v[178:181], v[202:205], v[122:125]
	v_mfma_f32_16x16x32_bf16 v[114:117], v[170:173], v[210:213], v[114:117]
	v_mfma_f32_16x16x32_bf16 v[106:109], v[178:181], v[210:213], v[106:109]
	v_mfma_f32_16x16x32_bf16 v[98:101], v[170:173], v[218:221], v[98:101]
	v_mfma_f32_16x16x32_bf16 v[90:93], v[178:181], v[218:221], v[90:93]
	v_mfma_f32_16x16x32_bf16 v[82:85], v[170:173], v[226:229], v[82:85]
	v_mfma_f32_16x16x32_bf16 v[74:77], v[178:181], v[226:229], v[74:77]
	v_mfma_f32_16x16x32_bf16 v[118:121], v[182:185], v[198:201], v[118:121]
	v_mfma_f32_16x16x32_bf16 v[110:113], v[190:193], v[198:201], v[110:113]
	v_mfma_f32_16x16x32_bf16 v[102:105], v[182:185], v[206:209], v[102:105]
	v_mfma_f32_16x16x32_bf16 v[94:97], v[190:193], v[206:209], v[94:97]
	v_mfma_f32_16x16x32_bf16 v[86:89], v[182:185], v[214:217], v[86:89]
	v_mfma_f32_16x16x32_bf16 v[78:81], v[190:193], v[214:217], v[78:81]
	v_mfma_f32_16x16x32_bf16 v[62:65], v[182:185], v[222:225], v[62:65]
	v_mfma_f32_16x16x32_bf16 v[58:61], v[190:193], v[222:225], v[58:61]
	v_mfma_f32_16x16x32_bf16 v[118:121], v[186:189], v[202:205], v[118:121]
	v_mfma_f32_16x16x32_bf16 v[110:113], v[194:197], v[202:205], v[110:113]
	v_mfma_f32_16x16x32_bf16 v[102:105], v[186:189], v[210:213], v[102:105]
	v_mfma_f32_16x16x32_bf16 v[94:97], v[194:197], v[210:213], v[94:97]
	s_barrier
	v_mfma_f32_16x16x32_bf16 v[86:89], v[186:189], v[218:221], v[86:89]
	v_mfma_f32_16x16x32_bf16 v[78:81], v[194:197], v[218:221], v[78:81]
	v_mfma_f32_16x16x32_bf16 v[62:65], v[186:189], v[226:229], v[62:65]
	v_mfma_f32_16x16x32_bf16 v[58:61], v[194:197], v[226:229], v[58:61]
	s_add_i32 s84, s73, s61
	v_lshl_add_u64 v[230:231], s[56:57], 0, v[132:133]
	s_mov_b32 m0, s84
	ds_read_b128 v[198:201], v159 offset:16384
	ds_read_b128 v[202:205], v159 offset:17408
	ds_read_b128 v[206:209], v159 offset:18432
	ds_read_b128 v[210:213], v159 offset:19456
	ds_read_b128 v[214:217], v159 offset:20480
	ds_read_b128 v[218:221], v159 offset:21504
	ds_read_b128 v[222:225], v159 offset:22528
	ds_read_b128 v[226:229], v159 offset:23552
	global_load_lds_dwordx4 v[230:231], off
	s_add_i32 m0, s84, 0x2000
	s_add_u32 s84, s56, 0x80000
	v_lshl_add_u64 v[232:233], s[56:57], 0, v[136:137]
	s_addc_u32 s85, s57, 0
	s_add_i32 s86, s74, s61
	global_load_lds_dwordx4 v[232:233], off
	v_lshl_add_u64 v[234:235], s[84:85], 0, v[132:133]
	s_mov_b32 m0, s86
	v_lshl_add_u64 v[236:237], s[58:59], 0, v[134:135]
	global_load_lds_dwordx4 v[234:235], off
	v_lshl_add_u64 v[234:235], s[84:85], 0, v[136:137]
	s_add_i32 m0, s86, 0x2000
	s_nop 0
	global_load_lds_dwordx4 v[234:235], off
	v_lshl_add_u64 v[234:235], s[58:59], 0, v[130:131]
	s_mov_b32 m0, s63
	s_nop 0
	global_load_lds_dwordx4 v[234:235], off
	s_mov_b32 m0, s64
	s_nop 0
	global_load_lds_dwordx4 v[236:237], off
	s_waitcnt vmcnt(8)
	s_waitcnt lgkmcnt(0)
	s_barrier
	v_mfma_f32_16x16x32_bf16 v[54:57], v[166:169], v[198:201], v[54:57]
	v_mfma_f32_16x16x32_bf16 v[42:45], v[174:177], v[198:201], v[42:45]
	v_mfma_f32_16x16x32_bf16 v[30:33], v[166:169], v[206:209], v[30:33]
	v_mfma_f32_16x16x32_bf16 v[26:29], v[174:177], v[206:209], v[26:29]
	v_mfma_f32_16x16x32_bf16 v[14:17], v[166:169], v[214:217], v[14:17]
	v_mfma_f32_16x16x32_bf16 v[10:13], v[174:177], v[214:217], v[10:13]
	v_mfma_f32_16x16x32_bf16 v[6:9], v[166:169], v[222:225], v[6:9]
	v_mfma_f32_16x16x32_bf16 v[2:5], v[174:177], v[222:225], v[2:5]
	v_mfma_f32_16x16x32_bf16 v[54:57], v[170:173], v[202:205], v[54:57]
	v_mfma_f32_16x16x32_bf16 v[42:45], v[178:181], v[202:205], v[42:45]
	v_mfma_f32_16x16x32_bf16 v[30:33], v[170:173], v[210:213], v[30:33]
	v_mfma_f32_16x16x32_bf16 v[26:29], v[178:181], v[210:213], v[26:29]
	v_mfma_f32_16x16x32_bf16 v[14:17], v[170:173], v[218:221], v[14:17]
	v_mfma_f32_16x16x32_bf16 v[10:13], v[178:181], v[218:221], v[10:13]
	v_mfma_f32_16x16x32_bf16 v[6:9], v[170:173], v[226:229], v[6:9]
	v_mfma_f32_16x16x32_bf16 v[2:5], v[178:181], v[226:229], v[2:5]
	v_mfma_f32_16x16x32_bf16 v[66:69], v[182:185], v[198:201], v[66:69]
	v_mfma_f32_16x16x32_bf16 v[70:73], v[190:193], v[198:201], v[70:73]
	v_mfma_f32_16x16x32_bf16 v[46:49], v[182:185], v[206:209], v[46:49]
	v_mfma_f32_16x16x32_bf16 v[50:53], v[190:193], v[206:209], v[50:53]
	v_mfma_f32_16x16x32_bf16 v[34:37], v[182:185], v[214:217], v[34:37]
	v_mfma_f32_16x16x32_bf16 v[38:41], v[190:193], v[214:217], v[38:41]
	v_mfma_f32_16x16x32_bf16 v[18:21], v[182:185], v[222:225], v[18:21]
	v_mfma_f32_16x16x32_bf16 v[22:25], v[190:193], v[222:225], v[22:25]
	v_mfma_f32_16x16x32_bf16 v[66:69], v[186:189], v[202:205], v[66:69]
	v_mfma_f32_16x16x32_bf16 v[70:73], v[194:197], v[202:205], v[70:73]
	v_mfma_f32_16x16x32_bf16 v[46:49], v[186:189], v[210:213], v[46:49]
	v_mfma_f32_16x16x32_bf16 v[50:53], v[194:197], v[210:213], v[50:53]
	s_barrier
; #define PG8_STAGE(bufoff, gbase, voff) do { _Pragma("unroll") for (int _i = 0; _i < 2; ++_i) \
;         __builtin_amdgcn_global_load_lds((const unsigned*)((const char*)(gbase) + (voff)[_i]), (PG8_LAS unsigned*)(lds + (bufoff) + ldsw + _i * 8192), 16, 0, 0); } while (0)
; #define PG8_LDA(dst, b, h) do { _Pragma("unroll") for (int m = 0; m < 4; ++m) _Pragma("unroll") for (int k = 0; k < 2; ++k) dst[m][k] = *(const PG8_LAS bf16x8*)(lds + PG8_SA(b, h) + aoff + m * 2048 + k * 1024); } while (0)
; #define PG8_LDB(dst, b, h) do { _Pragma("unroll") for (int n = 0; n < 2; ++n) _Pragma("unroll") for (int k = 0; k < 2; ++k) dst[n][k] = *(const PG8_LAS bf16x8*)(lds + PG8_SB(b, h) + boff + n * 2048 + k * 1024); } while (0)
; #define PG8_MMA(ai, bj, At, Bt) do { __builtin_amdgcn_s_setprio(1); _Pragma("unroll") for (int m = 0; m < 4; ++m) _Pragma("unroll") for (int n = 0; n < 2; ++n) _Pragma("unroll") for (int k = 0; k < 2; ++k) \
;         acc[ai][bj][m][n] = __builtin_amdgcn_mfma_f32_16x16x32_bf16(Bt[n][k], At[m][k], acc[ai][bj][m][n], 0, 0, 0); __builtin_amdgcn_s_setprio(0); } while (0)
; #define PG8_WAIT_V(n) asm volatile("s_waitcnt vmcnt(" #n ")" ::: "memory")
; #define PG8_WAIT_L(n) asm volatile("s_waitcnt lgkmcnt(" #n ")" ::: "memory")
; #define PG8_BAR __builtin_amdgcn_s_barrier()
; #define PG8_SCHED __builtin_amdgcn_sched_barrier(0)
; template <class Epi, class Sched, bool ALIGN_EPI = false>
; __device__ __forceinline__ void gemm_phase(PG8_LAS unsigned char* lds, const Gemm g, const Sched& S, const Epi& E) {
;     ...
;             PG8_WAIT_V(8); PG8_WAIT_L(0); PG8_BAR; PG8_MMA(1, 0, At, B0); PG8_MMA(1, 1, At, B1); PG8_BAR; PG8_SCHED;
;             PG8_LDB(B0, 1, 0); PG8_LDB(B1, 1, 1); PG8_SCHED; PG8_LDA(At, 1, 0); PG8_STAGE(PG8_SA(0, 1), a2 + hstepA, w1);
;             PG8_WAIT_V(8); PG8_WAIT_L(0); PG8_BAR; PG8_MMA(0, 0, At, B0); PG8_MMA(0, 1, At, B1); PG8_BAR; PG8_SCHED;
	v_mfma_f32_16x16x32_bf16 v[34:37], v[186:189], v[218:221], v[34:37]
	v_mfma_f32_16x16x32_bf16 v[38:41], v[194:197], v[218:221], v[38:41]
	v_mfma_f32_16x16x32_bf16 v[18:21], v[186:189], v[226:229], v[18:21]
	v_mfma_f32_16x16x32_bf16 v[22:25], v[194:197], v[226:229], v[22:25]
	s_add_i32 s84, 0, 0x18000
	v_add_u32_e32 v138, s84, v149
	s_add_i32 s85, 0, 0x1c000
	ds_read_b128 v[166:169], v138
	ds_read_b128 v[170:173], v138 offset:1024
	ds_read_b128 v[174:177], v138 offset:2048
	ds_read_b128 v[178:181], v138 offset:3072
	v_add_u32_e32 v138, s85, v149
	ds_read_b128 v[182:185], v138
	ds_read_b128 v[186:189], v138 offset:1024
	ds_read_b128 v[190:193], v138 offset:2048
	ds_read_b128 v[194:197], v138 offset:3072
	s_add_u32 s58, s58, 0x80000
	s_addc_u32 s59, s59, 0
	s_mov_b32 m0, s65
	v_lshl_add_u64 v[238:239], s[58:59], 0, v[130:131]
	ds_read_b128 v[198:201], v159 offset:32768
	ds_read_b128 v[202:205], v159 offset:33792
	ds_read_b128 v[206:209], v159 offset:34816
	ds_read_b128 v[210:213], v159 offset:35840
	ds_read_b128 v[214:217], v159 offset:36864
	ds_read_b128 v[218:221], v159 offset:37888
	ds_read_b128 v[222:225], v159 offset:38912
	ds_read_b128 v[226:229], v159 offset:39936
	global_load_lds_dwordx4 v[238:239], off
	v_lshl_add_u64 v[238:239], s[58:59], 0, v[134:135]
	s_mov_b32 m0, s66
	s_nop 0
	global_load_lds_dwordx4 v[238:239], off
	s_waitcnt vmcnt(8)
	s_waitcnt lgkmcnt(0)
	s_barrier
	v_mfma_f32_16x16x32_bf16 v[126:129], v[166:169], v[198:201], v[126:129]
	v_mfma_f32_16x16x32_bf16 v[122:125], v[174:177], v[198:201], v[122:125]
	v_mfma_f32_16x16x32_bf16 v[114:117], v[166:169], v[206:209], v[114:117]
	v_mfma_f32_16x16x32_bf16 v[106:109], v[174:177], v[206:209], v[106:109]
	v_mfma_f32_16x16x32_bf16 v[98:101], v[166:169], v[214:217], v[98:101]
	v_mfma_f32_16x16x32_bf16 v[90:93], v[174:177], v[214:217], v[90:93]
	v_mfma_f32_16x16x32_bf16 v[82:85], v[166:169], v[222:225], v[82:85]
	v_mfma_f32_16x16x32_bf16 v[74:77], v[174:177], v[222:225], v[74:77]
	v_mfma_f32_16x16x32_bf16 v[126:129], v[170:173], v[202:205], v[126:129]
	v_mfma_f32_16x16x32_bf16 v[122:125], v[178:181], v[202:205], v[122:125]
	v_mfma_f32_16x16x32_bf16 v[114:117], v[170:173], v[210:213], v[114:117]
	v_mfma_f32_16x16x32_bf16 v[106:109], v[178:181], v[210:213], v[106:109]
	v_mfma_f32_16x16x32_bf16 v[98:101], v[170:173], v[218:221], v[98:101]
	v_mfma_f32_16x16x32_bf16 v[90:93], v[178:181], v[218:221], v[90:93]
	v_mfma_f32_16x16x32_bf16 v[82:85], v[170:173], v[226:229], v[82:85]
	v_mfma_f32_16x16x32_bf16 v[74:77], v[178:181], v[226:229], v[74:77]
	v_mfma_f32_16x16x32_bf16 v[118:121], v[182:185], v[198:201], v[118:121]
	v_mfma_f32_16x16x32_bf16 v[110:113], v[190:193], v[198:201], v[110:113]
	v_mfma_f32_16x16x32_bf16 v[102:105], v[182:185], v[206:209], v[102:105]
	v_mfma_f32_16x16x32_bf16 v[94:97], v[190:193], v[206:209], v[94:97]
	v_mfma_f32_16x16x32_bf16 v[86:89], v[182:185], v[214:217], v[86:89]
	v_mfma_f32_16x16x32_bf16 v[78:81], v[190:193], v[214:217], v[78:81]
	v_mfma_f32_16x16x32_bf16 v[62:65], v[182:185], v[222:225], v[62:65]
	v_mfma_f32_16x16x32_bf16 v[58:61], v[190:193], v[222:225], v[58:61]
	v_mfma_f32_16x16x32_bf16 v[118:121], v[186:189], v[202:205], v[118:121]
	v_mfma_f32_16x16x32_bf16 v[110:113], v[194:197], v[202:205], v[110:113]
	v_mfma_f32_16x16x32_bf16 v[102:105], v[186:189], v[210:213], v[102:105]
	v_mfma_f32_16x16x32_bf16 v[94:97], v[194:197], v[210:213], v[94:97]
	s_barrier
; #define PG8_STAGE(bufoff, gbase, voff) do { _Pragma("unroll") for (int _i = 0; _i < 2; ++_i) \
;         __builtin_amdgcn_global_load_lds((const unsigned*)((const char*)(gbase) + (voff)[_i]), (PG8_LAS unsigned*)(lds + (bufoff) + ldsw + _i * 8192), 16, 0, 0); } while (0)
; #define PG8_LDA(dst, b, h) do { _Pragma("unroll") for (int m = 0; m < 4; ++m) _Pragma("unroll") for (int k = 0; k < 2; ++k) dst[m][k] = *(const PG8_LAS bf16x8*)(lds + PG8_SA(b, h) + aoff + m * 2048 + k * 1024); } while (0)
; #define PG8_MMA(ai, bj, At, Bt) do { __builtin_amdgcn_s_setprio(1); _Pragma("unroll") for (int m = 0; m < 4; ++m) _Pragma("unroll") for (int n = 0; n < 2; ++n) _Pragma("unroll") for (int k = 0; k < 2; ++k) \
;         acc[ai][bj][m][n] = __builtin_amdgcn_mfma_f32_16x16x32_bf16(Bt[n][k], At[m][k], acc[ai][bj][m][n], 0, 0, 0); __builtin_amdgcn_s_setprio(0); } while (0)
; #define PG8_WAIT_V(n) asm volatile("s_waitcnt vmcnt(" #n ")" ::: "memory")
; #define PG8_WAIT_L(n) asm volatile("s_waitcnt lgkmcnt(" #n ")" ::: "memory")
; #define PG8_BAR __builtin_amdgcn_s_barrier()
; #define PG8_SCHED __builtin_amdgcn_sched_barrier(0)
; template <class Epi, class Sched, bool ALIGN_EPI = false>
; __device__ __forceinline__ void gemm_phase(PG8_LAS unsigned char* lds, const Gemm g, const Sched& S, const Epi& E) {
;     ...
;             PG8_WAIT_V(8); PG8_WAIT_L(0); PG8_BAR; PG8_MMA(0, 0, At, B0); PG8_MMA(0, 1, At, B1); PG8_BAR; PG8_SCHED;
;             PG8_LDA(At, 1, 1); PG8_STAGE(PG8_SB(1, 0), b3, voffB); PG8_STAGE(PG8_SB(1, 1), b3 + hstep, voffB); PG8_STAGE(PG8_SA(1, 0), a3, w0);
;             PG8_WAIT_V(8); PG8_WAIT_L(0); PG8_BAR; PG8_MMA(1, 0, At, B0); PG8_MMA(1, 1, At, B1); PG8_BAR; PG8_SCHED;
;             if constexpr (Epi::KSCALE) { if (((t + 2) & 7) == 0 && t + 2 < nt) { E.kscale(acc, pf, ((t + 2) >> 3) - 1, wr, fr); PG8_SCHED; } }
;         }
;         if constexpr (ALIGN_EPI) { if (wr == 0) PG8_BAR; }
	v_mfma_f32_16x16x32_bf16 v[86:89], v[186:189], v[218:221], v[86:89]
	v_mfma_f32_16x16x32_bf16 v[78:81], v[194:197], v[218:221], v[78:81]
	v_mfma_f32_16x16x32_bf16 v[62:65], v[186:189], v[226:229], v[62:65]
	v_mfma_f32_16x16x32_bf16 v[58:61], v[194:197], v[226:229], v[58:61]
	s_add_i32 s58, s84, s61
	v_lshl_add_u64 v[230:231], v[230:231], 0, s[26:27]
	s_mov_b32 m0, s58
	ds_read_b128 v[198:201], v159 offset:49152
	ds_read_b128 v[202:205], v159 offset:50176
	ds_read_b128 v[206:209], v159 offset:51200
	ds_read_b128 v[210:213], v159 offset:52224
	ds_read_b128 v[214:217], v159 offset:53248
	ds_read_b128 v[218:221], v159 offset:54272
	ds_read_b128 v[222:225], v159 offset:55296
	ds_read_b128 v[226:229], v159 offset:56320
	global_load_lds_dwordx4 v[230:231], off
	s_add_i32 m0, s58, 0x2000
	s_add_u32 s56, s56, 0x80080
	v_lshl_add_u64 v[230:231], v[232:233], 0, s[26:27]
	s_addc_u32 s57, s57, 0
	s_add_i32 s58, s85, s61
	global_load_lds_dwordx4 v[230:231], off
	v_lshl_add_u64 v[230:231], s[56:57], 0, v[132:133]
	s_mov_b32 m0, s58
	s_nop 0
	global_load_lds_dwordx4 v[230:231], off
	v_lshl_add_u64 v[230:231], s[56:57], 0, v[136:137]
	s_add_i32 m0, s58, 0x2000
	s_nop 0
	global_load_lds_dwordx4 v[230:231], off
	v_lshl_add_u64 v[230:231], v[234:235], 0, s[26:27]
	s_mov_b32 m0, s69
	s_nop 0
	global_load_lds_dwordx4 v[230:231], off
	v_lshl_add_u64 v[230:231], v[236:237], 0, s[26:27]
	s_mov_b32 m0, s72
	s_nop 0
	global_load_lds_dwordx4 v[230:231], off
	s_waitcnt vmcnt(8)
	s_waitcnt lgkmcnt(0)
	s_barrier
	v_mfma_f32_16x16x32_bf16 v[54:57], v[166:169], v[198:201], v[54:57]
	v_mfma_f32_16x16x32_bf16 v[42:45], v[174:177], v[198:201], v[42:45]
	v_mfma_f32_16x16x32_bf16 v[30:33], v[166:169], v[206:209], v[30:33]
	v_mfma_f32_16x16x32_bf16 v[26:29], v[174:177], v[206:209], v[26:29]
	v_mfma_f32_16x16x32_bf16 v[14:17], v[166:169], v[214:217], v[14:17]
	v_mfma_f32_16x16x32_bf16 v[10:13], v[174:177], v[214:217], v[10:13]
	v_mfma_f32_16x16x32_bf16 v[6:9], v[166:169], v[222:225], v[6:9]
	v_mfma_f32_16x16x32_bf16 v[2:5], v[174:177], v[222:225], v[2:5]
	v_mfma_f32_16x16x32_bf16 v[54:57], v[170:173], v[202:205], v[54:57]
	v_mfma_f32_16x16x32_bf16 v[42:45], v[178:181], v[202:205], v[42:45]
	v_mfma_f32_16x16x32_bf16 v[30:33], v[170:173], v[210:213], v[30:33]
	v_mfma_f32_16x16x32_bf16 v[26:29], v[178:181], v[210:213], v[26:29]
	v_mfma_f32_16x16x32_bf16 v[14:17], v[170:173], v[218:221], v[14:17]
	v_mfma_f32_16x16x32_bf16 v[10:13], v[178:181], v[218:221], v[10:13]
	v_mfma_f32_16x16x32_bf16 v[6:9], v[170:173], v[226:229], v[6:9]
	v_mfma_f32_16x16x32_bf16 v[2:5], v[178:181], v[226:229], v[2:5]
	v_mfma_f32_16x16x32_bf16 v[66:69], v[182:185], v[198:201], v[66:69]
	v_mfma_f32_16x16x32_bf16 v[70:73], v[190:193], v[198:201], v[70:73]
	v_mfma_f32_16x16x32_bf16 v[46:49], v[182:185], v[206:209], v[46:49]
	v_mfma_f32_16x16x32_bf16 v[50:53], v[190:193], v[206:209], v[50:53]
	v_mfma_f32_16x16x32_bf16 v[34:37], v[182:185], v[214:217], v[34:37]
	v_mfma_f32_16x16x32_bf16 v[38:41], v[190:193], v[214:217], v[38:41]
	v_mfma_f32_16x16x32_bf16 v[18:21], v[182:185], v[222:225], v[18:21]
	v_mfma_f32_16x16x32_bf16 v[22:25], v[190:193], v[222:225], v[22:25]
	v_mfma_f32_16x16x32_bf16 v[66:69], v[186:189], v[202:205], v[66:69]
	v_mfma_f32_16x16x32_bf16 v[70:73], v[194:197], v[202:205], v[70:73]
	v_mfma_f32_16x16x32_bf16 v[46:49], v[186:189], v[210:213], v[46:49]
	v_mfma_f32_16x16x32_bf16 v[50:53], v[194:197], v[210:213], v[50:53]
	s_barrier
	v_mfma_f32_16x16x32_bf16 v[34:37], v[186:189], v[218:221], v[34:37]
	v_mfma_f32_16x16x32_bf16 v[38:41], v[194:197], v[218:221], v[38:41]
	v_mfma_f32_16x16x32_bf16 v[18:21], v[186:189], v[226:229], v[18:21]
	v_mfma_f32_16x16x32_bf16 v[22:25], v[194:197], v[226:229], v[22:25]
	s_add_i32 s83, s83, 2
	s_add_u32 s54, s54, 0x100
	s_addc_u32 s55, s55, 0
	s_add_u32 s81, s81, 0x100
	s_addc_u32 s82, s82, 0
	s_cmp_gt_u32 s83, 29
	s_cbranch_scc0 .LBB0_1055
	s_and_b64 vcc, exec, s[40:41]
	s_cbranch_vccz .LBB0_1058
	s_barrier

; #define PG8_STAGE(bufoff, gbase, voff) do { _Pragma("unroll") for (int _i = 0; _i < 2; ++_i) \
;         __builtin_amdgcn_global_load_lds((const unsigned*)((const char*)(gbase) + (voff)[_i]), (PG8_LAS unsigned*)(lds + (bufoff) + ldsw + _i * 8192), 16, 0, 0); } while (0)
; #define PG8_LDA(dst, b, h) do { _Pragma("unroll") for (int m = 0; m < 4; ++m) _Pragma("unroll") for (int k = 0; k < 2; ++k) dst[m][k] = *(const PG8_LAS bf16x8*)(lds + PG8_SA(b, h) + aoff + m * 2048 + k * 1024); } while (0)
; #define PG8_LDB(dst, b, h) do { _Pragma("unroll") for (int n = 0; n < 2; ++n) _Pragma("unroll") for (int k = 0; k < 2; ++k) dst[n][k] = *(const PG8_LAS bf16x8*)(lds + PG8_SB(b, h) + boff + n * 2048 + k * 1024); } while (0)
; #define PG8_MMA(ai, bj, At, Bt) do { __builtin_amdgcn_s_setprio(1); _Pragma("unroll") for (int m = 0; m < 4; ++m) _Pragma("unroll") for (int n = 0; n < 2; ++n) _Pragma("unroll") for (int k = 0; k < 2; ++k) \
;         acc[ai][bj][m][n] = __builtin_amdgcn_mfma_f32_16x16x32_bf16(Bt[n][k], At[m][k], acc[ai][bj][m][n], 0, 0, 0); __builtin_amdgcn_s_setprio(0); } while (0)
; template <class Epi, class Sched, bool ALIGN_EPI = false>
; __device__ __forceinline__ void gemm_phase(PG8_LAS unsigned char* lds, const Gemm g, const Sched& S, const Epi& E) {
;     ...
;         for (int t = 0; t < nt; t += 2) {
;             const bool last = (t == nt - 2);
;             const char* a1 = cA + (size_t)(t + 1) * kstep;
;             const char* a2 = last ? nA : cA + (size_t)(t + 2) * kstep; const char* b2 = last ? nB : cB + (size_t)(t + 2) * kstep;
;             const char* a3 = a2 + kstep; const char* b3 = b2 + kstep;
;             unsigned w0[2], w1[2];
; #pragma unroll
;             for (int i = 0; i < 2; ++i) { w0[i] = (Sched::GATHER && last) ? vn0[i] : vc0[i]; w1[i] = (Sched::GATHER && last) ? vn1[i] : vc1[i]; }
;             if (last && has_next) S.a_ready(nxt);
;             PG8_LDB(B0, 0, 0); PG8_LDB(B1, 0, 1); PG8_SCHED; PG8_LDA(At, 0, 0); PG8_STAGE(PG8_SA(1, 1), a1 + hstepA, vc1);
;             PG8_WAIT_V(8); PG8_WAIT_L(0); PG8_BAR; PG8_MMA(0, 0, At, B0); PG8_MMA(0, 1, At, B1); PG8_BAR; PG8_SCHED;
;             PG8_LDA(At, 0, 1); PG8_STAGE(PG8_SB(0, 0), b2, voffB); PG8_STAGE(PG8_SB(0, 1), b2 + hstep, voffB); PG8_STAGE(PG8_SA(0, 0), a2, w0);
;             PG8_WAIT_V(8); PG8_WAIT_L(0); PG8_BAR; PG8_MMA(1, 0, At, B0); PG8_MMA(1, 1, At, B1); PG8_BAR; PG8_SCHED;
.LBB0_1198:
	ds_read_b128 v[130:133], v168
	ds_read_b128 v[134:137], v168 offset:1024
	ds_read_b128 v[154:157], v168 offset:2048
	ds_read_b128 v[158:161], v168 offset:3072
	ds_read_b128 v[162:165], v169
	ds_read_b128 v[172:175], v169 offset:1024
	ds_read_b128 v[176:179], v169 offset:2048
	ds_read_b128 v[180:183], v169 offset:3072
	s_add_u32 s54, s52, 0xfff80080
	s_addc_u32 s55, s53, -1
	s_cmp_eq_u32 s78, 28
	s_cselect_b32 s57, s45, s55
	s_cselect_b32 s56, s74, s54
	s_cselect_b32 s55, s43, s77
	s_cselect_b32 s54, s75, s76
	v_lshl_add_u64 v[216:217], s[52:53], 0, v[146:147]
	s_add_i32 m0, s51, 0xc000
	ds_read_b128 v[184:187], v170
	ds_read_b128 v[188:191], v170 offset:1024
	ds_read_b128 v[192:195], v170 offset:2048
	ds_read_b128 v[196:199], v170 offset:3072
	ds_read_b128 v[200:203], v170 offset:4096
	ds_read_b128 v[204:207], v170 offset:5120
	ds_read_b128 v[208:211], v170 offset:6144
	ds_read_b128 v[212:215], v170 offset:7168
	global_load_lds_dwordx4 v[216:217], off
	v_lshl_add_u64 v[216:217], s[52:53], 0, v[148:149]
	s_add_i32 m0, s51, 0xe000
	s_nop 0
	global_load_lds_dwordx4 v[216:217], off
	s_waitcnt vmcnt(8)
	s_waitcnt lgkmcnt(0)
	s_barrier
	v_mfma_f32_16x16x32_bf16 v[126:129], v[130:133], v[184:187], v[126:129]
	v_mfma_f32_16x16x32_bf16 v[122:125], v[154:157], v[184:187], v[122:125]
	v_mfma_f32_16x16x32_bf16 v[118:121], v[130:133], v[192:195], v[118:121]
	v_mfma_f32_16x16x32_bf16 v[114:117], v[154:157], v[192:195], v[114:117]
	v_mfma_f32_16x16x32_bf16 v[94:97], v[130:133], v[200:203], v[94:97]
	v_mfma_f32_16x16x32_bf16 v[90:93], v[154:157], v[200:203], v[90:93]
	v_mfma_f32_16x16x32_bf16 v[78:81], v[130:133], v[208:211], v[78:81]
	v_mfma_f32_16x16x32_bf16 v[74:77], v[154:157], v[208:211], v[74:77]
	v_mfma_f32_16x16x32_bf16 v[126:129], v[134:137], v[188:191], v[126:129]
	v_mfma_f32_16x16x32_bf16 v[122:125], v[158:161], v[188:191], v[122:125]
	v_mfma_f32_16x16x32_bf16 v[118:121], v[134:137], v[196:199], v[118:121]
	v_mfma_f32_16x16x32_bf16 v[114:117], v[158:161], v[196:199], v[114:117]
	v_mfma_f32_16x16x32_bf16 v[94:97], v[134:137], v[204:207], v[94:97]
	v_mfma_f32_16x16x32_bf16 v[90:93], v[158:161], v[204:207], v[90:93]
	v_mfma_f32_16x16x32_bf16 v[78:81], v[134:137], v[212:215], v[78:81]
	v_mfma_f32_16x16x32_bf16 v[74:77], v[158:161], v[212:215], v[74:77]
	v_mfma_f32_16x16x32_bf16 v[110:113], v[162:165], v[184:187], v[110:113]
	v_mfma_f32_16x16x32_bf16 v[106:109], v[176:179], v[184:187], v[106:109]
	v_mfma_f32_16x16x32_bf16 v[102:105], v[162:165], v[192:195], v[102:105]
	v_mfma_f32_16x16x32_bf16 v[98:101], v[176:179], v[192:195], v[98:101]
	v_mfma_f32_16x16x32_bf16 v[86:89], v[162:165], v[200:203], v[86:89]
	v_mfma_f32_16x16x32_bf16 v[82:85], v[176:179], v[200:203], v[82:85]
	v_mfma_f32_16x16x32_bf16 v[70:73], v[162:165], v[208:211], v[70:73]
	v_mfma_f32_16x16x32_bf16 v[66:69], v[176:179], v[208:211], v[66:69]
	v_mfma_f32_16x16x32_bf16 v[110:113], v[172:175], v[188:191], v[110:113]
	v_mfma_f32_16x16x32_bf16 v[106:109], v[180:183], v[188:191], v[106:109]
	v_mfma_f32_16x16x32_bf16 v[102:105], v[172:175], v[196:199], v[102:105]
	v_mfma_f32_16x16x32_bf16 v[98:101], v[180:183], v[196:199], v[98:101]
	s_barrier
	v_mfma_f32_16x16x32_bf16 v[86:89], v[172:175], v[204:207], v[86:89]
	v_mfma_f32_16x16x32_bf16 v[82:85], v[180:183], v[204:207], v[82:85]
	v_mfma_f32_16x16x32_bf16 v[70:73], v[172:175], v[212:215], v[70:73]
	v_mfma_f32_16x16x32_bf16 v[66:69], v[180:183], v[212:215], v[66:69]
	s_add_i32 s79, s69, s61
	v_lshl_add_u64 v[216:217], s[54:55], 0, v[140:141]
	s_mov_b32 m0, s79
	ds_read_b128 v[184:187], v170 offset:16384
	ds_read_b128 v[188:191], v170 offset:17408
	ds_read_b128 v[192:195], v170 offset:18432
	ds_read_b128 v[196:199], v170 offset:19456
	ds_read_b128 v[200:203], v170 offset:20480
	ds_read_b128 v[204:207], v170 offset:21504
	ds_read_b128 v[208:211], v170 offset:22528
	ds_read_b128 v[212:215], v170 offset:23552
	global_load_lds_dwordx4 v[216:217], off
	s_add_i32 m0, s79, 0x2000
	s_add_u32 s80, s54, 0x80000
	v_lshl_add_u64 v[218:219], s[54:55], 0, v[144:145]
	s_addc_u32 s81, s55, 0
	s_add_i32 s79, s72, s61
	global_load_lds_dwordx4 v[218:219], off
	v_lshl_add_u64 v[220:221], s[80:81], 0, v[140:141]
	s_mov_b32 m0, s79
	v_lshl_add_u64 v[222:223], s[56:57], 0, v[142:143]
	global_load_lds_dwordx4 v[220:221], off
	v_lshl_add_u64 v[220:221], s[80:81], 0, v[144:145]
	s_add_i32 m0, s79, 0x2000
	s_nop 0
	global_load_lds_dwordx4 v[220:221], off
	v_lshl_add_u64 v[220:221], s[56:57], 0, v[138:139]
	s_mov_b32 m0, s51
	s_nop 0
	global_load_lds_dwordx4 v[220:221], off
	s_mov_b32 m0, s62
	s_nop 0
	global_load_lds_dwordx4 v[222:223], off
	s_waitcnt vmcnt(8)
	s_waitcnt lgkmcnt(0)
	s_barrier
	v_mfma_f32_16x16x32_bf16 v[54:57], v[130:133], v[184:187], v[54:57]
	v_mfma_f32_16x16x32_bf16 v[50:53], v[154:157], v[184:187], v[50:53]
	v_mfma_f32_16x16x32_bf16 v[38:41], v[130:133], v[192:195], v[38:41]
	v_mfma_f32_16x16x32_bf16 v[34:37], v[154:157], v[192:195], v[34:37]
	v_mfma_f32_16x16x32_bf16 v[22:25], v[130:133], v[200:203], v[22:25]
	v_mfma_f32_16x16x32_bf16 v[18:21], v[154:157], v[200:203], v[18:21]
	v_mfma_f32_16x16x32_bf16 v[6:9], v[130:133], v[208:211], v[6:9]
	v_mfma_f32_16x16x32_bf16 v[2:5], v[154:157], v[208:211], v[2:5]
	v_mfma_f32_16x16x32_bf16 v[54:57], v[134:137], v[188:191], v[54:57]
	v_mfma_f32_16x16x32_bf16 v[50:53], v[158:161], v[188:191], v[50:53]
	v_mfma_f32_16x16x32_bf16 v[38:41], v[134:137], v[196:199], v[38:41]
	v_mfma_f32_16x16x32_bf16 v[34:37], v[158:161], v[196:199], v[34:37]
	v_mfma_f32_16x16x32_bf16 v[22:25], v[134:137], v[204:207], v[22:25]
	v_mfma_f32_16x16x32_bf16 v[18:21], v[158:161], v[204:207], v[18:21]
	v_mfma_f32_16x16x32_bf16 v[6:9], v[134:137], v[212:215], v[6:9]
	v_mfma_f32_16x16x32_bf16 v[2:5], v[158:161], v[212:215], v[2:5]
	v_mfma_f32_16x16x32_bf16 v[62:65], v[162:165], v[184:187], v[62:65]
	v_mfma_f32_16x16x32_bf16 v[58:61], v[176:179], v[184:187], v[58:61]
	v_mfma_f32_16x16x32_bf16 v[46:49], v[162:165], v[192:195], v[46:49]
	v_mfma_f32_16x16x32_bf16 v[42:45], v[176:179], v[192:195], v[42:45]
	v_mfma_f32_16x16x32_bf16 v[30:33], v[162:165], v[200:203], v[30:33]
	v_mfma_f32_16x16x32_bf16 v[26:29], v[176:179], v[200:203], v[26:29]
	v_mfma_f32_16x16x32_bf16 v[14:17], v[162:165], v[208:211], v[14:17]
	v_mfma_f32_16x16x32_bf16 v[10:13], v[176:179], v[208:211], v[10:13]
	v_mfma_f32_16x16x32_bf16 v[62:65], v[172:175], v[188:191], v[62:65]
	v_mfma_f32_16x16x32_bf16 v[58:61], v[180:183], v[188:191], v[58:61]
	v_mfma_f32_16x16x32_bf16 v[46:49], v[172:175], v[196:199], v[46:49]
	v_mfma_f32_16x16x32_bf16 v[42:45], v[180:183], v[196:199], v[42:45]
	s_barrier
; #define PG8_STAGE(bufoff, gbase, voff) do { _Pragma("unroll") for (int _i = 0; _i < 2; ++_i) \
;         __builtin_amdgcn_global_load_lds((const unsigned*)((const char*)(gbase) + (voff)[_i]), (PG8_LAS unsigned*)(lds + (bufoff) + ldsw + _i * 8192), 16, 0, 0); } while (0)
; #define PG8_LDA(dst, b, h) do { _Pragma("unroll") for (int m = 0; m < 4; ++m) _Pragma("unroll") for (int k = 0; k < 2; ++k) dst[m][k] = *(const PG8_LAS bf16x8*)(lds + PG8_SA(b, h) + aoff + m * 2048 + k * 1024); } while (0)
; #define PG8_LDB(dst, b, h) do { _Pragma("unroll") for (int n = 0; n < 2; ++n) _Pragma("unroll") for (int k = 0; k < 2; ++k) dst[n][k] = *(const PG8_LAS bf16x8*)(lds + PG8_SB(b, h) + boff + n * 2048 + k * 1024); } while (0)
; #define PG8_MMA(ai, bj, At, Bt) do { __builtin_amdgcn_s_setprio(1); _Pragma("unroll") for (int m = 0; m < 4; ++m) _Pragma("unroll") for (int n = 0; n < 2; ++n) _Pragma("unroll") for (int k = 0; k < 2; ++k) \
;         acc[ai][bj][m][n] = __builtin_amdgcn_mfma_f32_16x16x32_bf16(Bt[n][k], At[m][k], acc[ai][bj][m][n], 0, 0, 0); __builtin_amdgcn_s_setprio(0); } while (0)
; #define PG8_WAIT_V(n) asm volatile("s_waitcnt vmcnt(" #n ")" ::: "memory")
; #define PG8_WAIT_L(n) asm volatile("s_waitcnt lgkmcnt(" #n ")" ::: "memory")
; #define PG8_BAR __builtin_amdgcn_s_barrier()
; #define PG8_SCHED __builtin_amdgcn_sched_barrier(0)
; template <class Epi, class Sched, bool ALIGN_EPI = false>
; __device__ __forceinline__ void gemm_phase(PG8_LAS unsigned char* lds, const Gemm g, const Sched& S, const Epi& E) {
;     ...
;             PG8_WAIT_V(8); PG8_WAIT_L(0); PG8_BAR; PG8_MMA(1, 0, At, B0); PG8_MMA(1, 1, At, B1); PG8_BAR; PG8_SCHED;
;             PG8_LDB(B0, 1, 0); PG8_LDB(B1, 1, 1); PG8_SCHED; PG8_LDA(At, 1, 0); PG8_STAGE(PG8_SA(0, 1), a2 + hstepA, w1);
;             PG8_WAIT_V(8); PG8_WAIT_L(0); PG8_BAR; PG8_MMA(0, 0, At, B0); PG8_MMA(0, 1, At, B1); PG8_BAR; PG8_SCHED;
	v_mfma_f32_16x16x32_bf16 v[30:33], v[172:175], v[204:207], v[30:33]
	v_mfma_f32_16x16x32_bf16 v[26:29], v[180:183], v[204:207], v[26:29]
	v_mfma_f32_16x16x32_bf16 v[14:17], v[172:175], v[212:215], v[14:17]
	v_mfma_f32_16x16x32_bf16 v[10:13], v[180:183], v[212:215], v[10:13]
	s_add_i32 s79, 0, 0x18000
	s_add_i32 s80, 0, 0x1c000
	v_add_u32_e32 v158, s79, v166
	v_add_u32_e32 v171, s80, v166
	ds_read_b128 v[130:133], v158
	ds_read_b128 v[134:137], v158 offset:1024
	ds_read_b128 v[154:157], v158 offset:2048
	ds_read_b128 v[158:161], v158 offset:3072
	ds_read_b128 v[162:165], v171
	ds_read_b128 v[172:175], v171 offset:1024
	ds_read_b128 v[176:179], v171 offset:2048
	ds_read_b128 v[180:183], v171 offset:3072
	s_add_u32 s56, s56, 0x80000
	s_addc_u32 s57, s57, 0
	s_mov_b32 m0, s63
	v_lshl_add_u64 v[224:225], s[56:57], 0, v[138:139]
	ds_read_b128 v[184:187], v170 offset:32768
	ds_read_b128 v[188:191], v170 offset:33792
	ds_read_b128 v[192:195], v170 offset:34816
	ds_read_b128 v[196:199], v170 offset:35840
	ds_read_b128 v[200:203], v170 offset:36864
	ds_read_b128 v[204:207], v170 offset:37888
	ds_read_b128 v[208:211], v170 offset:38912
	ds_read_b128 v[212:215], v170 offset:39936
	global_load_lds_dwordx4 v[224:225], off
	v_lshl_add_u64 v[224:225], s[56:57], 0, v[142:143]
	s_mov_b32 m0, s64
	s_nop 0
	global_load_lds_dwordx4 v[224:225], off
	s_waitcnt vmcnt(8)
	s_waitcnt lgkmcnt(0)
	s_barrier
	v_mfma_f32_16x16x32_bf16 v[126:129], v[130:133], v[184:187], v[126:129]
	v_mfma_f32_16x16x32_bf16 v[122:125], v[154:157], v[184:187], v[122:125]
	v_mfma_f32_16x16x32_bf16 v[118:121], v[130:133], v[192:195], v[118:121]
	v_mfma_f32_16x16x32_bf16 v[114:117], v[154:157], v[192:195], v[114:117]
	v_mfma_f32_16x16x32_bf16 v[94:97], v[130:133], v[200:203], v[94:97]
	v_mfma_f32_16x16x32_bf16 v[90:93], v[154:157], v[200:203], v[90:93]
	v_mfma_f32_16x16x32_bf16 v[78:81], v[130:133], v[208:211], v[78:81]
	v_mfma_f32_16x16x32_bf16 v[74:77], v[154:157], v[208:211], v[74:77]
	v_mfma_f32_16x16x32_bf16 v[126:129], v[134:137], v[188:191], v[126:129]
	v_mfma_f32_16x16x32_bf16 v[122:125], v[158:161], v[188:191], v[122:125]
	v_mfma_f32_16x16x32_bf16 v[118:121], v[134:137], v[196:199], v[118:121]
	v_mfma_f32_16x16x32_bf16 v[114:117], v[158:161], v[196:199], v[114:117]
	v_mfma_f32_16x16x32_bf16 v[94:97], v[134:137], v[204:207], v[94:97]
	v_mfma_f32_16x16x32_bf16 v[90:93], v[158:161], v[204:207], v[90:93]
	v_mfma_f32_16x16x32_bf16 v[78:81], v[134:137], v[212:215], v[78:81]
	v_mfma_f32_16x16x32_bf16 v[74:77], v[158:161], v[212:215], v[74:77]
	v_mfma_f32_16x16x32_bf16 v[110:113], v[162:165], v[184:187], v[110:113]
	v_mfma_f32_16x16x32_bf16 v[106:109], v[176:179], v[184:187], v[106:109]
	v_mfma_f32_16x16x32_bf16 v[102:105], v[162:165], v[192:195], v[102:105]
	v_mfma_f32_16x16x32_bf16 v[98:101], v[176:179], v[192:195], v[98:101]
	v_mfma_f32_16x16x32_bf16 v[86:89], v[162:165], v[200:203], v[86:89]
	v_mfma_f32_16x16x32_bf16 v[82:85], v[176:179], v[200:203], v[82:85]
	v_mfma_f32_16x16x32_bf16 v[70:73], v[162:165], v[208:211], v[70:73]
	v_mfma_f32_16x16x32_bf16 v[66:69], v[176:179], v[208:211], v[66:69]
	v_mfma_f32_16x16x32_bf16 v[110:113], v[172:175], v[188:191], v[110:113]
	v_mfma_f32_16x16x32_bf16 v[106:109], v[180:183], v[188:191], v[106:109]
	v_mfma_f32_16x16x32_bf16 v[102:105], v[172:175], v[196:199], v[102:105]
	v_mfma_f32_16x16x32_bf16 v[98:101], v[180:183], v[196:199], v[98:101]
	s_barrier
; #define PG8_STAGE(bufoff, gbase, voff) do { _Pragma("unroll") for (int _i = 0; _i < 2; ++_i) \
;         __builtin_amdgcn_global_load_lds((const unsigned*)((const char*)(gbase) + (voff)[_i]), (PG8_LAS unsigned*)(lds + (bufoff) + ldsw + _i * 8192), 16, 0, 0); } while (0)
; #define PG8_LDA(dst, b, h) do { _Pragma("unroll") for (int m = 0; m < 4; ++m) _Pragma("unroll") for (int k = 0; k < 2; ++k) dst[m][k] = *(const PG8_LAS bf16x8*)(lds + PG8_SA(b, h) + aoff + m * 2048 + k * 1024); } while (0)
; #define PG8_MMA(ai, bj, At, Bt) do { __builtin_amdgcn_s_setprio(1); _Pragma("unroll") for (int m = 0; m < 4; ++m) _Pragma("unroll") for (int n = 0; n < 2; ++n) _Pragma("unroll") for (int k = 0; k < 2; ++k) \
;         acc[ai][bj][m][n] = __builtin_amdgcn_mfma_f32_16x16x32_bf16(Bt[n][k], At[m][k], acc[ai][bj][m][n], 0, 0, 0); __builtin_amdgcn_s_setprio(0); } while (0)
; #define PG8_WAIT_V(n) asm volatile("s_waitcnt vmcnt(" #n ")" ::: "memory")
; #define PG8_WAIT_L(n) asm volatile("s_waitcnt lgkmcnt(" #n ")" ::: "memory")
; #define PG8_BAR __builtin_amdgcn_s_barrier()
; #define PG8_SCHED __builtin_amdgcn_sched_barrier(0)
; template <class Epi, class Sched, bool ALIGN_EPI = false>
; __device__ __forceinline__ void gemm_phase(PG8_LAS unsigned char* lds, const Gemm g, const Sched& S, const Epi& E) {
;     ...
;             PG8_WAIT_V(8); PG8_WAIT_L(0); PG8_BAR; PG8_MMA(0, 0, At, B0); PG8_MMA(0, 1, At, B1); PG8_BAR; PG8_SCHED;
;             PG8_LDA(At, 1, 1); PG8_STAGE(PG8_SB(1, 0), b3, voffB); PG8_STAGE(PG8_SB(1, 1), b3 + hstep, voffB); PG8_STAGE(PG8_SA(1, 0), a3, w0);
;             PG8_WAIT_V(8); PG8_WAIT_L(0); PG8_BAR; PG8_MMA(1, 0, At, B0); PG8_MMA(1, 1, At, B1); PG8_BAR; PG8_SCHED;
;             if constexpr (Epi::KSCALE) { if (((t + 2) & 7) == 0 && t + 2 < nt) { E.kscale(acc, pf, ((t + 2) >> 3) - 1, wr, fr); PG8_SCHED; } }
;         }
;         if constexpr (ALIGN_EPI) { if (wr == 0) PG8_BAR; }
	v_mfma_f32_16x16x32_bf16 v[86:89], v[172:175], v[204:207], v[86:89]
	v_mfma_f32_16x16x32_bf16 v[82:85], v[180:183], v[204:207], v[82:85]
	v_mfma_f32_16x16x32_bf16 v[70:73], v[172:175], v[212:215], v[70:73]
	v_mfma_f32_16x16x32_bf16 v[66:69], v[180:183], v[212:215], v[66:69]
	s_add_i32 s56, s79, s61
	v_lshl_add_u64 v[216:217], v[216:217], 0, s[18:19]
	s_mov_b32 m0, s56
	ds_read_b128 v[184:187], v170 offset:49152
	ds_read_b128 v[188:191], v170 offset:50176
	ds_read_b128 v[192:195], v170 offset:51200
	ds_read_b128 v[196:199], v170 offset:52224
	ds_read_b128 v[200:203], v170 offset:53248
	ds_read_b128 v[204:207], v170 offset:54272
	ds_read_b128 v[208:211], v170 offset:55296
	ds_read_b128 v[212:215], v170 offset:56320
	global_load_lds_dwordx4 v[216:217], off
	s_add_i32 m0, s56, 0x2000
	s_add_u32 s54, s54, 0x80080
	v_lshl_add_u64 v[216:217], v[218:219], 0, s[18:19]
	s_addc_u32 s55, s55, 0
	s_add_i32 s56, s80, s61
	global_load_lds_dwordx4 v[216:217], off
	v_lshl_add_u64 v[216:217], s[54:55], 0, v[140:141]
	s_mov_b32 m0, s56
	s_nop 0
	global_load_lds_dwordx4 v[216:217], off
	v_lshl_add_u64 v[216:217], s[54:55], 0, v[144:145]
	s_add_i32 m0, s56, 0x2000
	s_nop 0
	global_load_lds_dwordx4 v[216:217], off
	v_lshl_add_u64 v[216:217], v[220:221], 0, s[18:19]
	s_mov_b32 m0, s67
	s_nop 0
	global_load_lds_dwordx4 v[216:217], off
	v_lshl_add_u64 v[216:217], v[222:223], 0, s[18:19]
	s_mov_b32 m0, s68
	s_nop 0
	global_load_lds_dwordx4 v[216:217], off
	s_waitcnt vmcnt(8)
	s_waitcnt lgkmcnt(0)
	s_barrier
	v_mfma_f32_16x16x32_bf16 v[54:57], v[130:133], v[184:187], v[54:57]
	v_mfma_f32_16x16x32_bf16 v[50:53], v[154:157], v[184:187], v[50:53]
	v_mfma_f32_16x16x32_bf16 v[38:41], v[130:133], v[192:195], v[38:41]
	v_mfma_f32_16x16x32_bf16 v[34:37], v[154:157], v[192:195], v[34:37]
	v_mfma_f32_16x16x32_bf16 v[22:25], v[130:133], v[200:203], v[22:25]
	v_mfma_f32_16x16x32_bf16 v[18:21], v[154:157], v[200:203], v[18:21]
	v_mfma_f32_16x16x32_bf16 v[6:9], v[130:133], v[208:211], v[6:9]
	v_mfma_f32_16x16x32_bf16 v[2:5], v[154:157], v[208:211], v[2:5]
	v_mfma_f32_16x16x32_bf16 v[54:57], v[134:137], v[188:191], v[54:57]
	v_mfma_f32_16x16x32_bf16 v[50:53], v[158:161], v[188:191], v[50:53]
	v_mfma_f32_16x16x32_bf16 v[38:41], v[134:137], v[196:199], v[38:41]
	v_mfma_f32_16x16x32_bf16 v[34:37], v[158:161], v[196:199], v[34:37]
	v_mfma_f32_16x16x32_bf16 v[22:25], v[134:137], v[204:207], v[22:25]
	v_mfma_f32_16x16x32_bf16 v[18:21], v[158:161], v[204:207], v[18:21]
	v_mfma_f32_16x16x32_bf16 v[6:9], v[134:137], v[212:215], v[6:9]
	v_mfma_f32_16x16x32_bf16 v[2:5], v[158:161], v[212:215], v[2:5]
	v_mfma_f32_16x16x32_bf16 v[62:65], v[162:165], v[184:187], v[62:65]
	v_mfma_f32_16x16x32_bf16 v[58:61], v[176:179], v[184:187], v[58:61]
	v_mfma_f32_16x16x32_bf16 v[46:49], v[162:165], v[192:195], v[46:49]
	v_mfma_f32_16x16x32_bf16 v[42:45], v[176:179], v[192:195], v[42:45]
	v_mfma_f32_16x16x32_bf16 v[30:33], v[162:165], v[200:203], v[30:33]
	v_mfma_f32_16x16x32_bf16 v[26:29], v[176:179], v[200:203], v[26:29]
	v_mfma_f32_16x16x32_bf16 v[14:17], v[162:165], v[208:211], v[14:17]
	v_mfma_f32_16x16x32_bf16 v[10:13], v[176:179], v[208:211], v[10:13]
	v_mfma_f32_16x16x32_bf16 v[62:65], v[172:175], v[188:191], v[62:65]
	v_mfma_f32_16x16x32_bf16 v[58:61], v[180:183], v[188:191], v[58:61]
	v_mfma_f32_16x16x32_bf16 v[46:49], v[172:175], v[196:199], v[46:49]
	v_mfma_f32_16x16x32_bf16 v[42:45], v[180:183], v[196:199], v[42:45]
	s_barrier
	v_mfma_f32_16x16x32_bf16 v[30:33], v[172:175], v[204:207], v[30:33]
	v_mfma_f32_16x16x32_bf16 v[26:29], v[180:183], v[204:207], v[26:29]
	v_mfma_f32_16x16x32_bf16 v[14:17], v[172:175], v[212:215], v[14:17]
	v_mfma_f32_16x16x32_bf16 v[10:13], v[180:183], v[212:215], v[10:13]
	s_add_i32 s78, s78, 2
	s_add_u32 s52, s52, 0x100
	s_addc_u32 s53, s53, 0
	s_add_u32 s76, s76, 0x100
	s_addc_u32 s77, s77, 0
	s_cmp_gt_u32 s78, 29
	s_cbranch_scc0 .LBB0_1198
	s_and_b64 vcc, exec, s[22:23]
	s_cbranch_vccz .LBB0_1201
	s_barrier

; #define PG8_STAGE(bufoff, gbase, voff) do { _Pragma("unroll") for (int _i = 0; _i < 2; ++_i) \
;         __builtin_amdgcn_global_load_lds((const unsigned*)((const char*)(gbase) + (voff)[_i]), (PG8_LAS unsigned*)(lds + (bufoff) + ldsw + _i * 8192), 16, 0, 0); } while (0)
; #define PG8_LDA(dst, b, h) do { _Pragma("unroll") for (int m = 0; m < 4; ++m) _Pragma("unroll") for (int k = 0; k < 2; ++k) dst[m][k] = *(const PG8_LAS bf16x8*)(lds + PG8_SA(b, h) + aoff + m * 2048 + k * 1024); } while (0)
; #define PG8_LDB(dst, b, h) do { _Pragma("unroll") for (int n = 0; n < 2; ++n) _Pragma("unroll") for (int k = 0; k < 2; ++k) dst[n][k] = *(const PG8_LAS bf16x8*)(lds + PG8_SB(b, h) + boff + n * 2048 + k * 1024); } while (0)
; #define PG8_MMA(ai, bj, At, Bt) do { __builtin_amdgcn_s_setprio(1); _Pragma("unroll") for (int m = 0; m < 4; ++m) _Pragma("unroll") for (int n = 0; n < 2; ++n) _Pragma("unroll") for (int k = 0; k < 2; ++k) \
;         acc[ai][bj][m][n] = __builtin_amdgcn_mfma_f32_16x16x32_bf16(Bt[n][k], At[m][k], acc[ai][bj][m][n], 0, 0, 0); __builtin_amdgcn_s_setprio(0); } while (0)
; template <class Epi, class Sched, bool ALIGN_EPI = false>
; __device__ __forceinline__ void gemm_phase(PG8_LAS unsigned char* lds, const Gemm g, const Sched& S, const Epi& E) {
;     ...
;         for (int t = 0; t < nt; t += 2) {
;             const bool last = (t == nt - 2);
;             const char* a1 = cA + (size_t)(t + 1) * kstep;
;             const char* a2 = last ? nA : cA + (size_t)(t + 2) * kstep; const char* b2 = last ? nB : cB + (size_t)(t + 2) * kstep;
;             const char* a3 = a2 + kstep; const char* b3 = b2 + kstep;
;             unsigned w0[2], w1[2];
; #pragma unroll
;             for (int i = 0; i < 2; ++i) { w0[i] = (Sched::GATHER && last) ? vn0[i] : vc0[i]; w1[i] = (Sched::GATHER && last) ? vn1[i] : vc1[i]; }
;             if (last && has_next) S.a_ready(nxt);
;             PG8_LDB(B0, 0, 0); PG8_LDB(B1, 0, 1); PG8_SCHED; PG8_LDA(At, 0, 0); PG8_STAGE(PG8_SA(1, 1), a1 + hstepA, vc1);
;             PG8_WAIT_V(8); PG8_WAIT_L(0); PG8_BAR; PG8_MMA(0, 0, At, B0); PG8_MMA(0, 1, At, B1); PG8_BAR; PG8_SCHED;
;             PG8_LDA(At, 0, 1); PG8_STAGE(PG8_SB(0, 0), b2, voffB); PG8_STAGE(PG8_SB(0, 1), b2 + hstep, voffB); PG8_STAGE(PG8_SA(0, 0), a2, w0);
;             PG8_WAIT_V(8); PG8_WAIT_L(0); PG8_BAR; PG8_MMA(1, 0, At, B0); PG8_MMA(1, 1, At, B1); PG8_BAR; PG8_SCHED;
.LBB0_1414:
	s_add_u32 s56, s36, s54
	v_add_u32_e32 v155, s79, v143
	s_addc_u32 s57, s37, s55
	ds_read_b128 v[164:167], v155
	ds_read_b128 v[168:171], v155 offset:1024
	ds_read_b128 v[172:175], v155 offset:2048
	ds_read_b128 v[176:179], v155 offset:3072
	v_add_u32_e32 v155, s80, v143
	s_add_u32 s58, s56, 0x3c800100
	ds_read_b128 v[180:183], v155
	ds_read_b128 v[184:187], v155 offset:1024
	ds_read_b128 v[188:191], v155 offset:2048
	ds_read_b128 v[192:195], v155 offset:3072
	s_addc_u32 s59, s57, 0
	s_add_u32 s88, s47, s54
	s_addc_u32 s89, s86, s55
	s_cmpk_eq_i32 s54, 0xf00
	s_cselect_b64 vcc, -1, 0
	s_and_b64 s[56:57], vcc, exec
	v_cndmask_b32_e32 v134, v151, v149, vcc
	s_cselect_b32 s59, s21, s59
	s_cselect_b32 s58, s20, s58
	v_cndmask_b32_e32 v153, v152, v157, vcc
	v_cndmask_b32_e32 v228, v150, v162, vcc
	v_cndmask_b32_e32 v155, v154, v163, vcc
	s_cselect_b32 s57, s51, s89
	s_cselect_b32 s56, s50, s88
	v_lshl_add_u64 v[230:231], v[160:161], 0, s[54:55]
	s_add_i32 m0, s53, 0xc000
	ds_read_b128 v[196:199], v147
	ds_read_b128 v[200:203], v147 offset:1024
	ds_read_b128 v[204:207], v147 offset:2048
	ds_read_b128 v[208:211], v147 offset:3072
	ds_read_b128 v[212:215], v147 offset:4096
	ds_read_b128 v[216:219], v147 offset:5120
	ds_read_b128 v[220:223], v147 offset:6144
	ds_read_b128 v[224:227], v147 offset:7168
	global_load_lds_dwordx4 v[230:231], off
	v_lshl_add_u64 v[230:231], v[158:159], 0, s[54:55]
	s_add_i32 m0, s53, 0xe000
	s_nop 0
	global_load_lds_dwordx4 v[230:231], off
	s_waitcnt vmcnt(8)
	s_waitcnt lgkmcnt(0)
	s_barrier
	v_mfma_f32_16x16x32_bf16 v[126:129], v[164:167], v[196:199], v[126:129]
	v_mfma_f32_16x16x32_bf16 v[122:125], v[172:175], v[196:199], v[122:125]
	v_mfma_f32_16x16x32_bf16 v[110:113], v[164:167], v[204:207], v[110:113]
	v_mfma_f32_16x16x32_bf16 v[106:109], v[172:175], v[204:207], v[106:109]
	v_mfma_f32_16x16x32_bf16 v[94:97], v[164:167], v[212:215], v[94:97]
	v_mfma_f32_16x16x32_bf16 v[90:93], v[172:175], v[212:215], v[90:93]
	v_mfma_f32_16x16x32_bf16 v[78:81], v[164:167], v[220:223], v[78:81]
	v_mfma_f32_16x16x32_bf16 v[74:77], v[172:175], v[220:223], v[74:77]
	v_mfma_f32_16x16x32_bf16 v[126:129], v[168:171], v[200:203], v[126:129]
	v_mfma_f32_16x16x32_bf16 v[122:125], v[176:179], v[200:203], v[122:125]
	v_mfma_f32_16x16x32_bf16 v[110:113], v[168:171], v[208:211], v[110:113]
	v_mfma_f32_16x16x32_bf16 v[106:109], v[176:179], v[208:211], v[106:109]
	v_mfma_f32_16x16x32_bf16 v[94:97], v[168:171], v[216:219], v[94:97]
	v_mfma_f32_16x16x32_bf16 v[90:93], v[176:179], v[216:219], v[90:93]
	v_mfma_f32_16x16x32_bf16 v[78:81], v[168:171], v[224:227], v[78:81]
	v_mfma_f32_16x16x32_bf16 v[74:77], v[176:179], v[224:227], v[74:77]
	v_mfma_f32_16x16x32_bf16 v[118:121], v[180:183], v[196:199], v[118:121]
	v_mfma_f32_16x16x32_bf16 v[114:117], v[188:191], v[196:199], v[114:117]
	v_mfma_f32_16x16x32_bf16 v[102:105], v[180:183], v[204:207], v[102:105]
	v_mfma_f32_16x16x32_bf16 v[98:101], v[188:191], v[204:207], v[98:101]
	v_mfma_f32_16x16x32_bf16 v[86:89], v[180:183], v[212:215], v[86:89]
	v_mfma_f32_16x16x32_bf16 v[82:85], v[188:191], v[212:215], v[82:85]
	v_mfma_f32_16x16x32_bf16 v[70:73], v[180:183], v[220:223], v[70:73]
	v_mfma_f32_16x16x32_bf16 v[66:69], v[188:191], v[220:223], v[66:69]
	v_mfma_f32_16x16x32_bf16 v[118:121], v[184:187], v[200:203], v[118:121]
	v_mfma_f32_16x16x32_bf16 v[114:117], v[192:195], v[200:203], v[114:117]
	v_mfma_f32_16x16x32_bf16 v[102:105], v[184:187], v[208:211], v[102:105]
	v_mfma_f32_16x16x32_bf16 v[98:101], v[192:195], v[208:211], v[98:101]
	s_barrier
	v_mfma_f32_16x16x32_bf16 v[86:89], v[184:187], v[216:219], v[86:89]
	v_mfma_f32_16x16x32_bf16 v[82:85], v[192:195], v[216:219], v[82:85]
	v_mfma_f32_16x16x32_bf16 v[70:73], v[184:187], v[224:227], v[70:73]
	v_mfma_f32_16x16x32_bf16 v[66:69], v[192:195], v[224:227], v[66:69]
	s_add_i32 s88, s79, s71
	v_lshl_add_u64 v[230:231], s[56:57], 0, v[130:131]
	s_mov_b32 m0, s88
	ds_read_b128 v[196:199], v147 offset:16384
	ds_read_b128 v[200:203], v147 offset:17408
	ds_read_b128 v[204:207], v147 offset:18432
	ds_read_b128 v[208:211], v147 offset:19456
	ds_read_b128 v[212:215], v147 offset:20480
	ds_read_b128 v[216:219], v147 offset:21504
	ds_read_b128 v[220:223], v147 offset:22528
	ds_read_b128 v[224:227], v147 offset:23552
	global_load_lds_dwordx4 v[230:231], off
	s_add_i32 m0, s88, 0x2000
	s_add_u32 s88, s56, 0x80000
	v_lshl_add_u64 v[232:233], s[56:57], 0, v[132:133]
	s_addc_u32 s89, s57, 0
	s_add_i32 s90, s80, s71
	global_load_lds_dwordx4 v[232:233], off
	v_lshl_add_u64 v[234:235], s[88:89], 0, v[130:131]
	s_mov_b32 m0, s90
	v_mov_b32_e32 v229, v135
	global_load_lds_dwordx4 v[234:235], off
	v_lshl_add_u64 v[234:235], s[88:89], 0, v[132:133]
	s_add_i32 m0, s90, 0x2000
	s_nop 0
	global_load_lds_dwordx4 v[234:235], off
	s_mov_b32 m0, s53
	v_lshl_add_u64 v[234:235], s[58:59], 0, v[134:135]
	global_load_lds_dwordx4 v134, s[58:59]
	s_mov_b32 m0, s72
	s_nop 0
	global_load_lds_dwordx4 v228, s[58:59]
	s_waitcnt vmcnt(8)
	s_waitcnt lgkmcnt(0)
	v_lshl_add_u64 v[228:229], s[58:59], 0, v[228:229]
	s_barrier
; #define PG8_STAGE(bufoff, gbase, voff) do { _Pragma("unroll") for (int _i = 0; _i < 2; ++_i) \
;         __builtin_amdgcn_global_load_lds((const unsigned*)((const char*)(gbase) + (voff)[_i]), (PG8_LAS unsigned*)(lds + (bufoff) + ldsw + _i * 8192), 16, 0, 0); } while (0)
; #define PG8_LDA(dst, b, h) do { _Pragma("unroll") for (int m = 0; m < 4; ++m) _Pragma("unroll") for (int k = 0; k < 2; ++k) dst[m][k] = *(const PG8_LAS bf16x8*)(lds + PG8_SA(b, h) + aoff + m * 2048 + k * 1024); } while (0)
; #define PG8_LDB(dst, b, h) do { _Pragma("unroll") for (int n = 0; n < 2; ++n) _Pragma("unroll") for (int k = 0; k < 2; ++k) dst[n][k] = *(const PG8_LAS bf16x8*)(lds + PG8_SB(b, h) + boff + n * 2048 + k * 1024); } while (0)
; #define PG8_MMA(ai, bj, At, Bt) do { __builtin_amdgcn_s_setprio(1); _Pragma("unroll") for (int m = 0; m < 4; ++m) _Pragma("unroll") for (int n = 0; n < 2; ++n) _Pragma("unroll") for (int k = 0; k < 2; ++k) \
;         acc[ai][bj][m][n] = __builtin_amdgcn_mfma_f32_16x16x32_bf16(Bt[n][k], At[m][k], acc[ai][bj][m][n], 0, 0, 0); __builtin_amdgcn_s_setprio(0); } while (0)
; #define PG8_WAIT_V(n) asm volatile("s_waitcnt vmcnt(" #n ")" ::: "memory")
; #define PG8_WAIT_L(n) asm volatile("s_waitcnt lgkmcnt(" #n ")" ::: "memory")
; #define PG8_BAR __builtin_amdgcn_s_barrier()
; #define PG8_SCHED __builtin_amdgcn_sched_barrier(0)
; template <class Epi, class Sched, bool ALIGN_EPI = false>
; __device__ __forceinline__ void gemm_phase(PG8_LAS unsigned char* lds, const Gemm g, const Sched& S, const Epi& E) {
;     ...
;             PG8_WAIT_V(8); PG8_WAIT_L(0); PG8_BAR; PG8_MMA(1, 0, At, B0); PG8_MMA(1, 1, At, B1); PG8_BAR; PG8_SCHED;
;             PG8_LDB(B0, 1, 0); PG8_LDB(B1, 1, 1); PG8_SCHED; PG8_LDA(At, 1, 0); PG8_STAGE(PG8_SA(0, 1), a2 + hstepA, w1);
;             PG8_WAIT_V(8); PG8_WAIT_L(0); PG8_BAR; PG8_MMA(0, 0, At, B0); PG8_MMA(0, 1, At, B1); PG8_BAR; PG8_SCHED;
	v_mfma_f32_16x16x32_bf16 v[62:65], v[164:167], v[196:199], v[62:65]
	v_mfma_f32_16x16x32_bf16 v[58:61], v[172:175], v[196:199], v[58:61]
	v_mfma_f32_16x16x32_bf16 v[50:53], v[164:167], v[204:207], v[50:53]
	v_mfma_f32_16x16x32_bf16 v[42:45], v[172:175], v[204:207], v[42:45]
	v_mfma_f32_16x16x32_bf16 v[34:37], v[164:167], v[212:215], v[34:37]
	v_mfma_f32_16x16x32_bf16 v[30:33], v[172:175], v[212:215], v[30:33]
	v_mfma_f32_16x16x32_bf16 v[14:17], v[164:167], v[220:223], v[14:17]
	v_mfma_f32_16x16x32_bf16 v[2:5], v[172:175], v[220:223], v[2:5]
	v_mfma_f32_16x16x32_bf16 v[62:65], v[168:171], v[200:203], v[62:65]
	v_mfma_f32_16x16x32_bf16 v[58:61], v[176:179], v[200:203], v[58:61]
	v_mfma_f32_16x16x32_bf16 v[50:53], v[168:171], v[208:211], v[50:53]
	v_mfma_f32_16x16x32_bf16 v[42:45], v[176:179], v[208:211], v[42:45]
	v_mfma_f32_16x16x32_bf16 v[34:37], v[168:171], v[216:219], v[34:37]
	v_mfma_f32_16x16x32_bf16 v[30:33], v[176:179], v[216:219], v[30:33]
	v_mfma_f32_16x16x32_bf16 v[14:17], v[168:171], v[224:227], v[14:17]
	v_mfma_f32_16x16x32_bf16 v[2:5], v[176:179], v[224:227], v[2:5]
	v_mfma_f32_16x16x32_bf16 v[54:57], v[180:183], v[196:199], v[54:57]
	v_mfma_f32_16x16x32_bf16 v[46:49], v[188:191], v[196:199], v[46:49]
	v_mfma_f32_16x16x32_bf16 v[38:41], v[180:183], v[204:207], v[38:41]
	v_mfma_f32_16x16x32_bf16 v[26:29], v[188:191], v[204:207], v[26:29]
	v_mfma_f32_16x16x32_bf16 v[22:25], v[180:183], v[212:215], v[22:25]
	v_mfma_f32_16x16x32_bf16 v[18:21], v[188:191], v[212:215], v[18:21]
	v_mfma_f32_16x16x32_bf16 v[10:13], v[180:183], v[220:223], v[10:13]
	v_mfma_f32_16x16x32_bf16 v[6:9], v[188:191], v[220:223], v[6:9]
	v_mfma_f32_16x16x32_bf16 v[54:57], v[184:187], v[200:203], v[54:57]
	v_mfma_f32_16x16x32_bf16 v[46:49], v[192:195], v[200:203], v[46:49]
	v_mfma_f32_16x16x32_bf16 v[38:41], v[184:187], v[208:211], v[38:41]
	v_mfma_f32_16x16x32_bf16 v[26:29], v[192:195], v[208:211], v[26:29]
	s_barrier
	v_mfma_f32_16x16x32_bf16 v[22:25], v[184:187], v[216:219], v[22:25]
	v_mfma_f32_16x16x32_bf16 v[18:21], v[192:195], v[216:219], v[18:21]
	v_mfma_f32_16x16x32_bf16 v[10:13], v[184:187], v[224:227], v[10:13]
	v_mfma_f32_16x16x32_bf16 v[6:9], v[192:195], v[224:227], v[6:9]
	s_add_i32 s88, 0, 0x18000
	v_add_u32_e32 v134, s88, v143
	s_add_i32 s89, 0, 0x1c000
	ds_read_b128 v[164:167], v134
	ds_read_b128 v[168:171], v134 offset:1024
	ds_read_b128 v[172:175], v134 offset:2048
	ds_read_b128 v[176:179], v134 offset:3072
	v_add_u32_e32 v134, s89, v143
	ds_read_b128 v[180:183], v134
	ds_read_b128 v[184:187], v134 offset:1024
	ds_read_b128 v[188:191], v134 offset:2048
	ds_read_b128 v[192:195], v134 offset:3072
	s_mov_b32 m0, s73
	ds_read_b128 v[196:199], v147 offset:32768
	ds_read_b128 v[200:203], v147 offset:33792
	ds_read_b128 v[204:207], v147 offset:34816
	ds_read_b128 v[208:211], v147 offset:35840
	ds_read_b128 v[212:215], v147 offset:36864
	ds_read_b128 v[216:219], v147 offset:37888
	ds_read_b128 v[220:223], v147 offset:38912
	ds_read_b128 v[224:227], v147 offset:39936
	global_load_lds_dwordx4 v153, s[58:59]
	s_mov_b32 m0, s74
	s_nop 0
	global_load_lds_dwordx4 v155, s[58:59]
	s_waitcnt vmcnt(8)
	s_waitcnt lgkmcnt(0)
	s_barrier
	v_mfma_f32_16x16x32_bf16 v[126:129], v[164:167], v[196:199], v[126:129]
	v_mfma_f32_16x16x32_bf16 v[122:125], v[172:175], v[196:199], v[122:125]
	v_mfma_f32_16x16x32_bf16 v[110:113], v[164:167], v[204:207], v[110:113]
	v_mfma_f32_16x16x32_bf16 v[106:109], v[172:175], v[204:207], v[106:109]
	v_mfma_f32_16x16x32_bf16 v[94:97], v[164:167], v[212:215], v[94:97]
	v_mfma_f32_16x16x32_bf16 v[90:93], v[172:175], v[212:215], v[90:93]
	v_mfma_f32_16x16x32_bf16 v[78:81], v[164:167], v[220:223], v[78:81]
	v_mfma_f32_16x16x32_bf16 v[74:77], v[172:175], v[220:223], v[74:77]
	v_mfma_f32_16x16x32_bf16 v[126:129], v[168:171], v[200:203], v[126:129]
	v_mfma_f32_16x16x32_bf16 v[122:125], v[176:179], v[200:203], v[122:125]
	v_mfma_f32_16x16x32_bf16 v[110:113], v[168:171], v[208:211], v[110:113]
	v_mfma_f32_16x16x32_bf16 v[106:109], v[176:179], v[208:211], v[106:109]
	v_mfma_f32_16x16x32_bf16 v[94:97], v[168:171], v[216:219], v[94:97]
	v_mfma_f32_16x16x32_bf16 v[90:93], v[176:179], v[216:219], v[90:93]
	v_mfma_f32_16x16x32_bf16 v[78:81], v[168:171], v[224:227], v[78:81]
	v_mfma_f32_16x16x32_bf16 v[74:77], v[176:179], v[224:227], v[74:77]
	v_mfma_f32_16x16x32_bf16 v[118:121], v[180:183], v[196:199], v[118:121]
	v_mfma_f32_16x16x32_bf16 v[114:117], v[188:191], v[196:199], v[114:117]
	v_mfma_f32_16x16x32_bf16 v[102:105], v[180:183], v[204:207], v[102:105]
	v_mfma_f32_16x16x32_bf16 v[98:101], v[188:191], v[204:207], v[98:101]
	v_mfma_f32_16x16x32_bf16 v[86:89], v[180:183], v[212:215], v[86:89]
	v_mfma_f32_16x16x32_bf16 v[82:85], v[188:191], v[212:215], v[82:85]
	v_mfma_f32_16x16x32_bf16 v[70:73], v[180:183], v[220:223], v[70:73]
	v_mfma_f32_16x16x32_bf16 v[66:69], v[188:191], v[220:223], v[66:69]
	v_mfma_f32_16x16x32_bf16 v[118:121], v[184:187], v[200:203], v[118:121]
	v_mfma_f32_16x16x32_bf16 v[114:117], v[192:195], v[200:203], v[114:117]
	v_mfma_f32_16x16x32_bf16 v[102:105], v[184:187], v[208:211], v[102:105]
	v_mfma_f32_16x16x32_bf16 v[98:101], v[192:195], v[208:211], v[98:101]
	s_barrier
; #define PG8_STAGE(bufoff, gbase, voff) do { _Pragma("unroll") for (int _i = 0; _i < 2; ++_i) \
;         __builtin_amdgcn_global_load_lds((const unsigned*)((const char*)(gbase) + (voff)[_i]), (PG8_LAS unsigned*)(lds + (bufoff) + ldsw + _i * 8192), 16, 0, 0); } while (0)
; #define PG8_LDA(dst, b, h) do { _Pragma("unroll") for (int m = 0; m < 4; ++m) _Pragma("unroll") for (int k = 0; k < 2; ++k) dst[m][k] = *(const PG8_LAS bf16x8*)(lds + PG8_SA(b, h) + aoff + m * 2048 + k * 1024); } while (0)
; #define PG8_MMA(ai, bj, At, Bt) do { __builtin_amdgcn_s_setprio(1); _Pragma("unroll") for (int m = 0; m < 4; ++m) _Pragma("unroll") for (int n = 0; n < 2; ++n) _Pragma("unroll") for (int k = 0; k < 2; ++k) \
;         acc[ai][bj][m][n] = __builtin_amdgcn_mfma_f32_16x16x32_bf16(Bt[n][k], At[m][k], acc[ai][bj][m][n], 0, 0, 0); __builtin_amdgcn_s_setprio(0); } while (0)
; #define PG8_WAIT_V(n) asm volatile("s_waitcnt vmcnt(" #n ")" ::: "memory")
; #define PG8_WAIT_L(n) asm volatile("s_waitcnt lgkmcnt(" #n ")" ::: "memory")
; #define PG8_BAR __builtin_amdgcn_s_barrier()
; #define PG8_SCHED __builtin_amdgcn_sched_barrier(0)
; template <class Epi, class Sched, bool ALIGN_EPI = false>
; __device__ __forceinline__ void gemm_phase(PG8_LAS unsigned char* lds, const Gemm g, const Sched& S, const Epi& E) {
;     ...
;             PG8_WAIT_V(8); PG8_WAIT_L(0); PG8_BAR; PG8_MMA(0, 0, At, B0); PG8_MMA(0, 1, At, B1); PG8_BAR; PG8_SCHED;
;             PG8_LDA(At, 1, 1); PG8_STAGE(PG8_SB(1, 0), b3, voffB); PG8_STAGE(PG8_SB(1, 1), b3 + hstep, voffB); PG8_STAGE(PG8_SA(1, 0), a3, w0);
;             PG8_WAIT_V(8); PG8_WAIT_L(0); PG8_BAR; PG8_MMA(1, 0, At, B0); PG8_MMA(1, 1, At, B1); PG8_BAR; PG8_SCHED;
;             if constexpr (Epi::KSCALE) { if (((t + 2) & 7) == 0 && t + 2 < nt) { E.kscale(acc, pf, ((t + 2) >> 3) - 1, wr, fr); PG8_SCHED; } }
;         }
	v_mfma_f32_16x16x32_bf16 v[86:89], v[184:187], v[216:219], v[86:89]
	v_mfma_f32_16x16x32_bf16 v[82:85], v[192:195], v[216:219], v[82:85]
	v_mfma_f32_16x16x32_bf16 v[70:73], v[184:187], v[224:227], v[70:73]
	v_mfma_f32_16x16x32_bf16 v[66:69], v[192:195], v[224:227], v[66:69]
	s_add_i32 s58, s88, s71
	v_lshl_add_u64 v[230:231], v[230:231], 0, s[42:43]
	s_mov_b32 m0, s58
	ds_read_b128 v[196:199], v147 offset:49152
	ds_read_b128 v[200:203], v147 offset:50176
	ds_read_b128 v[204:207], v147 offset:51200
	ds_read_b128 v[208:211], v147 offset:52224
	ds_read_b128 v[212:215], v147 offset:53248
	ds_read_b128 v[216:219], v147 offset:54272
	ds_read_b128 v[220:223], v147 offset:55296
	ds_read_b128 v[224:227], v147 offset:56320
	global_load_lds_dwordx4 v[230:231], off
	s_add_i32 m0, s58, 0x2000
	s_add_u32 s56, s56, 0x80080
	v_lshl_add_u64 v[230:231], v[232:233], 0, s[42:43]
	s_addc_u32 s57, s57, 0
	s_add_i32 s58, s89, s71
	global_load_lds_dwordx4 v[230:231], off
	v_lshl_add_u64 v[230:231], s[56:57], 0, v[130:131]
	s_mov_b32 m0, s58
	v_lshl_add_u64 v[228:229], v[228:229], 0, s[42:43]
	global_load_lds_dwordx4 v[230:231], off
	v_lshl_add_u64 v[230:231], s[56:57], 0, v[132:133]
	s_add_i32 m0, s58, 0x2000
	s_nop 0
	global_load_lds_dwordx4 v[230:231], off
	v_lshl_add_u64 v[230:231], v[234:235], 0, s[42:43]
	s_mov_b32 m0, s77
	s_nop 0
	global_load_lds_dwordx4 v[230:231], off
	s_mov_b32 m0, s78
	s_nop 0
	global_load_lds_dwordx4 v[228:229], off
	s_waitcnt vmcnt(8)
	s_waitcnt lgkmcnt(0)
	s_barrier
	v_mfma_f32_16x16x32_bf16 v[62:65], v[164:167], v[196:199], v[62:65]
	v_mfma_f32_16x16x32_bf16 v[58:61], v[172:175], v[196:199], v[58:61]
	v_mfma_f32_16x16x32_bf16 v[50:53], v[164:167], v[204:207], v[50:53]
	v_mfma_f32_16x16x32_bf16 v[42:45], v[172:175], v[204:207], v[42:45]
	v_mfma_f32_16x16x32_bf16 v[34:37], v[164:167], v[212:215], v[34:37]
	v_mfma_f32_16x16x32_bf16 v[30:33], v[172:175], v[212:215], v[30:33]
	v_mfma_f32_16x16x32_bf16 v[14:17], v[164:167], v[220:223], v[14:17]
	v_mfma_f32_16x16x32_bf16 v[2:5], v[172:175], v[220:223], v[2:5]
	v_mfma_f32_16x16x32_bf16 v[62:65], v[168:171], v[200:203], v[62:65]
	v_mfma_f32_16x16x32_bf16 v[58:61], v[176:179], v[200:203], v[58:61]
	v_mfma_f32_16x16x32_bf16 v[50:53], v[168:171], v[208:211], v[50:53]
	v_mfma_f32_16x16x32_bf16 v[42:45], v[176:179], v[208:211], v[42:45]
	v_mfma_f32_16x16x32_bf16 v[34:37], v[168:171], v[216:219], v[34:37]
	v_mfma_f32_16x16x32_bf16 v[30:33], v[176:179], v[216:219], v[30:33]
	v_mfma_f32_16x16x32_bf16 v[14:17], v[168:171], v[224:227], v[14:17]
	v_mfma_f32_16x16x32_bf16 v[2:5], v[176:179], v[224:227], v[2:5]
	v_mfma_f32_16x16x32_bf16 v[54:57], v[180:183], v[196:199], v[54:57]
	v_mfma_f32_16x16x32_bf16 v[46:49], v[188:191], v[196:199], v[46:49]
	v_mfma_f32_16x16x32_bf16 v[38:41], v[180:183], v[204:207], v[38:41]
	v_mfma_f32_16x16x32_bf16 v[26:29], v[188:191], v[204:207], v[26:29]
	v_mfma_f32_16x16x32_bf16 v[22:25], v[180:183], v[212:215], v[22:25]
	v_mfma_f32_16x16x32_bf16 v[18:21], v[188:191], v[212:215], v[18:21]
	v_mfma_f32_16x16x32_bf16 v[10:13], v[180:183], v[220:223], v[10:13]
	v_mfma_f32_16x16x32_bf16 v[6:9], v[188:191], v[220:223], v[6:9]
	v_mfma_f32_16x16x32_bf16 v[54:57], v[184:187], v[200:203], v[54:57]
	v_mfma_f32_16x16x32_bf16 v[46:49], v[192:195], v[200:203], v[46:49]
	v_mfma_f32_16x16x32_bf16 v[38:41], v[184:187], v[208:211], v[38:41]
	v_mfma_f32_16x16x32_bf16 v[26:29], v[192:195], v[208:211], v[26:29]
	s_barrier
	v_mfma_f32_16x16x32_bf16 v[22:25], v[184:187], v[216:219], v[22:25]
	v_mfma_f32_16x16x32_bf16 v[18:21], v[192:195], v[216:219], v[18:21]
	v_mfma_f32_16x16x32_bf16 v[10:13], v[184:187], v[224:227], v[10:13]
	v_mfma_f32_16x16x32_bf16 v[6:9], v[192:195], v[224:227], v[6:9]
	s_add_i32 s87, s87, 2
	s_add_u32 s54, s54, 0x100
	s_addc_u32 s55, s55, 0
	s_cmp_gt_u32 s87, 29
	s_cbranch_scc0 .LBB0_1414
	s_and_b64 vcc, exec, s[44:45]
	s_cbranch_vccz .LBB0_1417
	s_barrier

; #define PG8_STAGE(bufoff, gbase, voff) do { _Pragma("unroll") for (int _i = 0; _i < 2; ++_i) \
;         __builtin_amdgcn_global_load_lds((const unsigned*)((const char*)(gbase) + (voff)[_i]), (PG8_LAS unsigned*)(lds + (bufoff) + ldsw + _i * 8192), 16, 0, 0); } while (0)
; #define PG8_LDA(dst, b, h) do { _Pragma("unroll") for (int m = 0; m < 4; ++m) _Pragma("unroll") for (int k = 0; k < 2; ++k) dst[m][k] = *(const PG8_LAS bf16x8*)(lds + PG8_SA(b, h) + aoff + m * 2048 + k * 1024); } while (0)
; #define PG8_LDB(dst, b, h) do { _Pragma("unroll") for (int n = 0; n < 2; ++n) _Pragma("unroll") for (int k = 0; k < 2; ++k) dst[n][k] = *(const PG8_LAS bf16x8*)(lds + PG8_SB(b, h) + boff + n * 2048 + k * 1024); } while (0)
; #define PG8_MMA(ai, bj, At, Bt) do { __builtin_amdgcn_s_setprio(1); _Pragma("unroll") for (int m = 0; m < 4; ++m) _Pragma("unroll") for (int n = 0; n < 2; ++n) _Pragma("unroll") for (int k = 0; k < 2; ++k) \
;         acc[ai][bj][m][n] = __builtin_amdgcn_mfma_f32_16x16x32_bf16(Bt[n][k], At[m][k], acc[ai][bj][m][n], 0, 0, 0); __builtin_amdgcn_s_setprio(0); } while (0)
; #define PG8_BAR __builtin_amdgcn_s_barrier()
; template <class Epi, class Sched, bool ALIGN_EPI = false>
; __device__ __forceinline__ void gemm_phase(PG8_LAS unsigned char* lds, const Gemm g, const Sched& S, const Epi& E) {
;     ...
;             const bool last = (t == nt - 2);
;             const char* a1 = cA + (size_t)(t + 1) * kstep;
;             const char* a2 = last ? nA : cA + (size_t)(t + 2) * kstep; const char* b2 = last ? nB : cB + (size_t)(t + 2) * kstep;
;             const char* a3 = a2 + kstep; const char* b3 = b2 + kstep;
;             unsigned w0[2], w1[2];
; #pragma unroll
;             for (int i = 0; i < 2; ++i) { w0[i] = (Sched::GATHER && last) ? vn0[i] : vc0[i]; w1[i] = (Sched::GATHER && last) ? vn1[i] : vc1[i]; }
;             if (last && has_next) S.a_ready(nxt);
;             PG8_LDB(B0, 0, 0); PG8_LDB(B1, 0, 1); PG8_SCHED; PG8_LDA(At, 0, 0); PG8_STAGE(PG8_SA(1, 1), a1 + hstepA, vc1);
;             PG8_WAIT_V(8); PG8_WAIT_L(0); PG8_BAR; PG8_MMA(0, 0, At, B0); PG8_MMA(0, 1, At, B1); PG8_BAR; PG8_SCHED;
;             PG8_LDA(At, 0, 1); PG8_STAGE(PG8_SB(0, 0), b2, voffB); PG8_STAGE(PG8_SB(0, 1), b2 + hstep, voffB); PG8_STAGE(PG8_SA(0, 0), a2, w0);
;             PG8_WAIT_V(8); PG8_WAIT_L(0); PG8_BAR; PG8_MMA(1, 0, At, B0); PG8_MMA(1, 1, At, B1); PG8_BAR; PG8_SCHED;
.LBB0_1480:
	ds_read_b128 v[172:175], v167
	ds_read_b128 v[176:179], v167 offset:1024
	ds_read_b128 v[180:183], v167 offset:2048
	ds_read_b128 v[184:187], v167 offset:3072
	ds_read_b128 v[188:191], v168
	ds_read_b128 v[192:195], v168 offset:1024
	ds_read_b128 v[196:199], v168 offset:2048
	ds_read_b128 v[200:203], v168 offset:3072
	s_add_u32 s16, s14, 0x3c800100
	s_addc_u32 s17, s15, 0
	s_add_u32 s56, s14, s43
	s_addc_u32 s57, s15, s44
	s_cmp_eq_u32 s45, 28
	s_cselect_b32 s19, s21, s17
	s_cselect_b32 s18, s20, s16
	s_cselect_b32 s17, s11, s57
	s_cselect_b32 s16, s10, s56
	s_mov_b32 m0, s46
	v_lshl_add_u64 v[236:237], s[14:15], 0, v[160:161]
	ds_read_b128 v[204:207], v169
	ds_read_b128 v[208:211], v169 offset:1024
	ds_read_b128 v[212:215], v169 offset:2048
	ds_read_b128 v[216:219], v169 offset:3072
	ds_read_b128 v[220:223], v169 offset:4096
	ds_read_b128 v[224:227], v169 offset:5120
	ds_read_b128 v[228:231], v169 offset:6144
	ds_read_b128 v[232:235], v169 offset:7168
	global_load_lds_dwordx4 v[236:237], off
	v_lshl_add_u64 v[236:237], s[14:15], 0, v[158:159]
	s_mov_b32 m0, s47
	s_nop 0
	global_load_lds_dwordx4 v[236:237], off
	s_waitcnt vmcnt(8)
	s_waitcnt lgkmcnt(0)
	s_barrier
	v_mfma_f32_16x16x32_bf16 v[126:129], v[172:175], v[204:207], v[126:129]
	v_mfma_f32_16x16x32_bf16 v[122:125], v[180:183], v[204:207], v[122:125]
	v_mfma_f32_16x16x32_bf16 v[110:113], v[172:175], v[212:215], v[110:113]
	v_mfma_f32_16x16x32_bf16 v[106:109], v[180:183], v[212:215], v[106:109]
	v_mfma_f32_16x16x32_bf16 v[94:97], v[172:175], v[220:223], v[94:97]
	v_mfma_f32_16x16x32_bf16 v[90:93], v[180:183], v[220:223], v[90:93]
	v_mfma_f32_16x16x32_bf16 v[78:81], v[172:175], v[228:231], v[78:81]
	v_mfma_f32_16x16x32_bf16 v[74:77], v[180:183], v[228:231], v[74:77]
	v_mfma_f32_16x16x32_bf16 v[126:129], v[176:179], v[208:211], v[126:129]
	v_mfma_f32_16x16x32_bf16 v[122:125], v[184:187], v[208:211], v[122:125]
	v_mfma_f32_16x16x32_bf16 v[110:113], v[176:179], v[216:219], v[110:113]
	v_mfma_f32_16x16x32_bf16 v[106:109], v[184:187], v[216:219], v[106:109]
	v_mfma_f32_16x16x32_bf16 v[94:97], v[176:179], v[224:227], v[94:97]
	v_mfma_f32_16x16x32_bf16 v[90:93], v[184:187], v[224:227], v[90:93]
	v_mfma_f32_16x16x32_bf16 v[78:81], v[176:179], v[232:235], v[78:81]
	v_mfma_f32_16x16x32_bf16 v[74:77], v[184:187], v[232:235], v[74:77]
	v_mfma_f32_16x16x32_bf16 v[118:121], v[188:191], v[204:207], v[118:121]
	v_mfma_f32_16x16x32_bf16 v[114:117], v[196:199], v[204:207], v[114:117]
	v_mfma_f32_16x16x32_bf16 v[102:105], v[188:191], v[212:215], v[102:105]
	v_mfma_f32_16x16x32_bf16 v[98:101], v[196:199], v[212:215], v[98:101]
	v_mfma_f32_16x16x32_bf16 v[86:89], v[188:191], v[220:223], v[86:89]
	v_mfma_f32_16x16x32_bf16 v[82:85], v[196:199], v[220:223], v[82:85]
	v_mfma_f32_16x16x32_bf16 v[70:73], v[188:191], v[228:231], v[70:73]
	v_mfma_f32_16x16x32_bf16 v[66:69], v[196:199], v[228:231], v[66:69]
	v_mfma_f32_16x16x32_bf16 v[118:121], v[192:195], v[208:211], v[118:121]
	v_mfma_f32_16x16x32_bf16 v[114:117], v[200:203], v[208:211], v[114:117]
	v_mfma_f32_16x16x32_bf16 v[102:105], v[192:195], v[216:219], v[102:105]
	v_mfma_f32_16x16x32_bf16 v[98:101], v[200:203], v[216:219], v[98:101]
	s_barrier
	v_mfma_f32_16x16x32_bf16 v[86:89], v[192:195], v[224:227], v[86:89]
	v_mfma_f32_16x16x32_bf16 v[82:85], v[200:203], v[224:227], v[82:85]
	v_mfma_f32_16x16x32_bf16 v[70:73], v[192:195], v[232:235], v[70:73]
	v_mfma_f32_16x16x32_bf16 v[66:69], v[200:203], v[232:235], v[66:69]
	s_mov_b32 m0, s48
	v_lshl_add_u64 v[236:237], s[16:17], 0, v[146:147]
	s_add_u32 s56, s16, 0x80000
	ds_read_b128 v[204:207], v169 offset:16384
	ds_read_b128 v[208:211], v169 offset:17408
	ds_read_b128 v[212:215], v169 offset:18432
	ds_read_b128 v[216:219], v169 offset:19456
	ds_read_b128 v[220:223], v169 offset:20480
	ds_read_b128 v[224:227], v169 offset:21504
	ds_read_b128 v[228:231], v169 offset:22528
	ds_read_b128 v[232:235], v169 offset:23552
	global_load_lds_dwordx4 v[236:237], off
	v_lshl_add_u64 v[238:239], s[16:17], 0, v[144:145]
	s_mov_b32 m0, s49
	s_addc_u32 s57, s17, 0
	global_load_lds_dwordx4 v[238:239], off
	v_lshl_add_u64 v[240:241], s[56:57], 0, v[146:147]
	s_mov_b32 m0, s50
	v_lshl_add_u64 v[242:243], s[18:19], 0, v[150:151]
	global_load_lds_dwordx4 v[240:241], off
	v_lshl_add_u64 v[240:241], s[56:57], 0, v[144:145]
	s_mov_b32 m0, s51
	s_nop 0
	global_load_lds_dwordx4 v[240:241], off
	v_lshl_add_u64 v[240:241], s[18:19], 0, v[148:149]
	s_mov_b32 m0, s25
	s_nop 0
	global_load_lds_dwordx4 v[240:241], off
	s_mov_b32 m0, s26
	s_nop 0
	global_load_lds_dwordx4 v[242:243], off
	s_waitcnt vmcnt(8)
	s_waitcnt lgkmcnt(0)
	s_barrier
	v_mfma_f32_16x16x32_bf16 v[62:65], v[172:175], v[204:207], v[62:65]
	v_mfma_f32_16x16x32_bf16 v[58:61], v[180:183], v[204:207], v[58:61]
	v_mfma_f32_16x16x32_bf16 v[50:53], v[172:175], v[212:215], v[50:53]
	v_mfma_f32_16x16x32_bf16 v[42:45], v[180:183], v[212:215], v[42:45]
	v_mfma_f32_16x16x32_bf16 v[34:37], v[172:175], v[220:223], v[34:37]
	v_mfma_f32_16x16x32_bf16 v[26:29], v[180:183], v[220:223], v[26:29]
	v_mfma_f32_16x16x32_bf16 v[14:17], v[172:175], v[228:231], v[14:17]
	v_mfma_f32_16x16x32_bf16 v[2:5], v[180:183], v[228:231], v[2:5]
	v_mfma_f32_16x16x32_bf16 v[62:65], v[176:179], v[208:211], v[62:65]
	v_mfma_f32_16x16x32_bf16 v[58:61], v[184:187], v[208:211], v[58:61]
	v_mfma_f32_16x16x32_bf16 v[50:53], v[176:179], v[216:219], v[50:53]
	v_mfma_f32_16x16x32_bf16 v[42:45], v[184:187], v[216:219], v[42:45]
	v_mfma_f32_16x16x32_bf16 v[34:37], v[176:179], v[224:227], v[34:37]
	v_mfma_f32_16x16x32_bf16 v[26:29], v[184:187], v[224:227], v[26:29]
	v_mfma_f32_16x16x32_bf16 v[14:17], v[176:179], v[232:235], v[14:17]
	v_mfma_f32_16x16x32_bf16 v[2:5], v[184:187], v[232:235], v[2:5]
	v_mfma_f32_16x16x32_bf16 v[54:57], v[188:191], v[204:207], v[54:57]
	v_mfma_f32_16x16x32_bf16 v[46:49], v[196:199], v[204:207], v[46:49]
	v_mfma_f32_16x16x32_bf16 v[38:41], v[188:191], v[212:215], v[38:41]
	v_mfma_f32_16x16x32_bf16 v[30:33], v[196:199], v[212:215], v[30:33]
	v_mfma_f32_16x16x32_bf16 v[22:25], v[188:191], v[220:223], v[22:25]
	v_mfma_f32_16x16x32_bf16 v[18:21], v[196:199], v[220:223], v[18:21]
	v_mfma_f32_16x16x32_bf16 v[10:13], v[188:191], v[228:231], v[10:13]
	v_mfma_f32_16x16x32_bf16 v[6:9], v[196:199], v[228:231], v[6:9]
	v_mfma_f32_16x16x32_bf16 v[54:57], v[192:195], v[208:211], v[54:57]
	v_mfma_f32_16x16x32_bf16 v[46:49], v[200:203], v[208:211], v[46:49]
	v_mfma_f32_16x16x32_bf16 v[38:41], v[192:195], v[216:219], v[38:41]
	v_mfma_f32_16x16x32_bf16 v[30:33], v[200:203], v[216:219], v[30:33]
	s_barrier
; #define PG8_STAGE(bufoff, gbase, voff) do { _Pragma("unroll") for (int _i = 0; _i < 2; ++_i) \
;         __builtin_amdgcn_global_load_lds((const unsigned*)((const char*)(gbase) + (voff)[_i]), (PG8_LAS unsigned*)(lds + (bufoff) + ldsw + _i * 8192), 16, 0, 0); } while (0)
; #define PG8_LDA(dst, b, h) do { _Pragma("unroll") for (int m = 0; m < 4; ++m) _Pragma("unroll") for (int k = 0; k < 2; ++k) dst[m][k] = *(const PG8_LAS bf16x8*)(lds + PG8_SA(b, h) + aoff + m * 2048 + k * 1024); } while (0)
; #define PG8_LDB(dst, b, h) do { _Pragma("unroll") for (int n = 0; n < 2; ++n) _Pragma("unroll") for (int k = 0; k < 2; ++k) dst[n][k] = *(const PG8_LAS bf16x8*)(lds + PG8_SB(b, h) + boff + n * 2048 + k * 1024); } while (0)
; #define PG8_MMA(ai, bj, At, Bt) do { __builtin_amdgcn_s_setprio(1); _Pragma("unroll") for (int m = 0; m < 4; ++m) _Pragma("unroll") for (int n = 0; n < 2; ++n) _Pragma("unroll") for (int k = 0; k < 2; ++k) \
;         acc[ai][bj][m][n] = __builtin_amdgcn_mfma_f32_16x16x32_bf16(Bt[n][k], At[m][k], acc[ai][bj][m][n], 0, 0, 0); __builtin_amdgcn_s_setprio(0); } while (0)
; #define PG8_WAIT_V(n) asm volatile("s_waitcnt vmcnt(" #n ")" ::: "memory")
; #define PG8_WAIT_L(n) asm volatile("s_waitcnt lgkmcnt(" #n ")" ::: "memory")
; #define PG8_BAR __builtin_amdgcn_s_barrier()
; #define PG8_SCHED __builtin_amdgcn_sched_barrier(0)
; template <class Epi, class Sched, bool ALIGN_EPI = false>
; __device__ __forceinline__ void gemm_phase(PG8_LAS unsigned char* lds, const Gemm g, const Sched& S, const Epi& E) {
;     ...
;             PG8_WAIT_V(8); PG8_WAIT_L(0); PG8_BAR; PG8_MMA(1, 0, At, B0); PG8_MMA(1, 1, At, B1); PG8_BAR; PG8_SCHED;
;             PG8_LDB(B0, 1, 0); PG8_LDB(B1, 1, 1); PG8_SCHED; PG8_LDA(At, 1, 0); PG8_STAGE(PG8_SA(0, 1), a2 + hstepA, w1);
;             PG8_WAIT_V(8); PG8_WAIT_L(0); PG8_BAR; PG8_MMA(0, 0, At, B0); PG8_MMA(0, 1, At, B1); PG8_BAR; PG8_SCHED;
	v_mfma_f32_16x16x32_bf16 v[22:25], v[192:195], v[224:227], v[22:25]
	v_mfma_f32_16x16x32_bf16 v[18:21], v[200:203], v[224:227], v[18:21]
	v_mfma_f32_16x16x32_bf16 v[10:13], v[192:195], v[232:235], v[10:13]
	v_mfma_f32_16x16x32_bf16 v[6:9], v[200:203], v[232:235], v[6:9]
	ds_read_b128 v[172:175], v170
	ds_read_b128 v[176:179], v170 offset:1024
	ds_read_b128 v[180:183], v170 offset:2048
	ds_read_b128 v[184:187], v170 offset:3072
	ds_read_b128 v[188:191], v171
	ds_read_b128 v[192:195], v171 offset:1024
	ds_read_b128 v[196:199], v171 offset:2048
	ds_read_b128 v[200:203], v171 offset:3072
	s_mov_b32 m0, s27
	v_lshl_add_u64 v[244:245], s[18:19], 0, v[152:153]
	ds_read_b128 v[204:207], v169 offset:32768
	ds_read_b128 v[208:211], v169 offset:33792
	ds_read_b128 v[212:215], v169 offset:34816
	ds_read_b128 v[216:219], v169 offset:35840
	ds_read_b128 v[220:223], v169 offset:36864
	ds_read_b128 v[224:227], v169 offset:37888
	ds_read_b128 v[228:231], v169 offset:38912
	ds_read_b128 v[232:235], v169 offset:39936
	global_load_lds_dwordx4 v[244:245], off
	v_lshl_add_u64 v[244:245], s[18:19], 0, v[154:155]
	s_mov_b32 m0, s35
	s_nop 0
	global_load_lds_dwordx4 v[244:245], off
	s_waitcnt vmcnt(8)
	s_waitcnt lgkmcnt(0)
	s_barrier
	v_mfma_f32_16x16x32_bf16 v[126:129], v[172:175], v[204:207], v[126:129]
	v_mfma_f32_16x16x32_bf16 v[122:125], v[180:183], v[204:207], v[122:125]
	v_mfma_f32_16x16x32_bf16 v[110:113], v[172:175], v[212:215], v[110:113]
	v_mfma_f32_16x16x32_bf16 v[106:109], v[180:183], v[212:215], v[106:109]
	v_mfma_f32_16x16x32_bf16 v[94:97], v[172:175], v[220:223], v[94:97]
	v_mfma_f32_16x16x32_bf16 v[90:93], v[180:183], v[220:223], v[90:93]
	v_mfma_f32_16x16x32_bf16 v[78:81], v[172:175], v[228:231], v[78:81]
	v_mfma_f32_16x16x32_bf16 v[74:77], v[180:183], v[228:231], v[74:77]
	v_mfma_f32_16x16x32_bf16 v[126:129], v[176:179], v[208:211], v[126:129]
	v_mfma_f32_16x16x32_bf16 v[122:125], v[184:187], v[208:211], v[122:125]
	v_mfma_f32_16x16x32_bf16 v[110:113], v[176:179], v[216:219], v[110:113]
	v_mfma_f32_16x16x32_bf16 v[106:109], v[184:187], v[216:219], v[106:109]
	v_mfma_f32_16x16x32_bf16 v[94:97], v[176:179], v[224:227], v[94:97]
	v_mfma_f32_16x16x32_bf16 v[90:93], v[184:187], v[224:227], v[90:93]
	v_mfma_f32_16x16x32_bf16 v[78:81], v[176:179], v[232:235], v[78:81]
	v_mfma_f32_16x16x32_bf16 v[74:77], v[184:187], v[232:235], v[74:77]
	v_mfma_f32_16x16x32_bf16 v[118:121], v[188:191], v[204:207], v[118:121]
	v_mfma_f32_16x16x32_bf16 v[114:117], v[196:199], v[204:207], v[114:117]
	v_mfma_f32_16x16x32_bf16 v[102:105], v[188:191], v[212:215], v[102:105]
	v_mfma_f32_16x16x32_bf16 v[98:101], v[196:199], v[212:215], v[98:101]
	v_mfma_f32_16x16x32_bf16 v[86:89], v[188:191], v[220:223], v[86:89]
	v_mfma_f32_16x16x32_bf16 v[82:85], v[196:199], v[220:223], v[82:85]
	v_mfma_f32_16x16x32_bf16 v[70:73], v[188:191], v[228:231], v[70:73]
	v_mfma_f32_16x16x32_bf16 v[66:69], v[196:199], v[228:231], v[66:69]
	v_mfma_f32_16x16x32_bf16 v[118:121], v[192:195], v[208:211], v[118:121]
	v_mfma_f32_16x16x32_bf16 v[114:117], v[200:203], v[208:211], v[114:117]
	v_mfma_f32_16x16x32_bf16 v[102:105], v[192:195], v[216:219], v[102:105]
	v_mfma_f32_16x16x32_bf16 v[98:101], v[200:203], v[216:219], v[98:101]
	s_barrier
; #define PG8_STAGE(bufoff, gbase, voff) do { _Pragma("unroll") for (int _i = 0; _i < 2; ++_i) \
;         __builtin_amdgcn_global_load_lds((const unsigned*)((const char*)(gbase) + (voff)[_i]), (PG8_LAS unsigned*)(lds + (bufoff) + ldsw + _i * 8192), 16, 0, 0); } while (0)
; #define PG8_LDA(dst, b, h) do { _Pragma("unroll") for (int m = 0; m < 4; ++m) _Pragma("unroll") for (int k = 0; k < 2; ++k) dst[m][k] = *(const PG8_LAS bf16x8*)(lds + PG8_SA(b, h) + aoff + m * 2048 + k * 1024); } while (0)
; #define PG8_MMA(ai, bj, At, Bt) do { __builtin_amdgcn_s_setprio(1); _Pragma("unroll") for (int m = 0; m < 4; ++m) _Pragma("unroll") for (int n = 0; n < 2; ++n) _Pragma("unroll") for (int k = 0; k < 2; ++k) \
;         acc[ai][bj][m][n] = __builtin_amdgcn_mfma_f32_16x16x32_bf16(Bt[n][k], At[m][k], acc[ai][bj][m][n], 0, 0, 0); __builtin_amdgcn_s_setprio(0); } while (0)
; #define PG8_WAIT_V(n) asm volatile("s_waitcnt vmcnt(" #n ")" ::: "memory")
; #define PG8_WAIT_L(n) asm volatile("s_waitcnt lgkmcnt(" #n ")" ::: "memory")
; #define PG8_BAR __builtin_amdgcn_s_barrier()
; #define PG8_SCHED __builtin_amdgcn_sched_barrier(0)
; template <class Epi, class Sched, bool ALIGN_EPI = false>
; __device__ __forceinline__ void gemm_phase(PG8_LAS unsigned char* lds, const Gemm g, const Sched& S, const Epi& E) {
;     ...
;             PG8_WAIT_V(8); PG8_WAIT_L(0); PG8_BAR; PG8_MMA(0, 0, At, B0); PG8_MMA(0, 1, At, B1); PG8_BAR; PG8_SCHED;
;             PG8_LDA(At, 1, 1); PG8_STAGE(PG8_SB(1, 0), b3, voffB); PG8_STAGE(PG8_SB(1, 1), b3 + hstep, voffB); PG8_STAGE(PG8_SA(1, 0), a3, w0);
;             PG8_WAIT_V(8); PG8_WAIT_L(0); PG8_BAR; PG8_MMA(1, 0, At, B0); PG8_MMA(1, 1, At, B1); PG8_BAR; PG8_SCHED;
;             if constexpr (Epi::KSCALE) { if (((t + 2) & 7) == 0 && t + 2 < nt) { E.kscale(acc, pf, ((t + 2) >> 3) - 1, wr, fr); PG8_SCHED; } }
;         }
	v_mfma_f32_16x16x32_bf16 v[86:89], v[192:195], v[224:227], v[86:89]
	v_mfma_f32_16x16x32_bf16 v[82:85], v[200:203], v[224:227], v[82:85]
	v_mfma_f32_16x16x32_bf16 v[70:73], v[192:195], v[232:235], v[70:73]
	v_mfma_f32_16x16x32_bf16 v[66:69], v[200:203], v[232:235], v[66:69]
	s_mov_b32 m0, s52
	v_lshl_add_u64 v[236:237], v[236:237], 0, s[12:13]
	s_add_u32 s16, s16, 0x80080
	ds_read_b128 v[204:207], v169 offset:49152
	ds_read_b128 v[208:211], v169 offset:50176
	ds_read_b128 v[212:215], v169 offset:51200
	ds_read_b128 v[216:219], v169 offset:52224
	ds_read_b128 v[220:223], v169 offset:53248
	ds_read_b128 v[224:227], v169 offset:54272
	ds_read_b128 v[228:231], v169 offset:55296
	ds_read_b128 v[232:235], v169 offset:56320
	global_load_lds_dwordx4 v[236:237], off
	v_lshl_add_u64 v[236:237], v[238:239], 0, s[12:13]
	s_mov_b32 m0, s53
	s_addc_u32 s17, s17, 0
	global_load_lds_dwordx4 v[236:237], off
	v_lshl_add_u64 v[236:237], s[16:17], 0, v[146:147]
	s_mov_b32 m0, s54
	s_nop 0
	global_load_lds_dwordx4 v[236:237], off
	v_lshl_add_u64 v[236:237], s[16:17], 0, v[144:145]
	s_mov_b32 m0, s55
	s_nop 0
	global_load_lds_dwordx4 v[236:237], off
	v_lshl_add_u64 v[236:237], v[240:241], 0, s[12:13]
	s_mov_b32 m0, s41
	s_nop 0
	global_load_lds_dwordx4 v[236:237], off
	v_lshl_add_u64 v[236:237], v[242:243], 0, s[12:13]
	s_mov_b32 m0, s42
	s_nop 0
	global_load_lds_dwordx4 v[236:237], off
	s_waitcnt vmcnt(8)
	s_waitcnt lgkmcnt(0)
	s_barrier
	v_mfma_f32_16x16x32_bf16 v[62:65], v[172:175], v[204:207], v[62:65]
	v_mfma_f32_16x16x32_bf16 v[58:61], v[180:183], v[204:207], v[58:61]
	v_mfma_f32_16x16x32_bf16 v[50:53], v[172:175], v[212:215], v[50:53]
	v_mfma_f32_16x16x32_bf16 v[42:45], v[180:183], v[212:215], v[42:45]
	v_mfma_f32_16x16x32_bf16 v[34:37], v[172:175], v[220:223], v[34:37]
	v_mfma_f32_16x16x32_bf16 v[26:29], v[180:183], v[220:223], v[26:29]
	v_mfma_f32_16x16x32_bf16 v[14:17], v[172:175], v[228:231], v[14:17]
	v_mfma_f32_16x16x32_bf16 v[2:5], v[180:183], v[228:231], v[2:5]
	v_mfma_f32_16x16x32_bf16 v[62:65], v[176:179], v[208:211], v[62:65]
	v_mfma_f32_16x16x32_bf16 v[58:61], v[184:187], v[208:211], v[58:61]
	v_mfma_f32_16x16x32_bf16 v[50:53], v[176:179], v[216:219], v[50:53]
	v_mfma_f32_16x16x32_bf16 v[42:45], v[184:187], v[216:219], v[42:45]
	v_mfma_f32_16x16x32_bf16 v[34:37], v[176:179], v[224:227], v[34:37]
	v_mfma_f32_16x16x32_bf16 v[26:29], v[184:187], v[224:227], v[26:29]
	v_mfma_f32_16x16x32_bf16 v[14:17], v[176:179], v[232:235], v[14:17]
	v_mfma_f32_16x16x32_bf16 v[2:5], v[184:187], v[232:235], v[2:5]
	v_mfma_f32_16x16x32_bf16 v[54:57], v[188:191], v[204:207], v[54:57]
	v_mfma_f32_16x16x32_bf16 v[46:49], v[196:199], v[204:207], v[46:49]
	v_mfma_f32_16x16x32_bf16 v[38:41], v[188:191], v[212:215], v[38:41]
	v_mfma_f32_16x16x32_bf16 v[30:33], v[196:199], v[212:215], v[30:33]
	v_mfma_f32_16x16x32_bf16 v[22:25], v[188:191], v[220:223], v[22:25]
	v_mfma_f32_16x16x32_bf16 v[18:21], v[196:199], v[220:223], v[18:21]
	v_mfma_f32_16x16x32_bf16 v[10:13], v[188:191], v[228:231], v[10:13]
	v_mfma_f32_16x16x32_bf16 v[6:9], v[196:199], v[228:231], v[6:9]
	v_mfma_f32_16x16x32_bf16 v[54:57], v[192:195], v[208:211], v[54:57]
	v_mfma_f32_16x16x32_bf16 v[46:49], v[200:203], v[208:211], v[46:49]
	v_mfma_f32_16x16x32_bf16 v[38:41], v[192:195], v[216:219], v[38:41]
	v_mfma_f32_16x16x32_bf16 v[30:33], v[200:203], v[216:219], v[30:33]
	s_barrier
	v_mfma_f32_16x16x32_bf16 v[22:25], v[192:195], v[224:227], v[22:25]
	v_mfma_f32_16x16x32_bf16 v[18:21], v[200:203], v[224:227], v[18:21]
	v_mfma_f32_16x16x32_bf16 v[10:13], v[192:195], v[232:235], v[10:13]
	v_mfma_f32_16x16x32_bf16 v[6:9], v[200:203], v[232:235], v[6:9]
	s_add_i32 s45, s45, 2
	s_add_u32 s14, s14, 0x100
	s_addc_u32 s15, s15, 0
	s_cmp_gt_u32 s45, 29
	s_cbranch_scc0 .LBB0_1480
	s_cmpk_lt_u32 s22, 0x100
	s_cbranch_scc0 .LBB0_1483
	s_barrier

; #define PG8_STAGE(bufoff, gbase, voff) do { _Pragma("unroll") for (int _i = 0; _i < 2; ++_i) \
;         __builtin_amdgcn_global_load_lds((const unsigned*)((const char*)(gbase) + (voff)[_i]), (PG8_LAS unsigned*)(lds + (bufoff) + ldsw + _i * 8192), 16, 0, 0); } while (0)
; #define PG8_LDA(dst, b, h) do { _Pragma("unroll") for (int m = 0; m < 4; ++m) _Pragma("unroll") for (int k = 0; k < 2; ++k) dst[m][k] = *(const PG8_LAS bf16x8*)(lds + PG8_SA(b, h) + aoff + m * 2048 + k * 1024); } while (0)
; #define PG8_LDB(dst, b, h) do { _Pragma("unroll") for (int n = 0; n < 2; ++n) _Pragma("unroll") for (int k = 0; k < 2; ++k) dst[n][k] = *(const PG8_LAS bf16x8*)(lds + PG8_SB(b, h) + boff + n * 2048 + k * 1024); } while (0)
; #define PG8_MMA(ai, bj, At, Bt) do { __builtin_amdgcn_s_setprio(1); _Pragma("unroll") for (int m = 0; m < 4; ++m) _Pragma("unroll") for (int n = 0; n < 2; ++n) _Pragma("unroll") for (int k = 0; k < 2; ++k) \
;         acc[ai][bj][m][n] = __builtin_amdgcn_mfma_f32_16x16x32_bf16(Bt[n][k], At[m][k], acc[ai][bj][m][n], 0, 0, 0); __builtin_amdgcn_s_setprio(0); } while (0)
; #define PG8_BAR __builtin_amdgcn_s_barrier()
; template <class Epi, class Sched, bool ALIGN_EPI = false>
; __device__ __forceinline__ void gemm_phase(PG8_LAS unsigned char* lds, const Gemm g, const Sched& S, const Epi& E) {
;     ...
;             const bool last = (t == nt - 2);
;             const char* a1 = cA + (size_t)(t + 1) * kstep;
;             const char* a2 = last ? nA : cA + (size_t)(t + 2) * kstep; const char* b2 = last ? nB : cB + (size_t)(t + 2) * kstep;
;             const char* a3 = a2 + kstep; const char* b3 = b2 + kstep;
;             unsigned w0[2], w1[2];
; #pragma unroll
;             for (int i = 0; i < 2; ++i) { w0[i] = (Sched::GATHER && last) ? vn0[i] : vc0[i]; w1[i] = (Sched::GATHER && last) ? vn1[i] : vc1[i]; }
;             if (last && has_next) S.a_ready(nxt);
;             PG8_LDB(B0, 0, 0); PG8_LDB(B1, 0, 1); PG8_SCHED; PG8_LDA(At, 0, 0); PG8_STAGE(PG8_SA(1, 1), a1 + hstepA, vc1);
;             PG8_WAIT_V(8); PG8_WAIT_L(0); PG8_BAR; PG8_MMA(0, 0, At, B0); PG8_MMA(0, 1, At, B1); PG8_BAR; PG8_SCHED;
;             PG8_LDA(At, 0, 1); PG8_STAGE(PG8_SB(0, 0), b2, voffB); PG8_STAGE(PG8_SB(0, 1), b2 + hstep, voffB); PG8_STAGE(PG8_SA(0, 0), a2, w0);
;             PG8_WAIT_V(8); PG8_WAIT_L(0); PG8_BAR; PG8_MMA(1, 0, At, B0); PG8_MMA(1, 1, At, B1); PG8_BAR; PG8_SCHED;
.LBB0_1498:
	ds_read_b128 v[142:145], v1
	ds_read_b128 v[158:161], v1 offset:1024
	ds_read_b128 v[162:165], v1 offset:2048
	ds_read_b128 v[166:169], v1 offset:3072
	ds_read_b128 v[170:173], v156
	ds_read_b128 v[174:177], v156 offset:1024
	ds_read_b128 v[178:181], v156 offset:2048
	ds_read_b128 v[182:185], v156 offset:3072
	s_add_u32 s58, s56, 0xfffe0080
	s_addc_u32 s59, s57, -1
	s_cmp_eq_u32 s87, 4
	s_cselect_b32 s61, s41, s59
	s_cselect_b32 s60, s53, s58
	s_cselect_b32 s59, s43, s86
	s_cselect_b32 s58, s84, s85
	v_lshl_add_u64 v[218:219], s[56:57], 0, v[140:141]
	s_add_i32 m0, s55, 0xc000
	ds_read_b128 v[186:189], v157
	ds_read_b128 v[190:193], v157 offset:1024
	ds_read_b128 v[194:197], v157 offset:2048
	ds_read_b128 v[198:201], v157 offset:3072
	ds_read_b128 v[202:205], v157 offset:4096
	ds_read_b128 v[206:209], v157 offset:5120
	ds_read_b128 v[210:213], v157 offset:6144
	ds_read_b128 v[214:217], v157 offset:7168
	global_load_lds_dwordx4 v[218:219], off
	v_lshl_add_u64 v[218:219], s[56:57], 0, v[138:139]
	s_add_i32 m0, s55, 0xe000
	s_nop 0
	global_load_lds_dwordx4 v[218:219], off
	s_waitcnt vmcnt(8)
	s_waitcnt lgkmcnt(0)
	s_barrier
	v_mfma_f32_16x16x32_bf16 v[126:129], v[142:145], v[186:189], v[126:129]
	v_mfma_f32_16x16x32_bf16 v[122:125], v[162:165], v[186:189], v[122:125]
	v_mfma_f32_16x16x32_bf16 v[114:117], v[142:145], v[194:197], v[114:117]
	v_mfma_f32_16x16x32_bf16 v[106:109], v[162:165], v[194:197], v[106:109]
	v_mfma_f32_16x16x32_bf16 v[98:101], v[142:145], v[202:205], v[98:101]
	v_mfma_f32_16x16x32_bf16 v[90:93], v[162:165], v[202:205], v[90:93]
	v_mfma_f32_16x16x32_bf16 v[82:85], v[142:145], v[210:213], v[82:85]
	v_mfma_f32_16x16x32_bf16 v[74:77], v[162:165], v[210:213], v[74:77]
	v_mfma_f32_16x16x32_bf16 v[126:129], v[158:161], v[190:193], v[126:129]
	v_mfma_f32_16x16x32_bf16 v[122:125], v[166:169], v[190:193], v[122:125]
	v_mfma_f32_16x16x32_bf16 v[114:117], v[158:161], v[198:201], v[114:117]
	v_mfma_f32_16x16x32_bf16 v[106:109], v[166:169], v[198:201], v[106:109]
	v_mfma_f32_16x16x32_bf16 v[98:101], v[158:161], v[206:209], v[98:101]
	v_mfma_f32_16x16x32_bf16 v[90:93], v[166:169], v[206:209], v[90:93]
	v_mfma_f32_16x16x32_bf16 v[82:85], v[158:161], v[214:217], v[82:85]
	v_mfma_f32_16x16x32_bf16 v[74:77], v[166:169], v[214:217], v[74:77]
	v_mfma_f32_16x16x32_bf16 v[118:121], v[170:173], v[186:189], v[118:121]
	v_mfma_f32_16x16x32_bf16 v[110:113], v[178:181], v[186:189], v[110:113]
	v_mfma_f32_16x16x32_bf16 v[102:105], v[170:173], v[194:197], v[102:105]
	v_mfma_f32_16x16x32_bf16 v[94:97], v[178:181], v[194:197], v[94:97]
	v_mfma_f32_16x16x32_bf16 v[86:89], v[170:173], v[202:205], v[86:89]
	v_mfma_f32_16x16x32_bf16 v[78:81], v[178:181], v[202:205], v[78:81]
	v_mfma_f32_16x16x32_bf16 v[62:65], v[170:173], v[210:213], v[62:65]
	v_mfma_f32_16x16x32_bf16 v[58:61], v[178:181], v[210:213], v[58:61]
	v_mfma_f32_16x16x32_bf16 v[118:121], v[174:177], v[190:193], v[118:121]
	v_mfma_f32_16x16x32_bf16 v[110:113], v[182:185], v[190:193], v[110:113]
	v_mfma_f32_16x16x32_bf16 v[102:105], v[174:177], v[198:201], v[102:105]
	v_mfma_f32_16x16x32_bf16 v[94:97], v[182:185], v[198:201], v[94:97]
	s_barrier
	v_mfma_f32_16x16x32_bf16 v[86:89], v[174:177], v[206:209], v[86:89]
	v_mfma_f32_16x16x32_bf16 v[78:81], v[182:185], v[206:209], v[78:81]
	v_mfma_f32_16x16x32_bf16 v[62:65], v[174:177], v[214:217], v[62:65]
	v_mfma_f32_16x16x32_bf16 v[58:61], v[182:185], v[214:217], v[58:61]
	s_add_i32 s88, s74, s62
	v_lshl_add_u64 v[218:219], s[58:59], 0, v[132:133]
	s_mov_b32 m0, s88
	ds_read_b128 v[186:189], v157 offset:16384
	ds_read_b128 v[190:193], v157 offset:17408
	ds_read_b128 v[194:197], v157 offset:18432
	ds_read_b128 v[198:201], v157 offset:19456
	ds_read_b128 v[202:205], v157 offset:20480
	ds_read_b128 v[206:209], v157 offset:21504
	ds_read_b128 v[210:213], v157 offset:22528
	ds_read_b128 v[214:217], v157 offset:23552
	global_load_lds_dwordx4 v[218:219], off
	s_add_i32 m0, s88, 0x2000
	s_add_u32 s88, s58, 0x20000
	v_lshl_add_u64 v[220:221], s[58:59], 0, v[136:137]
	s_addc_u32 s89, s59, 0
	s_add_i32 s90, s75, s62
	global_load_lds_dwordx4 v[220:221], off
	v_lshl_add_u64 v[222:223], s[88:89], 0, v[132:133]
	s_mov_b32 m0, s90
	v_lshl_add_u64 v[224:225], s[60:61], 0, v[134:135]
	global_load_lds_dwordx4 v[222:223], off
	v_lshl_add_u64 v[222:223], s[88:89], 0, v[136:137]
	s_add_i32 m0, s90, 0x2000
	s_nop 0
	global_load_lds_dwordx4 v[222:223], off
	v_lshl_add_u64 v[222:223], s[60:61], 0, v[130:131]
	s_mov_b32 m0, s55
	s_nop 0
	global_load_lds_dwordx4 v[222:223], off
	s_mov_b32 m0, s63
	s_nop 0
	global_load_lds_dwordx4 v[224:225], off
	s_waitcnt vmcnt(8)
	s_waitcnt lgkmcnt(0)
	s_barrier
	v_mfma_f32_16x16x32_bf16 v[54:57], v[142:145], v[186:189], v[54:57]
	v_mfma_f32_16x16x32_bf16 v[42:45], v[162:165], v[186:189], v[42:45]
	v_mfma_f32_16x16x32_bf16 v[30:33], v[142:145], v[194:197], v[30:33]
	v_mfma_f32_16x16x32_bf16 v[26:29], v[162:165], v[194:197], v[26:29]
	v_mfma_f32_16x16x32_bf16 v[14:17], v[142:145], v[202:205], v[14:17]
	v_mfma_f32_16x16x32_bf16 v[10:13], v[162:165], v[202:205], v[10:13]
	v_mfma_f32_16x16x32_bf16 v[6:9], v[142:145], v[210:213], v[6:9]
	v_mfma_f32_16x16x32_bf16 v[2:5], v[162:165], v[210:213], v[2:5]
	v_mfma_f32_16x16x32_bf16 v[54:57], v[158:161], v[190:193], v[54:57]
	v_mfma_f32_16x16x32_bf16 v[42:45], v[166:169], v[190:193], v[42:45]
	v_mfma_f32_16x16x32_bf16 v[30:33], v[158:161], v[198:201], v[30:33]
	v_mfma_f32_16x16x32_bf16 v[26:29], v[166:169], v[198:201], v[26:29]
	v_mfma_f32_16x16x32_bf16 v[14:17], v[158:161], v[206:209], v[14:17]
	v_mfma_f32_16x16x32_bf16 v[10:13], v[166:169], v[206:209], v[10:13]
	v_mfma_f32_16x16x32_bf16 v[6:9], v[158:161], v[214:217], v[6:9]
	v_mfma_f32_16x16x32_bf16 v[2:5], v[166:169], v[214:217], v[2:5]
	v_mfma_f32_16x16x32_bf16 v[70:73], v[170:173], v[186:189], v[70:73]
	v_mfma_f32_16x16x32_bf16 v[66:69], v[178:181], v[186:189], v[66:69]
	v_mfma_f32_16x16x32_bf16 v[50:53], v[170:173], v[194:197], v[50:53]
	v_mfma_f32_16x16x32_bf16 v[46:49], v[178:181], v[194:197], v[46:49]
	v_mfma_f32_16x16x32_bf16 v[38:41], v[170:173], v[202:205], v[38:41]
	v_mfma_f32_16x16x32_bf16 v[34:37], v[178:181], v[202:205], v[34:37]
	v_mfma_f32_16x16x32_bf16 v[22:25], v[170:173], v[210:213], v[22:25]
	v_mfma_f32_16x16x32_bf16 v[18:21], v[178:181], v[210:213], v[18:21]
	v_mfma_f32_16x16x32_bf16 v[70:73], v[174:177], v[190:193], v[70:73]
	v_mfma_f32_16x16x32_bf16 v[66:69], v[182:185], v[190:193], v[66:69]
	v_mfma_f32_16x16x32_bf16 v[50:53], v[174:177], v[198:201], v[50:53]
	v_mfma_f32_16x16x32_bf16 v[46:49], v[182:185], v[198:201], v[46:49]
	s_barrier
; #define PG8_STAGE(bufoff, gbase, voff) do { _Pragma("unroll") for (int _i = 0; _i < 2; ++_i) \
;         __builtin_amdgcn_global_load_lds((const unsigned*)((const char*)(gbase) + (voff)[_i]), (PG8_LAS unsigned*)(lds + (bufoff) + ldsw + _i * 8192), 16, 0, 0); } while (0)
; #define PG8_LDA(dst, b, h) do { _Pragma("unroll") for (int m = 0; m < 4; ++m) _Pragma("unroll") for (int k = 0; k < 2; ++k) dst[m][k] = *(const PG8_LAS bf16x8*)(lds + PG8_SA(b, h) + aoff + m * 2048 + k * 1024); } while (0)
; #define PG8_LDB(dst, b, h) do { _Pragma("unroll") for (int n = 0; n < 2; ++n) _Pragma("unroll") for (int k = 0; k < 2; ++k) dst[n][k] = *(const PG8_LAS bf16x8*)(lds + PG8_SB(b, h) + boff + n * 2048 + k * 1024); } while (0)
; #define PG8_MMA(ai, bj, At, Bt) do { __builtin_amdgcn_s_setprio(1); _Pragma("unroll") for (int m = 0; m < 4; ++m) _Pragma("unroll") for (int n = 0; n < 2; ++n) _Pragma("unroll") for (int k = 0; k < 2; ++k) \
;         acc[ai][bj][m][n] = __builtin_amdgcn_mfma_f32_16x16x32_bf16(Bt[n][k], At[m][k], acc[ai][bj][m][n], 0, 0, 0); __builtin_amdgcn_s_setprio(0); } while (0)
; #define PG8_WAIT_V(n) asm volatile("s_waitcnt vmcnt(" #n ")" ::: "memory")
; #define PG8_WAIT_L(n) asm volatile("s_waitcnt lgkmcnt(" #n ")" ::: "memory")
; #define PG8_BAR __builtin_amdgcn_s_barrier()
; #define PG8_SCHED __builtin_amdgcn_sched_barrier(0)
; template <class Epi, class Sched, bool ALIGN_EPI = false>
; __device__ __forceinline__ void gemm_phase(PG8_LAS unsigned char* lds, const Gemm g, const Sched& S, const Epi& E) {
;     ...
;             PG8_WAIT_V(8); PG8_WAIT_L(0); PG8_BAR; PG8_MMA(1, 0, At, B0); PG8_MMA(1, 1, At, B1); PG8_BAR; PG8_SCHED;
;             PG8_LDB(B0, 1, 0); PG8_LDB(B1, 1, 1); PG8_SCHED; PG8_LDA(At, 1, 0); PG8_STAGE(PG8_SA(0, 1), a2 + hstepA, w1);
;             PG8_WAIT_V(8); PG8_WAIT_L(0); PG8_BAR; PG8_MMA(0, 0, At, B0); PG8_MMA(0, 1, At, B1); PG8_BAR; PG8_SCHED;
	v_mfma_f32_16x16x32_bf16 v[38:41], v[174:177], v[206:209], v[38:41]
	v_mfma_f32_16x16x32_bf16 v[34:37], v[182:185], v[206:209], v[34:37]
	v_mfma_f32_16x16x32_bf16 v[22:25], v[174:177], v[214:217], v[22:25]
	v_mfma_f32_16x16x32_bf16 v[18:21], v[182:185], v[214:217], v[18:21]
	s_add_i32 s88, 0, 0x18000
	s_add_i32 s89, 0, 0x1c000
	v_add_u32_e32 v166, s88, v147
	v_add_u32_e32 v182, s89, v147
	ds_read_b128 v[142:145], v166
	ds_read_b128 v[158:161], v166 offset:1024
	ds_read_b128 v[162:165], v166 offset:2048
	ds_read_b128 v[166:169], v166 offset:3072
	ds_read_b128 v[170:173], v182
	ds_read_b128 v[174:177], v182 offset:1024
	ds_read_b128 v[178:181], v182 offset:2048
	ds_read_b128 v[182:185], v182 offset:3072
	s_add_u32 s60, s60, 0x20000
	s_addc_u32 s61, s61, 0
	s_mov_b32 m0, s64
	v_lshl_add_u64 v[226:227], s[60:61], 0, v[130:131]
	ds_read_b128 v[186:189], v157 offset:32768
	ds_read_b128 v[190:193], v157 offset:33792
	ds_read_b128 v[194:197], v157 offset:34816
	ds_read_b128 v[198:201], v157 offset:35840
	ds_read_b128 v[202:205], v157 offset:36864
	ds_read_b128 v[206:209], v157 offset:37888
	ds_read_b128 v[210:213], v157 offset:38912
	ds_read_b128 v[214:217], v157 offset:39936
	global_load_lds_dwordx4 v[226:227], off
	v_lshl_add_u64 v[226:227], s[60:61], 0, v[134:135]
	s_mov_b32 m0, s65
	s_nop 0
	global_load_lds_dwordx4 v[226:227], off
	s_waitcnt vmcnt(8)
	s_waitcnt lgkmcnt(0)
	s_barrier
	v_mfma_f32_16x16x32_bf16 v[126:129], v[142:145], v[186:189], v[126:129]
	v_mfma_f32_16x16x32_bf16 v[122:125], v[162:165], v[186:189], v[122:125]
	v_mfma_f32_16x16x32_bf16 v[114:117], v[142:145], v[194:197], v[114:117]
	v_mfma_f32_16x16x32_bf16 v[106:109], v[162:165], v[194:197], v[106:109]
	v_mfma_f32_16x16x32_bf16 v[98:101], v[142:145], v[202:205], v[98:101]
	v_mfma_f32_16x16x32_bf16 v[90:93], v[162:165], v[202:205], v[90:93]
	v_mfma_f32_16x16x32_bf16 v[82:85], v[142:145], v[210:213], v[82:85]
	v_mfma_f32_16x16x32_bf16 v[74:77], v[162:165], v[210:213], v[74:77]
	v_mfma_f32_16x16x32_bf16 v[126:129], v[158:161], v[190:193], v[126:129]
	v_mfma_f32_16x16x32_bf16 v[122:125], v[166:169], v[190:193], v[122:125]
	v_mfma_f32_16x16x32_bf16 v[114:117], v[158:161], v[198:201], v[114:117]
	v_mfma_f32_16x16x32_bf16 v[106:109], v[166:169], v[198:201], v[106:109]
	v_mfma_f32_16x16x32_bf16 v[98:101], v[158:161], v[206:209], v[98:101]
	v_mfma_f32_16x16x32_bf16 v[90:93], v[166:169], v[206:209], v[90:93]
	v_mfma_f32_16x16x32_bf16 v[82:85], v[158:161], v[214:217], v[82:85]
	v_mfma_f32_16x16x32_bf16 v[74:77], v[166:169], v[214:217], v[74:77]
	v_mfma_f32_16x16x32_bf16 v[118:121], v[170:173], v[186:189], v[118:121]
	v_mfma_f32_16x16x32_bf16 v[110:113], v[178:181], v[186:189], v[110:113]
	v_mfma_f32_16x16x32_bf16 v[102:105], v[170:173], v[194:197], v[102:105]
	v_mfma_f32_16x16x32_bf16 v[94:97], v[178:181], v[194:197], v[94:97]
	v_mfma_f32_16x16x32_bf16 v[86:89], v[170:173], v[202:205], v[86:89]
	v_mfma_f32_16x16x32_bf16 v[78:81], v[178:181], v[202:205], v[78:81]
	v_mfma_f32_16x16x32_bf16 v[62:65], v[170:173], v[210:213], v[62:65]
	v_mfma_f32_16x16x32_bf16 v[58:61], v[178:181], v[210:213], v[58:61]
	v_mfma_f32_16x16x32_bf16 v[118:121], v[174:177], v[190:193], v[118:121]
	v_mfma_f32_16x16x32_bf16 v[110:113], v[182:185], v[190:193], v[110:113]
	v_mfma_f32_16x16x32_bf16 v[102:105], v[174:177], v[198:201], v[102:105]
	v_mfma_f32_16x16x32_bf16 v[94:97], v[182:185], v[198:201], v[94:97]
	s_barrier
; #define PG8_STAGE(bufoff, gbase, voff) do { _Pragma("unroll") for (int _i = 0; _i < 2; ++_i) \
;         __builtin_amdgcn_global_load_lds((const unsigned*)((const char*)(gbase) + (voff)[_i]), (PG8_LAS unsigned*)(lds + (bufoff) + ldsw + _i * 8192), 16, 0, 0); } while (0)
; #define PG8_LDA(dst, b, h) do { _Pragma("unroll") for (int m = 0; m < 4; ++m) _Pragma("unroll") for (int k = 0; k < 2; ++k) dst[m][k] = *(const PG8_LAS bf16x8*)(lds + PG8_SA(b, h) + aoff + m * 2048 + k * 1024); } while (0)
; #define PG8_MMA(ai, bj, At, Bt) do { __builtin_amdgcn_s_setprio(1); _Pragma("unroll") for (int m = 0; m < 4; ++m) _Pragma("unroll") for (int n = 0; n < 2; ++n) _Pragma("unroll") for (int k = 0; k < 2; ++k) \
;         acc[ai][bj][m][n] = __builtin_amdgcn_mfma_f32_16x16x32_bf16(Bt[n][k], At[m][k], acc[ai][bj][m][n], 0, 0, 0); __builtin_amdgcn_s_setprio(0); } while (0)
; #define PG8_WAIT_V(n) asm volatile("s_waitcnt vmcnt(" #n ")" ::: "memory")
; #define PG8_WAIT_L(n) asm volatile("s_waitcnt lgkmcnt(" #n ")" ::: "memory")
; #define PG8_BAR __builtin_amdgcn_s_barrier()
; #define PG8_SCHED __builtin_amdgcn_sched_barrier(0)
; template <class Epi, class Sched, bool ALIGN_EPI = false>
; __device__ __forceinline__ void gemm_phase(PG8_LAS unsigned char* lds, const Gemm g, const Sched& S, const Epi& E) {
;     ...
;             PG8_WAIT_V(8); PG8_WAIT_L(0); PG8_BAR; PG8_MMA(0, 0, At, B0); PG8_MMA(0, 1, At, B1); PG8_BAR; PG8_SCHED;
;             PG8_LDA(At, 1, 1); PG8_STAGE(PG8_SB(1, 0), b3, voffB); PG8_STAGE(PG8_SB(1, 1), b3 + hstep, voffB); PG8_STAGE(PG8_SA(1, 0), a3, w0);
;             PG8_WAIT_V(8); PG8_WAIT_L(0); PG8_BAR; PG8_MMA(1, 0, At, B0); PG8_MMA(1, 1, At, B1); PG8_BAR; PG8_SCHED;
;             if constexpr (Epi::KSCALE) { if (((t + 2) & 7) == 0 && t + 2 < nt) { E.kscale(acc, pf, ((t + 2) >> 3) - 1, wr, fr); PG8_SCHED; } }
;         }
	v_mfma_f32_16x16x32_bf16 v[86:89], v[174:177], v[206:209], v[86:89]
	v_mfma_f32_16x16x32_bf16 v[78:81], v[182:185], v[206:209], v[78:81]
	v_mfma_f32_16x16x32_bf16 v[62:65], v[174:177], v[214:217], v[62:65]
	v_mfma_f32_16x16x32_bf16 v[58:61], v[182:185], v[214:217], v[58:61]
	s_add_i32 s60, s88, s62
	v_lshl_add_u64 v[218:219], v[218:219], 0, s[16:17]
	s_mov_b32 m0, s60
	ds_read_b128 v[186:189], v157 offset:49152
	ds_read_b128 v[190:193], v157 offset:50176
	ds_read_b128 v[194:197], v157 offset:51200
	ds_read_b128 v[198:201], v157 offset:52224
	ds_read_b128 v[202:205], v157 offset:53248
	ds_read_b128 v[206:209], v157 offset:54272
	ds_read_b128 v[210:213], v157 offset:55296
	ds_read_b128 v[214:217], v157 offset:56320
	global_load_lds_dwordx4 v[218:219], off
	s_add_i32 m0, s60, 0x2000
	s_add_u32 s58, s58, 0x20080
	v_lshl_add_u64 v[218:219], v[220:221], 0, s[16:17]
	s_addc_u32 s59, s59, 0
	s_add_i32 s60, s89, s62
	global_load_lds_dwordx4 v[218:219], off
	v_lshl_add_u64 v[218:219], s[58:59], 0, v[132:133]
	s_mov_b32 m0, s60
	s_nop 0
	global_load_lds_dwordx4 v[218:219], off
	v_lshl_add_u64 v[218:219], s[58:59], 0, v[136:137]
	s_add_i32 m0, s60, 0x2000
	s_nop 0
	global_load_lds_dwordx4 v[218:219], off
	v_lshl_add_u64 v[218:219], v[222:223], 0, s[16:17]
	s_mov_b32 m0, s67
	s_nop 0
	global_load_lds_dwordx4 v[218:219], off
	v_lshl_add_u64 v[218:219], v[224:225], 0, s[16:17]
	s_mov_b32 m0, s68
	s_nop 0
	global_load_lds_dwordx4 v[218:219], off
	s_waitcnt vmcnt(8)
	s_waitcnt lgkmcnt(0)
	s_barrier
	v_mfma_f32_16x16x32_bf16 v[54:57], v[142:145], v[186:189], v[54:57]
	v_mfma_f32_16x16x32_bf16 v[42:45], v[162:165], v[186:189], v[42:45]
	v_mfma_f32_16x16x32_bf16 v[30:33], v[142:145], v[194:197], v[30:33]
	v_mfma_f32_16x16x32_bf16 v[26:29], v[162:165], v[194:197], v[26:29]
	v_mfma_f32_16x16x32_bf16 v[14:17], v[142:145], v[202:205], v[14:17]
	v_mfma_f32_16x16x32_bf16 v[10:13], v[162:165], v[202:205], v[10:13]
	v_mfma_f32_16x16x32_bf16 v[6:9], v[142:145], v[210:213], v[6:9]
	v_mfma_f32_16x16x32_bf16 v[2:5], v[162:165], v[210:213], v[2:5]
	v_mfma_f32_16x16x32_bf16 v[54:57], v[158:161], v[190:193], v[54:57]
	v_mfma_f32_16x16x32_bf16 v[42:45], v[166:169], v[190:193], v[42:45]
	v_mfma_f32_16x16x32_bf16 v[30:33], v[158:161], v[198:201], v[30:33]
	v_mfma_f32_16x16x32_bf16 v[26:29], v[166:169], v[198:201], v[26:29]
	v_mfma_f32_16x16x32_bf16 v[14:17], v[158:161], v[206:209], v[14:17]
	v_mfma_f32_16x16x32_bf16 v[10:13], v[166:169], v[206:209], v[10:13]
	v_mfma_f32_16x16x32_bf16 v[6:9], v[158:161], v[214:217], v[6:9]
	v_mfma_f32_16x16x32_bf16 v[2:5], v[166:169], v[214:217], v[2:5]
	v_mfma_f32_16x16x32_bf16 v[70:73], v[170:173], v[186:189], v[70:73]
	v_mfma_f32_16x16x32_bf16 v[66:69], v[178:181], v[186:189], v[66:69]
	v_mfma_f32_16x16x32_bf16 v[50:53], v[170:173], v[194:197], v[50:53]
	v_mfma_f32_16x16x32_bf16 v[46:49], v[178:181], v[194:197], v[46:49]
	v_mfma_f32_16x16x32_bf16 v[38:41], v[170:173], v[202:205], v[38:41]
	v_mfma_f32_16x16x32_bf16 v[34:37], v[178:181], v[202:205], v[34:37]
	v_mfma_f32_16x16x32_bf16 v[22:25], v[170:173], v[210:213], v[22:25]
	v_mfma_f32_16x16x32_bf16 v[18:21], v[178:181], v[210:213], v[18:21]
	v_mfma_f32_16x16x32_bf16 v[70:73], v[174:177], v[190:193], v[70:73]
	v_mfma_f32_16x16x32_bf16 v[66:69], v[182:185], v[190:193], v[66:69]
	v_mfma_f32_16x16x32_bf16 v[50:53], v[174:177], v[198:201], v[50:53]
	v_mfma_f32_16x16x32_bf16 v[46:49], v[182:185], v[198:201], v[46:49]
	s_barrier
	v_mfma_f32_16x16x32_bf16 v[38:41], v[174:177], v[206:209], v[38:41]
	v_mfma_f32_16x16x32_bf16 v[34:37], v[182:185], v[206:209], v[34:37]
	v_mfma_f32_16x16x32_bf16 v[22:25], v[174:177], v[214:217], v[22:25]
	v_mfma_f32_16x16x32_bf16 v[18:21], v[182:185], v[214:217], v[18:21]
	s_add_i32 s87, s87, 2
	s_add_u32 s85, s85, 0x100
	s_addc_u32 s86, s86, 0
	s_add_u32 s56, s56, 0x100
	s_addc_u32 s57, s57, 0
	s_cmp_gt_u32 s87, 5
	s_cbranch_scc0 .LBB0_1498
	s_and_b64 vcc, exec, s[18:19]
	s_cbranch_vccz .LBB0_1501
	s_barrier

; #define PG8_STAGE(bufoff, gbase, voff) do { _Pragma("unroll") for (int _i = 0; _i < 2; ++_i) \
;         __builtin_amdgcn_global_load_lds((const unsigned*)((const char*)(gbase) + (voff)[_i]), (PG8_LAS unsigned*)(lds + (bufoff) + ldsw + _i * 8192), 16, 0, 0); } while (0)
; #define PG8_LDA(dst, b, h) do { _Pragma("unroll") for (int m = 0; m < 4; ++m) _Pragma("unroll") for (int k = 0; k < 2; ++k) dst[m][k] = *(const PG8_LAS bf16x8*)(lds + PG8_SA(b, h) + aoff + m * 2048 + k * 1024); } while (0)
; #define PG8_LDB(dst, b, h) do { _Pragma("unroll") for (int n = 0; n < 2; ++n) _Pragma("unroll") for (int k = 0; k < 2; ++k) dst[n][k] = *(const PG8_LAS bf16x8*)(lds + PG8_SB(b, h) + boff + n * 2048 + k * 1024); } while (0)
; #define PG8_MMA(ai, bj, At, Bt) do { __builtin_amdgcn_s_setprio(1); _Pragma("unroll") for (int m = 0; m < 4; ++m) _Pragma("unroll") for (int n = 0; n < 2; ++n) _Pragma("unroll") for (int k = 0; k < 2; ++k) \
;         acc[ai][bj][m][n] = __builtin_amdgcn_mfma_f32_16x16x32_bf16(Bt[n][k], At[m][k], acc[ai][bj][m][n], 0, 0, 0); __builtin_amdgcn_s_setprio(0); } while (0)
; #define PG8_BAR __builtin_amdgcn_s_barrier()
; template <class Epi, class Sched, bool ALIGN_EPI = false>
; __device__ __forceinline__ void gemm_phase(PG8_LAS unsigned char* lds, const Gemm g, const Sched& S, const Epi& E) {
;     ...
;             const bool last = (t == nt - 2);
;             const char* a1 = cA + (size_t)(t + 1) * kstep;
;             const char* a2 = last ? nA : cA + (size_t)(t + 2) * kstep; const char* b2 = last ? nB : cB + (size_t)(t + 2) * kstep;
;             const char* a3 = a2 + kstep; const char* b3 = b2 + kstep;
;             unsigned w0[2], w1[2];
; #pragma unroll
;             for (int i = 0; i < 2; ++i) { w0[i] = (Sched::GATHER && last) ? vn0[i] : vc0[i]; w1[i] = (Sched::GATHER && last) ? vn1[i] : vc1[i]; }
;             if (last && has_next) S.a_ready(nxt);
;             PG8_LDB(B0, 0, 0); PG8_LDB(B1, 0, 1); PG8_SCHED; PG8_LDA(At, 0, 0); PG8_STAGE(PG8_SA(1, 1), a1 + hstepA, vc1);
;             PG8_WAIT_V(8); PG8_WAIT_L(0); PG8_BAR; PG8_MMA(0, 0, At, B0); PG8_MMA(0, 1, At, B1); PG8_BAR; PG8_SCHED;
;             PG8_LDA(At, 0, 1); PG8_STAGE(PG8_SB(0, 0), b2, voffB); PG8_STAGE(PG8_SB(0, 1), b2 + hstep, voffB); PG8_STAGE(PG8_SA(0, 0), a2, w0);
;             PG8_WAIT_V(8); PG8_WAIT_L(0); PG8_BAR; PG8_MMA(1, 0, At, B0); PG8_MMA(1, 1, At, B1); PG8_BAR; PG8_SCHED;
.LBB0_1601:
	ds_read_b128 v[144:147], v157
	ds_read_b128 v[160:163], v157 offset:1024
	ds_read_b128 v[164:167], v157 offset:2048
	ds_read_b128 v[168:171], v157 offset:3072
	ds_read_b128 v[172:175], v158
	ds_read_b128 v[176:179], v158 offset:1024
	ds_read_b128 v[180:183], v158 offset:2048
	ds_read_b128 v[184:187], v158 offset:3072
	s_add_u32 s54, s52, 0xfffe0080
	s_addc_u32 s55, s53, -1
	s_cmp_eq_u32 s87, 4
	s_cselect_b32 s57, s25, s55
	s_cselect_b32 s56, s43, s54
	s_cselect_b32 s55, s27, s86
	s_cselect_b32 s54, s84, s85
	v_lshl_add_u64 v[220:221], s[52:53], 0, v[142:143]
	s_add_i32 m0, s45, 0xc000
	ds_read_b128 v[188:191], v159
	ds_read_b128 v[192:195], v159 offset:1024
	ds_read_b128 v[196:199], v159 offset:2048
	ds_read_b128 v[200:203], v159 offset:3072
	ds_read_b128 v[204:207], v159 offset:4096
	ds_read_b128 v[208:211], v159 offset:5120
	ds_read_b128 v[212:215], v159 offset:6144
	ds_read_b128 v[216:219], v159 offset:7168
	global_load_lds_dwordx4 v[220:221], off
	v_lshl_add_u64 v[220:221], s[52:53], 0, v[140:141]
	s_add_i32 m0, s45, 0xe000
	s_nop 0
	global_load_lds_dwordx4 v[220:221], off
	s_waitcnt vmcnt(8)
	s_waitcnt lgkmcnt(0)
	s_barrier
	v_mfma_f32_16x16x32_bf16 v[126:129], v[144:147], v[188:191], v[126:129]
	v_mfma_f32_16x16x32_bf16 v[122:125], v[164:167], v[188:191], v[122:125]
	v_mfma_f32_16x16x32_bf16 v[114:117], v[144:147], v[196:199], v[114:117]
	v_mfma_f32_16x16x32_bf16 v[106:109], v[164:167], v[196:199], v[106:109]
	v_mfma_f32_16x16x32_bf16 v[98:101], v[144:147], v[204:207], v[98:101]
	v_mfma_f32_16x16x32_bf16 v[90:93], v[164:167], v[204:207], v[90:93]
	v_mfma_f32_16x16x32_bf16 v[82:85], v[144:147], v[212:215], v[82:85]
	v_mfma_f32_16x16x32_bf16 v[74:77], v[164:167], v[212:215], v[74:77]
	v_mfma_f32_16x16x32_bf16 v[126:129], v[160:163], v[192:195], v[126:129]
	v_mfma_f32_16x16x32_bf16 v[122:125], v[168:171], v[192:195], v[122:125]
	v_mfma_f32_16x16x32_bf16 v[114:117], v[160:163], v[200:203], v[114:117]
	v_mfma_f32_16x16x32_bf16 v[106:109], v[168:171], v[200:203], v[106:109]
	v_mfma_f32_16x16x32_bf16 v[98:101], v[160:163], v[208:211], v[98:101]
	v_mfma_f32_16x16x32_bf16 v[90:93], v[168:171], v[208:211], v[90:93]
	v_mfma_f32_16x16x32_bf16 v[82:85], v[160:163], v[216:219], v[82:85]
	v_mfma_f32_16x16x32_bf16 v[74:77], v[168:171], v[216:219], v[74:77]
	v_mfma_f32_16x16x32_bf16 v[118:121], v[172:175], v[188:191], v[118:121]
	v_mfma_f32_16x16x32_bf16 v[110:113], v[180:183], v[188:191], v[110:113]
	v_mfma_f32_16x16x32_bf16 v[102:105], v[172:175], v[196:199], v[102:105]
	v_mfma_f32_16x16x32_bf16 v[94:97], v[180:183], v[196:199], v[94:97]
	v_mfma_f32_16x16x32_bf16 v[86:89], v[172:175], v[204:207], v[86:89]
	v_mfma_f32_16x16x32_bf16 v[78:81], v[180:183], v[204:207], v[78:81]
	v_mfma_f32_16x16x32_bf16 v[62:65], v[172:175], v[212:215], v[62:65]
	v_mfma_f32_16x16x32_bf16 v[58:61], v[180:183], v[212:215], v[58:61]
	v_mfma_f32_16x16x32_bf16 v[118:121], v[176:179], v[192:195], v[118:121]
	v_mfma_f32_16x16x32_bf16 v[110:113], v[184:187], v[192:195], v[110:113]
	v_mfma_f32_16x16x32_bf16 v[102:105], v[176:179], v[200:203], v[102:105]
	v_mfma_f32_16x16x32_bf16 v[94:97], v[184:187], v[200:203], v[94:97]
	s_barrier
	v_mfma_f32_16x16x32_bf16 v[86:89], v[176:179], v[208:211], v[86:89]
	v_mfma_f32_16x16x32_bf16 v[78:81], v[184:187], v[208:211], v[78:81]
	v_mfma_f32_16x16x32_bf16 v[62:65], v[176:179], v[216:219], v[62:65]
	v_mfma_f32_16x16x32_bf16 v[58:61], v[184:187], v[216:219], v[58:61]
	s_add_i32 s88, s74, s62
	v_lshl_add_u64 v[220:221], s[54:55], 0, v[134:135]
	s_mov_b32 m0, s88
	ds_read_b128 v[188:191], v159 offset:16384
	ds_read_b128 v[192:195], v159 offset:17408
	ds_read_b128 v[196:199], v159 offset:18432
	ds_read_b128 v[200:203], v159 offset:19456
	ds_read_b128 v[204:207], v159 offset:20480
	ds_read_b128 v[208:211], v159 offset:21504
	ds_read_b128 v[212:215], v159 offset:22528
	ds_read_b128 v[216:219], v159 offset:23552
	global_load_lds_dwordx4 v[220:221], off
	s_add_i32 m0, s88, 0x2000
	s_add_u32 s88, s54, 0x20000
	v_lshl_add_u64 v[222:223], s[54:55], 0, v[138:139]
	s_addc_u32 s89, s55, 0
	s_add_i32 s90, s75, s62
	global_load_lds_dwordx4 v[222:223], off
	v_lshl_add_u64 v[224:225], s[88:89], 0, v[134:135]
	s_mov_b32 m0, s90
	v_lshl_add_u64 v[226:227], s[56:57], 0, v[136:137]
	global_load_lds_dwordx4 v[224:225], off
	v_lshl_add_u64 v[224:225], s[88:89], 0, v[138:139]
	s_add_i32 m0, s90, 0x2000
	s_nop 0
	global_load_lds_dwordx4 v[224:225], off
	v_lshl_add_u64 v[224:225], s[56:57], 0, v[132:133]
	s_mov_b32 m0, s45
	s_nop 0
	global_load_lds_dwordx4 v[224:225], off
	s_mov_b32 m0, s63
	s_nop 0
	global_load_lds_dwordx4 v[226:227], off
	s_waitcnt vmcnt(8)
	s_waitcnt lgkmcnt(0)
	s_barrier
	v_mfma_f32_16x16x32_bf16 v[54:57], v[144:147], v[188:191], v[54:57]
	v_mfma_f32_16x16x32_bf16 v[42:45], v[164:167], v[188:191], v[42:45]
	v_mfma_f32_16x16x32_bf16 v[30:33], v[144:147], v[196:199], v[30:33]
	v_mfma_f32_16x16x32_bf16 v[26:29], v[164:167], v[196:199], v[26:29]
	v_mfma_f32_16x16x32_bf16 v[14:17], v[144:147], v[204:207], v[14:17]
	v_mfma_f32_16x16x32_bf16 v[10:13], v[164:167], v[204:207], v[10:13]
	v_mfma_f32_16x16x32_bf16 v[6:9], v[144:147], v[212:215], v[6:9]
	v_mfma_f32_16x16x32_bf16 v[2:5], v[164:167], v[212:215], v[2:5]
	v_mfma_f32_16x16x32_bf16 v[54:57], v[160:163], v[192:195], v[54:57]
	v_mfma_f32_16x16x32_bf16 v[42:45], v[168:171], v[192:195], v[42:45]
	v_mfma_f32_16x16x32_bf16 v[30:33], v[160:163], v[200:203], v[30:33]
	v_mfma_f32_16x16x32_bf16 v[26:29], v[168:171], v[200:203], v[26:29]
	v_mfma_f32_16x16x32_bf16 v[14:17], v[160:163], v[208:211], v[14:17]
	v_mfma_f32_16x16x32_bf16 v[10:13], v[168:171], v[208:211], v[10:13]
	v_mfma_f32_16x16x32_bf16 v[6:9], v[160:163], v[216:219], v[6:9]
	v_mfma_f32_16x16x32_bf16 v[2:5], v[168:171], v[216:219], v[2:5]
	v_mfma_f32_16x16x32_bf16 v[70:73], v[172:175], v[188:191], v[70:73]
	v_mfma_f32_16x16x32_bf16 v[66:69], v[180:183], v[188:191], v[66:69]
	v_mfma_f32_16x16x32_bf16 v[50:53], v[172:175], v[196:199], v[50:53]
	v_mfma_f32_16x16x32_bf16 v[46:49], v[180:183], v[196:199], v[46:49]
	v_mfma_f32_16x16x32_bf16 v[38:41], v[172:175], v[204:207], v[38:41]
	v_mfma_f32_16x16x32_bf16 v[34:37], v[180:183], v[204:207], v[34:37]
	v_mfma_f32_16x16x32_bf16 v[22:25], v[172:175], v[212:215], v[22:25]
	v_mfma_f32_16x16x32_bf16 v[18:21], v[180:183], v[212:215], v[18:21]
	v_mfma_f32_16x16x32_bf16 v[70:73], v[176:179], v[192:195], v[70:73]
	v_mfma_f32_16x16x32_bf16 v[66:69], v[184:187], v[192:195], v[66:69]
	v_mfma_f32_16x16x32_bf16 v[50:53], v[176:179], v[200:203], v[50:53]
	v_mfma_f32_16x16x32_bf16 v[46:49], v[184:187], v[200:203], v[46:49]
	s_barrier
; #define PG8_STAGE(bufoff, gbase, voff) do { _Pragma("unroll") for (int _i = 0; _i < 2; ++_i) \
;         __builtin_amdgcn_global_load_lds((const unsigned*)((const char*)(gbase) + (voff)[_i]), (PG8_LAS unsigned*)(lds + (bufoff) + ldsw + _i * 8192), 16, 0, 0); } while (0)
; #define PG8_LDA(dst, b, h) do { _Pragma("unroll") for (int m = 0; m < 4; ++m) _Pragma("unroll") for (int k = 0; k < 2; ++k) dst[m][k] = *(const PG8_LAS bf16x8*)(lds + PG8_SA(b, h) + aoff + m * 2048 + k * 1024); } while (0)
; #define PG8_LDB(dst, b, h) do { _Pragma("unroll") for (int n = 0; n < 2; ++n) _Pragma("unroll") for (int k = 0; k < 2; ++k) dst[n][k] = *(const PG8_LAS bf16x8*)(lds + PG8_SB(b, h) + boff + n * 2048 + k * 1024); } while (0)
; #define PG8_MMA(ai, bj, At, Bt) do { __builtin_amdgcn_s_setprio(1); _Pragma("unroll") for (int m = 0; m < 4; ++m) _Pragma("unroll") for (int n = 0; n < 2; ++n) _Pragma("unroll") for (int k = 0; k < 2; ++k) \
;         acc[ai][bj][m][n] = __builtin_amdgcn_mfma_f32_16x16x32_bf16(Bt[n][k], At[m][k], acc[ai][bj][m][n], 0, 0, 0); __builtin_amdgcn_s_setprio(0); } while (0)
; #define PG8_WAIT_V(n) asm volatile("s_waitcnt vmcnt(" #n ")" ::: "memory")
; #define PG8_WAIT_L(n) asm volatile("s_waitcnt lgkmcnt(" #n ")" ::: "memory")
; #define PG8_BAR __builtin_amdgcn_s_barrier()
; #define PG8_SCHED __builtin_amdgcn_sched_barrier(0)
; template <class Epi, class Sched, bool ALIGN_EPI = false>
; __device__ __forceinline__ void gemm_phase(PG8_LAS unsigned char* lds, const Gemm g, const Sched& S, const Epi& E) {
;     ...
;             PG8_WAIT_V(8); PG8_WAIT_L(0); PG8_BAR; PG8_MMA(1, 0, At, B0); PG8_MMA(1, 1, At, B1); PG8_BAR; PG8_SCHED;
;             PG8_LDB(B0, 1, 0); PG8_LDB(B1, 1, 1); PG8_SCHED; PG8_LDA(At, 1, 0); PG8_STAGE(PG8_SA(0, 1), a2 + hstepA, w1);
;             PG8_WAIT_V(8); PG8_WAIT_L(0); PG8_BAR; PG8_MMA(0, 0, At, B0); PG8_MMA(0, 1, At, B1); PG8_BAR; PG8_SCHED;
	v_mfma_f32_16x16x32_bf16 v[38:41], v[176:179], v[208:211], v[38:41]
	v_mfma_f32_16x16x32_bf16 v[34:37], v[184:187], v[208:211], v[34:37]
	v_mfma_f32_16x16x32_bf16 v[22:25], v[176:179], v[216:219], v[22:25]
	v_mfma_f32_16x16x32_bf16 v[18:21], v[184:187], v[216:219], v[18:21]
	s_add_i32 s88, 0, 0x18000
	s_add_i32 s89, 0, 0x1c000
	v_add_u32_e32 v168, s88, v148
	v_add_u32_e32 v184, s89, v148
	ds_read_b128 v[144:147], v168
	ds_read_b128 v[160:163], v168 offset:1024
	ds_read_b128 v[164:167], v168 offset:2048
	ds_read_b128 v[168:171], v168 offset:3072
	ds_read_b128 v[172:175], v184
	ds_read_b128 v[176:179], v184 offset:1024
	ds_read_b128 v[180:183], v184 offset:2048
	ds_read_b128 v[184:187], v184 offset:3072
	s_add_u32 s56, s56, 0x20000
	s_addc_u32 s57, s57, 0
	s_mov_b32 m0, s64
	v_lshl_add_u64 v[228:229], s[56:57], 0, v[132:133]
	ds_read_b128 v[188:191], v159 offset:32768
	ds_read_b128 v[192:195], v159 offset:33792
	ds_read_b128 v[196:199], v159 offset:34816
	ds_read_b128 v[200:203], v159 offset:35840
	ds_read_b128 v[204:207], v159 offset:36864
	ds_read_b128 v[208:211], v159 offset:37888
	ds_read_b128 v[212:215], v159 offset:38912
	ds_read_b128 v[216:219], v159 offset:39936
	global_load_lds_dwordx4 v[228:229], off
	v_lshl_add_u64 v[228:229], s[56:57], 0, v[136:137]
	s_mov_b32 m0, s65
	s_nop 0
	global_load_lds_dwordx4 v[228:229], off
	s_waitcnt vmcnt(8)
	s_waitcnt lgkmcnt(0)
	s_barrier
	v_mfma_f32_16x16x32_bf16 v[126:129], v[144:147], v[188:191], v[126:129]
	v_mfma_f32_16x16x32_bf16 v[122:125], v[164:167], v[188:191], v[122:125]
	v_mfma_f32_16x16x32_bf16 v[114:117], v[144:147], v[196:199], v[114:117]
	v_mfma_f32_16x16x32_bf16 v[106:109], v[164:167], v[196:199], v[106:109]
	v_mfma_f32_16x16x32_bf16 v[98:101], v[144:147], v[204:207], v[98:101]
	v_mfma_f32_16x16x32_bf16 v[90:93], v[164:167], v[204:207], v[90:93]
	v_mfma_f32_16x16x32_bf16 v[82:85], v[144:147], v[212:215], v[82:85]
	v_mfma_f32_16x16x32_bf16 v[74:77], v[164:167], v[212:215], v[74:77]
	v_mfma_f32_16x16x32_bf16 v[126:129], v[160:163], v[192:195], v[126:129]
	v_mfma_f32_16x16x32_bf16 v[122:125], v[168:171], v[192:195], v[122:125]
	v_mfma_f32_16x16x32_bf16 v[114:117], v[160:163], v[200:203], v[114:117]
	v_mfma_f32_16x16x32_bf16 v[106:109], v[168:171], v[200:203], v[106:109]
	v_mfma_f32_16x16x32_bf16 v[98:101], v[160:163], v[208:211], v[98:101]
	v_mfma_f32_16x16x32_bf16 v[90:93], v[168:171], v[208:211], v[90:93]
	v_mfma_f32_16x16x32_bf16 v[82:85], v[160:163], v[216:219], v[82:85]
	v_mfma_f32_16x16x32_bf16 v[74:77], v[168:171], v[216:219], v[74:77]
	v_mfma_f32_16x16x32_bf16 v[118:121], v[172:175], v[188:191], v[118:121]
	v_mfma_f32_16x16x32_bf16 v[110:113], v[180:183], v[188:191], v[110:113]
	v_mfma_f32_16x16x32_bf16 v[102:105], v[172:175], v[196:199], v[102:105]
	v_mfma_f32_16x16x32_bf16 v[94:97], v[180:183], v[196:199], v[94:97]
	v_mfma_f32_16x16x32_bf16 v[86:89], v[172:175], v[204:207], v[86:89]
	v_mfma_f32_16x16x32_bf16 v[78:81], v[180:183], v[204:207], v[78:81]
	v_mfma_f32_16x16x32_bf16 v[62:65], v[172:175], v[212:215], v[62:65]
	v_mfma_f32_16x16x32_bf16 v[58:61], v[180:183], v[212:215], v[58:61]
	v_mfma_f32_16x16x32_bf16 v[118:121], v[176:179], v[192:195], v[118:121]
	v_mfma_f32_16x16x32_bf16 v[110:113], v[184:187], v[192:195], v[110:113]
	v_mfma_f32_16x16x32_bf16 v[102:105], v[176:179], v[200:203], v[102:105]
	v_mfma_f32_16x16x32_bf16 v[94:97], v[184:187], v[200:203], v[94:97]
	s_barrier
; #define PG8_STAGE(bufoff, gbase, voff) do { _Pragma("unroll") for (int _i = 0; _i < 2; ++_i) \
;         __builtin_amdgcn_global_load_lds((const unsigned*)((const char*)(gbase) + (voff)[_i]), (PG8_LAS unsigned*)(lds + (bufoff) + ldsw + _i * 8192), 16, 0, 0); } while (0)
; #define PG8_LDA(dst, b, h) do { _Pragma("unroll") for (int m = 0; m < 4; ++m) _Pragma("unroll") for (int k = 0; k < 2; ++k) dst[m][k] = *(const PG8_LAS bf16x8*)(lds + PG8_SA(b, h) + aoff + m * 2048 + k * 1024); } while (0)
; #define PG8_MMA(ai, bj, At, Bt) do { __builtin_amdgcn_s_setprio(1); _Pragma("unroll") for (int m = 0; m < 4; ++m) _Pragma("unroll") for (int n = 0; n < 2; ++n) _Pragma("unroll") for (int k = 0; k < 2; ++k) \
;         acc[ai][bj][m][n] = __builtin_amdgcn_mfma_f32_16x16x32_bf16(Bt[n][k], At[m][k], acc[ai][bj][m][n], 0, 0, 0); __builtin_amdgcn_s_setprio(0); } while (0)
; #define PG8_WAIT_V(n) asm volatile("s_waitcnt vmcnt(" #n ")" ::: "memory")
; #define PG8_WAIT_L(n) asm volatile("s_waitcnt lgkmcnt(" #n ")" ::: "memory")
; #define PG8_BAR __builtin_amdgcn_s_barrier()
; #define PG8_SCHED __builtin_amdgcn_sched_barrier(0)
; template <class Epi, class Sched, bool ALIGN_EPI = false>
; __device__ __forceinline__ void gemm_phase(PG8_LAS unsigned char* lds, const Gemm g, const Sched& S, const Epi& E) {
;     ...
;             PG8_WAIT_V(8); PG8_WAIT_L(0); PG8_BAR; PG8_MMA(0, 0, At, B0); PG8_MMA(0, 1, At, B1); PG8_BAR; PG8_SCHED;
;             PG8_LDA(At, 1, 1); PG8_STAGE(PG8_SB(1, 0), b3, voffB); PG8_STAGE(PG8_SB(1, 1), b3 + hstep, voffB); PG8_STAGE(PG8_SA(1, 0), a3, w0);
;             PG8_WAIT_V(8); PG8_WAIT_L(0); PG8_BAR; PG8_MMA(1, 0, At, B0); PG8_MMA(1, 1, At, B1); PG8_BAR; PG8_SCHED;
;             if constexpr (Epi::KSCALE) { if (((t + 2) & 7) == 0 && t + 2 < nt) { E.kscale(acc, pf, ((t + 2) >> 3) - 1, wr, fr); PG8_SCHED; } }
;         }
	v_mfma_f32_16x16x32_bf16 v[86:89], v[176:179], v[208:211], v[86:89]
	v_mfma_f32_16x16x32_bf16 v[78:81], v[184:187], v[208:211], v[78:81]
	v_mfma_f32_16x16x32_bf16 v[62:65], v[176:179], v[216:219], v[62:65]
	v_mfma_f32_16x16x32_bf16 v[58:61], v[184:187], v[216:219], v[58:61]
	s_add_i32 s56, s88, s62
	v_lshl_add_u64 v[220:221], v[220:221], 0, s[12:13]
	s_mov_b32 m0, s56
	ds_read_b128 v[188:191], v159 offset:49152
	ds_read_b128 v[192:195], v159 offset:50176
	ds_read_b128 v[196:199], v159 offset:51200
	ds_read_b128 v[200:203], v159 offset:52224
	ds_read_b128 v[204:207], v159 offset:53248
	ds_read_b128 v[208:211], v159 offset:54272
	ds_read_b128 v[212:215], v159 offset:55296
	ds_read_b128 v[216:219], v159 offset:56320
	global_load_lds_dwordx4 v[220:221], off
	s_add_i32 m0, s56, 0x2000
	s_add_u32 s54, s54, 0x20080
	v_lshl_add_u64 v[220:221], v[222:223], 0, s[12:13]
	s_addc_u32 s55, s55, 0
	s_add_i32 s56, s89, s62
	global_load_lds_dwordx4 v[220:221], off
	v_lshl_add_u64 v[220:221], s[54:55], 0, v[134:135]
	s_mov_b32 m0, s56
	s_nop 0
	global_load_lds_dwordx4 v[220:221], off
	v_lshl_add_u64 v[220:221], s[54:55], 0, v[138:139]
	s_add_i32 m0, s56, 0x2000
	s_nop 0
	global_load_lds_dwordx4 v[220:221], off
	v_lshl_add_u64 v[220:221], v[224:225], 0, s[12:13]
	s_mov_b32 m0, s68
	s_nop 0
	global_load_lds_dwordx4 v[220:221], off
	v_lshl_add_u64 v[220:221], v[226:227], 0, s[12:13]
	s_mov_b32 m0, s69
	s_nop 0
	global_load_lds_dwordx4 v[220:221], off
	s_waitcnt vmcnt(8)
	s_waitcnt lgkmcnt(0)
	s_barrier
	v_mfma_f32_16x16x32_bf16 v[54:57], v[144:147], v[188:191], v[54:57]
	v_mfma_f32_16x16x32_bf16 v[42:45], v[164:167], v[188:191], v[42:45]
	v_mfma_f32_16x16x32_bf16 v[30:33], v[144:147], v[196:199], v[30:33]
	v_mfma_f32_16x16x32_bf16 v[26:29], v[164:167], v[196:199], v[26:29]
	v_mfma_f32_16x16x32_bf16 v[14:17], v[144:147], v[204:207], v[14:17]
	v_mfma_f32_16x16x32_bf16 v[10:13], v[164:167], v[204:207], v[10:13]
	v_mfma_f32_16x16x32_bf16 v[6:9], v[144:147], v[212:215], v[6:9]
	v_mfma_f32_16x16x32_bf16 v[2:5], v[164:167], v[212:215], v[2:5]
	v_mfma_f32_16x16x32_bf16 v[54:57], v[160:163], v[192:195], v[54:57]
	v_mfma_f32_16x16x32_bf16 v[42:45], v[168:171], v[192:195], v[42:45]
	v_mfma_f32_16x16x32_bf16 v[30:33], v[160:163], v[200:203], v[30:33]
	v_mfma_f32_16x16x32_bf16 v[26:29], v[168:171], v[200:203], v[26:29]
	v_mfma_f32_16x16x32_bf16 v[14:17], v[160:163], v[208:211], v[14:17]
	v_mfma_f32_16x16x32_bf16 v[10:13], v[168:171], v[208:211], v[10:13]
	v_mfma_f32_16x16x32_bf16 v[6:9], v[160:163], v[216:219], v[6:9]
	v_mfma_f32_16x16x32_bf16 v[2:5], v[168:171], v[216:219], v[2:5]
	v_mfma_f32_16x16x32_bf16 v[70:73], v[172:175], v[188:191], v[70:73]
	v_mfma_f32_16x16x32_bf16 v[66:69], v[180:183], v[188:191], v[66:69]
	v_mfma_f32_16x16x32_bf16 v[50:53], v[172:175], v[196:199], v[50:53]
	v_mfma_f32_16x16x32_bf16 v[46:49], v[180:183], v[196:199], v[46:49]
	v_mfma_f32_16x16x32_bf16 v[38:41], v[172:175], v[204:207], v[38:41]
	v_mfma_f32_16x16x32_bf16 v[34:37], v[180:183], v[204:207], v[34:37]
	v_mfma_f32_16x16x32_bf16 v[22:25], v[172:175], v[212:215], v[22:25]
	v_mfma_f32_16x16x32_bf16 v[18:21], v[180:183], v[212:215], v[18:21]
	v_mfma_f32_16x16x32_bf16 v[70:73], v[176:179], v[192:195], v[70:73]
	v_mfma_f32_16x16x32_bf16 v[66:69], v[184:187], v[192:195], v[66:69]
	v_mfma_f32_16x16x32_bf16 v[50:53], v[176:179], v[200:203], v[50:53]
	v_mfma_f32_16x16x32_bf16 v[46:49], v[184:187], v[200:203], v[46:49]
	s_barrier
	v_mfma_f32_16x16x32_bf16 v[38:41], v[176:179], v[208:211], v[38:41]
	v_mfma_f32_16x16x32_bf16 v[34:37], v[184:187], v[208:211], v[34:37]
	v_mfma_f32_16x16x32_bf16 v[22:25], v[176:179], v[216:219], v[22:25]
	v_mfma_f32_16x16x32_bf16 v[18:21], v[184:187], v[216:219], v[18:21]
	s_add_i32 s87, s87, 2
	s_add_u32 s85, s85, 0x100
	s_addc_u32 s86, s86, 0
	s_add_u32 s52, s52, 0x100
	s_addc_u32 s53, s53, 0
	s_cmp_gt_u32 s87, 5
	s_cbranch_scc0 .LBB0_1601
	s_and_b64 vcc, exec, s[14:15]
	s_cbranch_vccz .LBB0_1604
	s_barrier
